# v027 + load phases of the K-loops run at s_setprio 3 (MFMA blocks stay at 1): LDS-DMA/ds_read issue is the latency-critical path
# baseline (speedup 1.0000x reference)
; #define PG8_STAGE(bufoff, gbase, voff) do { _Pragma("unroll") for (int _i = 0; _i < 2; ++_i) \
;         __builtin_amdgcn_global_load_lds((const unsigned*)((const char*)(gbase) + (voff)[_i]), (LAS unsigned*)(lds + (bufoff) + ldsw + _i * 8192), 16, 0, 0); } while (0)
; #define PG8_LDA(dst, b, h) do { _Pragma("unroll") for (int m = 0; m < 4; ++m) _Pragma("unroll") for (int k = 0; k < 2; ++k) dst[m][k] = *(const LAS bf16x8*)(lds + PG8_SA(b, h) + ((aoff ^ (k * 64)) + m * 2048)); } while (0)
; #define PG8_LDB(dst, b, h) do { _Pragma("unroll") for (int n = 0; n < 2; ++n) _Pragma("unroll") for (int k = 0; k < 2; ++k) dst[n][k] = *(const LAS bf16x8*)(lds + PG8_SB(b, h) + ((boff ^ (k * 64)) + n * 2048)); } while (0)
; #define PG8_WAIT_V(n) asm volatile("s_waitcnt vmcnt(" #n ")" ::: "memory")
; #define PG8_WAIT_L(n) asm volatile("s_waitcnt lgkmcnt(" #n ")" ::: "memory")
;     ...
;             const bool last = (t == nt - 2);
;             const char* a1 = cA + (size_t)(t + 1) * kstepA;
;             const char* a2 = last ? nA : cA + (size_t)(t + 2) * kstepA; const char* b2 = last ? nB : cB + (size_t)(t + 2) * kstepB;
;             const char* a3 = a2 + kstepA; const char* b3 = b2 + kstepB;
;             unsigned vs[2][2];
;             if constexpr (GATHER) {
;                 if (last && has_next) {
; #pragma unroll
;                     for (int hh = 0; hh < 2; ++hh)
; #pragma unroll
;                         for (int i = 0; i < 2; ++i) voffN[hh][i] = (unsigned)idxl[(ui + 1) * 256 + hh * HALF + sR[i]] * (unsigned)(K * 2) + (unsigned)sC[i] * 2u;
;                 }
; #pragma unroll
;                 for (int hh = 0; hh < 2; ++hh)
; #pragma unroll
;                     for (int i = 0; i < 2; ++i) vs[hh][i] = last ? voffN[hh][i] : voffA[hh][i];
;             } else {
; #pragma unroll
;                 for (int hh = 0; hh < 2; ++hh)
; #pragma unroll
;                     for (int i = 0; i < 2; ++i) vs[hh][i] = voffA[hh][i];
;             }
;             PG8_LDB(B0, 0, 0); PG8_LDB(B1, 0, 1); PG8_SCHED; PG8_LDA(At, 0, 0); PG8_STAGE(PG8_SA(1, 1), a1, voffA[1]);
;             PG8_WAIT_V(8); PG8_WAIT_L(0); PG8_BAR; if (do0) { PG8_MMA(0, 0, At, B0); PG8_MMA(0, 1, At, B1); } PG8_BAR; PG8_SCHED;
;             PG8_LDA(At, 0, 1); PG8_STAGE(PG8_SB(0, 0), b2, voffB); PG8_STAGE(PG8_SB(0, 1), b2 + hstep, voffB); PG8_STAGE(PG8_SA(0, 0), a2, vs[0]);
.LBB0_192:
	ds_read_b128 v[158:161], v166
	ds_read_b128 v[180:183], v167
	ds_read_b128 v[184:187], v168
	ds_read_b128 v[188:191], v169
	ds_read_b128 v[192:195], v170
	ds_read_b128 v[200:203], v171
	ds_read_b128 v[204:207], v172
	ds_read_b128 v[208:211], v173
	s_add_u32 s28, s4, 0x80
	s_addc_u32 s29, s5, 0
	s_cmp_eq_u32 s64, 12
	s_cselect_b32 s35, s17, s29
	s_cselect_b32 s34, s60, s28
	s_cselect_b32 s29, s19, s63
	s_cselect_b32 s28, s61, s62
	v_lshl_add_u64 v[162:163], s[4:5], 0, v[152:153]
	s_add_i32 m0, s25, 0xc000
	ds_read_b128 v[212:215], v174
	ds_read_b128 v[216:219], v174 offset:2048
	ds_read_b128 v[220:223], v175
	ds_read_b128 v[224:227], v175 offset:2048
	ds_read_b128 v[228:231], v174 offset:4096
	ds_read_b128 v[232:235], v174 offset:6144
	ds_read_b128 v[236:239], v175 offset:4096
	ds_read_b128 v[240:243], v175 offset:6144
	global_load_lds_dwordx4 v[162:163], off
	v_lshl_add_u64 v[162:163], s[4:5], 0, v[150:151]
	s_add_i32 m0, s25, 0xe000
	s_add_u32 s30, s28, 0x4000
	global_load_lds_dwordx4 v[162:163], off
	s_waitcnt vmcnt(8)
	s_waitcnt lgkmcnt(0)
	s_addc_u32 s31, s29, 0
	s_barrier
	s_setprio 1
	s_waitcnt lgkmcnt(0)
	v_mfma_f32_16x16x32_bf16 v[126:129], v[158:161], v[212:215], v[126:129]
	v_mfma_f32_16x16x32_bf16 v[122:125], v[184:187], v[212:215], v[122:125]
	v_mfma_f32_16x16x32_bf16 v[110:113], v[158:161], v[216:219], v[110:113]
	v_mfma_f32_16x16x32_bf16 v[106:109], v[184:187], v[216:219], v[106:109]
	v_mfma_f32_16x16x32_bf16 v[94:97], v[158:161], v[228:231], v[94:97]
	v_mfma_f32_16x16x32_bf16 v[90:93], v[184:187], v[228:231], v[90:93]
	v_mfma_f32_16x16x32_bf16 v[78:81], v[158:161], v[232:235], v[78:81]
	v_mfma_f32_16x16x32_bf16 v[74:77], v[184:187], v[232:235], v[74:77]
	v_mfma_f32_16x16x32_bf16 v[126:129], v[180:183], v[220:223], v[126:129]
	v_mfma_f32_16x16x32_bf16 v[122:125], v[188:191], v[220:223], v[122:125]
	v_mfma_f32_16x16x32_bf16 v[110:113], v[180:183], v[224:227], v[110:113]
	v_mfma_f32_16x16x32_bf16 v[106:109], v[188:191], v[224:227], v[106:109]
	v_mfma_f32_16x16x32_bf16 v[94:97], v[180:183], v[236:239], v[94:97]
	v_mfma_f32_16x16x32_bf16 v[90:93], v[188:191], v[236:239], v[90:93]
	v_mfma_f32_16x16x32_bf16 v[78:81], v[180:183], v[240:243], v[78:81]
	v_mfma_f32_16x16x32_bf16 v[74:77], v[188:191], v[240:243], v[74:77]
	v_mfma_f32_16x16x32_bf16 v[118:121], v[192:195], v[212:215], v[118:121]
	v_mfma_f32_16x16x32_bf16 v[114:117], v[204:207], v[212:215], v[114:117]
	v_mfma_f32_16x16x32_bf16 v[102:105], v[192:195], v[216:219], v[102:105]
	v_mfma_f32_16x16x32_bf16 v[98:101], v[204:207], v[216:219], v[98:101]
	v_mfma_f32_16x16x32_bf16 v[86:89], v[192:195], v[228:231], v[86:89]
	v_mfma_f32_16x16x32_bf16 v[82:85], v[204:207], v[228:231], v[82:85]
	v_mfma_f32_16x16x32_bf16 v[70:73], v[192:195], v[232:235], v[70:73]
	v_mfma_f32_16x16x32_bf16 v[66:69], v[204:207], v[232:235], v[66:69]
	v_mfma_f32_16x16x32_bf16 v[118:121], v[200:203], v[220:223], v[118:121]
	v_mfma_f32_16x16x32_bf16 v[114:117], v[208:211], v[220:223], v[114:117]
	v_mfma_f32_16x16x32_bf16 v[102:105], v[200:203], v[224:227], v[102:105]
	v_mfma_f32_16x16x32_bf16 v[98:101], v[208:211], v[224:227], v[98:101]
	v_mfma_f32_16x16x32_bf16 v[86:89], v[200:203], v[236:239], v[86:89]
	v_mfma_f32_16x16x32_bf16 v[82:85], v[208:211], v[236:239], v[82:85]
	v_mfma_f32_16x16x32_bf16 v[70:73], v[200:203], v[240:243], v[70:73]
	v_mfma_f32_16x16x32_bf16 v[66:69], v[208:211], v[240:243], v[66:69]
	s_setprio 0
	s_barrier
	s_setprio 3
	s_add_i32 s65, s56, s37
	v_lshl_add_u64 v[162:163], s[28:29], 0, v[130:131]
	s_mov_b32 m0, s65
	ds_read_b128 v[212:215], v174 offset:16384
	ds_read_b128 v[216:219], v174 offset:18432
	ds_read_b128 v[220:223], v175 offset:16384
	ds_read_b128 v[224:227], v175 offset:18432
	ds_read_b128 v[228:231], v174 offset:20480
	ds_read_b128 v[232:235], v174 offset:22528
	ds_read_b128 v[236:239], v175 offset:20480
	ds_read_b128 v[240:243], v175 offset:22528
	global_load_lds_dwordx4 v[162:163], off
	s_add_i32 m0, s65, 0x2000
	s_add_u32 s66, s28, 0x40000
	v_lshl_add_u64 v[162:163], s[28:29], 0, v[132:133]
	s_addc_u32 s67, s29, 0
	s_add_i32 s65, s57, s37
	global_load_lds_dwordx4 v[162:163], off
	v_lshl_add_u64 v[162:163], s[66:67], 0, v[130:131]
	s_mov_b32 m0, s65
	v_lshl_add_u64 v[196:197], s[34:35], 0, v[136:137]
	global_load_lds_dwordx4 v[162:163], off
	v_lshl_add_u64 v[162:163], s[66:67], 0, v[132:133]
	s_add_i32 m0, s65, 0x2000
	s_nop 0
	global_load_lds_dwordx4 v[162:163], off
	v_lshl_add_u64 v[162:163], s[34:35], 0, v[134:135]
	s_mov_b32 m0, s25
	s_nop 0
	global_load_lds_dwordx4 v[162:163], off
	s_mov_b32 m0, s27
	s_nop 0
	global_load_lds_dwordx4 v[196:197], off
	s_waitcnt vmcnt(8)
	s_waitcnt lgkmcnt(0)
	s_barrier
; #define PG8_STAGE(bufoff, gbase, voff) do { _Pragma("unroll") for (int _i = 0; _i < 2; ++_i) \
;         __builtin_amdgcn_global_load_lds((const unsigned*)((const char*)(gbase) + (voff)[_i]), (LAS unsigned*)(lds + (bufoff) + ldsw + _i * 8192), 16, 0, 0); } while (0)
; #define PG8_LDA(dst, b, h) do { _Pragma("unroll") for (int m = 0; m < 4; ++m) _Pragma("unroll") for (int k = 0; k < 2; ++k) dst[m][k] = *(const LAS bf16x8*)(lds + PG8_SA(b, h) + ((aoff ^ (k * 64)) + m * 2048)); } while (0)
; #define PG8_LDB(dst, b, h) do { _Pragma("unroll") for (int n = 0; n < 2; ++n) _Pragma("unroll") for (int k = 0; k < 2; ++k) dst[n][k] = *(const LAS bf16x8*)(lds + PG8_SB(b, h) + ((boff ^ (k * 64)) + n * 2048)); } while (0)
; #define PG8_MMA(ai, bj, At, Bt) do { __builtin_amdgcn_s_setprio(1); _Pragma("unroll") for (int m = 0; m < 4; ++m) _Pragma("unroll") for (int n = 0; n < 2; ++n) _Pragma("unroll") for (int k = 0; k < 2; ++k) \
;         acc[ai][bj][m][n] = __builtin_amdgcn_mfma_f32_16x16x32_bf16(Bt[n][k], At[m][k], acc[ai][bj][m][n], 0, 0, 0); __builtin_amdgcn_s_setprio(0); } while (0)
; #define PG8_WAIT_V(n) asm volatile("s_waitcnt vmcnt(" #n ")" ::: "memory")
; #define PG8_WAIT_L(n) asm volatile("s_waitcnt lgkmcnt(" #n ")" ::: "memory")
; #define PG8_BAR __builtin_amdgcn_s_barrier()
; #define PG8_SCHED __builtin_amdgcn_sched_barrier(0)
;     ...
;             PG8_WAIT_V(8); PG8_WAIT_L(0); PG8_BAR; if (do1) { PG8_MMA(1, 0, At, B0); PG8_MMA(1, 1, At, B1); } PG8_BAR; PG8_SCHED;
;             PG8_LDB(B0, 1, 0); PG8_LDB(B1, 1, 1); PG8_SCHED; PG8_LDA(At, 1, 0); PG8_STAGE(PG8_SA(0, 1), a2, vs[1]);
;             PG8_WAIT_V(8); PG8_WAIT_L(0); PG8_BAR; if (do0) { PG8_MMA(0, 0, At, B0); PG8_MMA(0, 1, At, B1); } PG8_BAR; PG8_SCHED;
	s_setprio 1
	s_waitcnt lgkmcnt(0)
	v_mfma_f32_16x16x32_bf16 v[62:65], v[158:161], v[212:215], v[62:65]
	v_mfma_f32_16x16x32_bf16 v[58:61], v[184:187], v[212:215], v[58:61]
	v_mfma_f32_16x16x32_bf16 v[46:49], v[158:161], v[216:219], v[46:49]
	v_mfma_f32_16x16x32_bf16 v[42:45], v[184:187], v[216:219], v[42:45]
	v_mfma_f32_16x16x32_bf16 v[30:33], v[158:161], v[228:231], v[30:33]
	v_mfma_f32_16x16x32_bf16 v[26:29], v[184:187], v[228:231], v[26:29]
	v_mfma_f32_16x16x32_bf16 v[14:17], v[158:161], v[232:235], v[14:17]
	v_mfma_f32_16x16x32_bf16 v[10:13], v[184:187], v[232:235], v[10:13]
	v_mfma_f32_16x16x32_bf16 v[62:65], v[180:183], v[220:223], v[62:65]
	v_mfma_f32_16x16x32_bf16 v[58:61], v[188:191], v[220:223], v[58:61]
	v_mfma_f32_16x16x32_bf16 v[46:49], v[180:183], v[224:227], v[46:49]
	v_mfma_f32_16x16x32_bf16 v[42:45], v[188:191], v[224:227], v[42:45]
	v_mfma_f32_16x16x32_bf16 v[30:33], v[180:183], v[236:239], v[30:33]
	v_mfma_f32_16x16x32_bf16 v[26:29], v[188:191], v[236:239], v[26:29]
	v_mfma_f32_16x16x32_bf16 v[14:17], v[180:183], v[240:243], v[14:17]
	v_mfma_f32_16x16x32_bf16 v[10:13], v[188:191], v[240:243], v[10:13]
	v_mfma_f32_16x16x32_bf16 v[54:57], v[192:195], v[212:215], v[54:57]
	v_mfma_f32_16x16x32_bf16 v[50:53], v[204:207], v[212:215], v[50:53]
	v_mfma_f32_16x16x32_bf16 v[38:41], v[192:195], v[216:219], v[38:41]
	v_mfma_f32_16x16x32_bf16 v[34:37], v[204:207], v[216:219], v[34:37]
	v_mfma_f32_16x16x32_bf16 v[22:25], v[192:195], v[228:231], v[22:25]
	v_mfma_f32_16x16x32_bf16 v[18:21], v[204:207], v[228:231], v[18:21]
	v_mfma_f32_16x16x32_bf16 v[6:9], v[192:195], v[232:235], v[6:9]
	v_mfma_f32_16x16x32_bf16 v[2:5], v[204:207], v[232:235], v[2:5]
	v_mfma_f32_16x16x32_bf16 v[54:57], v[200:203], v[220:223], v[54:57]
	v_mfma_f32_16x16x32_bf16 v[50:53], v[208:211], v[220:223], v[50:53]
	v_mfma_f32_16x16x32_bf16 v[38:41], v[200:203], v[224:227], v[38:41]
	v_mfma_f32_16x16x32_bf16 v[34:37], v[208:211], v[224:227], v[34:37]
	v_mfma_f32_16x16x32_bf16 v[22:25], v[200:203], v[236:239], v[22:25]
	v_mfma_f32_16x16x32_bf16 v[18:21], v[208:211], v[236:239], v[18:21]
	v_mfma_f32_16x16x32_bf16 v[6:9], v[200:203], v[240:243], v[6:9]
	v_mfma_f32_16x16x32_bf16 v[2:5], v[208:211], v[240:243], v[2:5]
	s_setprio 0
	s_barrier
	s_setprio 3
	s_add_i32 s65, 0, 0x18000
	v_add_u32_e32 v142, s65, v145
	v_add_u32_e32 v180, s65, v165
	s_add_i32 s66, 0, 0x1c000
	ds_read_b128 v[158:161], v142
	ds_read_b128 v[180:183], v180
	ds_read_b128 v[184:187], v176
	ds_read_b128 v[188:191], v177
	v_add_u32_e32 v142, s66, v145
	v_add_u32_e32 v199, s66, v165
	ds_read_b128 v[192:195], v142
	ds_read_b128 v[200:203], v199
	ds_read_b128 v[204:207], v178
	ds_read_b128 v[208:211], v179
	s_mov_b32 m0, s38
	v_lshl_add_u64 v[244:245], s[34:35], 0, v[138:139]
	ds_read_b128 v[212:215], v174 offset:32768
	ds_read_b128 v[216:219], v174 offset:34816
	ds_read_b128 v[220:223], v175 offset:32768
	ds_read_b128 v[224:227], v175 offset:34816
	ds_read_b128 v[228:231], v174 offset:36864
	ds_read_b128 v[232:235], v174 offset:38912
	ds_read_b128 v[236:239], v175 offset:36864
	ds_read_b128 v[240:243], v175 offset:38912
	global_load_lds_dwordx4 v[244:245], off
	v_lshl_add_u64 v[244:245], s[34:35], 0, v[140:141]
	s_mov_b32 m0, s39
	s_nop 0
	global_load_lds_dwordx4 v[244:245], off
	s_waitcnt vmcnt(8)
	s_waitcnt lgkmcnt(0)
	s_barrier
	s_setprio 1
	s_waitcnt lgkmcnt(0)
	v_mfma_f32_16x16x32_bf16 v[126:129], v[158:161], v[212:215], v[126:129]
	v_mfma_f32_16x16x32_bf16 v[122:125], v[184:187], v[212:215], v[122:125]
	v_mfma_f32_16x16x32_bf16 v[110:113], v[158:161], v[216:219], v[110:113]
	v_mfma_f32_16x16x32_bf16 v[106:109], v[184:187], v[216:219], v[106:109]
	v_mfma_f32_16x16x32_bf16 v[94:97], v[158:161], v[228:231], v[94:97]
	v_mfma_f32_16x16x32_bf16 v[90:93], v[184:187], v[228:231], v[90:93]
	v_mfma_f32_16x16x32_bf16 v[78:81], v[158:161], v[232:235], v[78:81]
	v_mfma_f32_16x16x32_bf16 v[74:77], v[184:187], v[232:235], v[74:77]
	v_mfma_f32_16x16x32_bf16 v[126:129], v[180:183], v[220:223], v[126:129]
	v_mfma_f32_16x16x32_bf16 v[122:125], v[188:191], v[220:223], v[122:125]
	v_mfma_f32_16x16x32_bf16 v[110:113], v[180:183], v[224:227], v[110:113]
	v_mfma_f32_16x16x32_bf16 v[106:109], v[188:191], v[224:227], v[106:109]
	v_mfma_f32_16x16x32_bf16 v[94:97], v[180:183], v[236:239], v[94:97]
	v_mfma_f32_16x16x32_bf16 v[90:93], v[188:191], v[236:239], v[90:93]
	v_mfma_f32_16x16x32_bf16 v[78:81], v[180:183], v[240:243], v[78:81]
	v_mfma_f32_16x16x32_bf16 v[74:77], v[188:191], v[240:243], v[74:77]
	v_mfma_f32_16x16x32_bf16 v[118:121], v[192:195], v[212:215], v[118:121]
	v_mfma_f32_16x16x32_bf16 v[114:117], v[204:207], v[212:215], v[114:117]
	v_mfma_f32_16x16x32_bf16 v[102:105], v[192:195], v[216:219], v[102:105]
	v_mfma_f32_16x16x32_bf16 v[98:101], v[204:207], v[216:219], v[98:101]
	v_mfma_f32_16x16x32_bf16 v[86:89], v[192:195], v[228:231], v[86:89]
	v_mfma_f32_16x16x32_bf16 v[82:85], v[204:207], v[228:231], v[82:85]
	v_mfma_f32_16x16x32_bf16 v[70:73], v[192:195], v[232:235], v[70:73]
	v_mfma_f32_16x16x32_bf16 v[66:69], v[204:207], v[232:235], v[66:69]
	v_mfma_f32_16x16x32_bf16 v[118:121], v[200:203], v[220:223], v[118:121]
	v_mfma_f32_16x16x32_bf16 v[114:117], v[208:211], v[220:223], v[114:117]
	v_mfma_f32_16x16x32_bf16 v[102:105], v[200:203], v[224:227], v[102:105]
	v_mfma_f32_16x16x32_bf16 v[98:101], v[208:211], v[224:227], v[98:101]
	v_mfma_f32_16x16x32_bf16 v[86:89], v[200:203], v[236:239], v[86:89]
	v_mfma_f32_16x16x32_bf16 v[82:85], v[208:211], v[236:239], v[82:85]
	v_mfma_f32_16x16x32_bf16 v[70:73], v[200:203], v[240:243], v[70:73]
	v_mfma_f32_16x16x32_bf16 v[66:69], v[208:211], v[240:243], v[66:69]
	s_setprio 0
	s_barrier
; #define PG8_STAGE(bufoff, gbase, voff) do { _Pragma("unroll") for (int _i = 0; _i < 2; ++_i) \
;         __builtin_amdgcn_global_load_lds((const unsigned*)((const char*)(gbase) + (voff)[_i]), (LAS unsigned*)(lds + (bufoff) + ldsw + _i * 8192), 16, 0, 0); } while (0)
; #define PG8_LDA(dst, b, h) do { _Pragma("unroll") for (int m = 0; m < 4; ++m) _Pragma("unroll") for (int k = 0; k < 2; ++k) dst[m][k] = *(const LAS bf16x8*)(lds + PG8_SA(b, h) + ((aoff ^ (k * 64)) + m * 2048)); } while (0)
; #define PG8_MMA(ai, bj, At, Bt) do { __builtin_amdgcn_s_setprio(1); _Pragma("unroll") for (int m = 0; m < 4; ++m) _Pragma("unroll") for (int n = 0; n < 2; ++n) _Pragma("unroll") for (int k = 0; k < 2; ++k) \
;         acc[ai][bj][m][n] = __builtin_amdgcn_mfma_f32_16x16x32_bf16(Bt[n][k], At[m][k], acc[ai][bj][m][n], 0, 0, 0); __builtin_amdgcn_s_setprio(0); } while (0)
; #define PG8_WAIT_V(n) asm volatile("s_waitcnt vmcnt(" #n ")" ::: "memory")
; #define PG8_WAIT_L(n) asm volatile("s_waitcnt lgkmcnt(" #n ")" ::: "memory")
; #define PG8_BAR __builtin_amdgcn_s_barrier()
; #define PG8_SCHED __builtin_amdgcn_sched_barrier(0)
;     ...
;             PG8_LDA(At, 1, 1); PG8_STAGE(PG8_SB(1, 0), b3, voffB); PG8_STAGE(PG8_SB(1, 1), b3 + hstep, voffB); PG8_STAGE(PG8_SA(1, 0), a3, vs[0]);
;             PG8_WAIT_V(8); PG8_WAIT_L(0); PG8_BAR; if (do1) { PG8_MMA(1, 0, At, B0); PG8_MMA(1, 1, At, B1); } PG8_BAR; PG8_SCHED;
;         }
;         if (wr == 0) PG8_BAR;
	s_setprio 3
	s_add_i32 s34, s65, s37
	v_lshl_add_u64 v[244:245], s[30:31], 0, v[130:131]
	s_mov_b32 m0, s34
	ds_read_b128 v[212:215], v174 offset:49152
	ds_read_b128 v[216:219], v174 offset:51200
	ds_read_b128 v[220:223], v175 offset:49152
	ds_read_b128 v[224:227], v175 offset:51200
	ds_read_b128 v[228:231], v174 offset:53248
	ds_read_b128 v[232:235], v174 offset:55296
	ds_read_b128 v[236:239], v175 offset:53248
	ds_read_b128 v[240:243], v175 offset:55296
	global_load_lds_dwordx4 v[244:245], off
	s_add_i32 m0, s34, 0x2000
	s_add_u32 s28, s28, 0x44000
	v_lshl_add_u64 v[244:245], s[30:31], 0, v[132:133]
	s_addc_u32 s29, s29, 0
	s_add_i32 s30, s66, s37
	global_load_lds_dwordx4 v[244:245], off
	v_lshl_add_u64 v[244:245], s[28:29], 0, v[130:131]
	s_mov_b32 m0, s30
	v_lshl_add_u64 v[162:163], v[162:163], 0, s[8:9]
	global_load_lds_dwordx4 v[244:245], off
	v_lshl_add_u64 v[244:245], s[28:29], 0, v[132:133]
	s_add_i32 m0, s30, 0x2000
	s_nop 0
	global_load_lds_dwordx4 v[244:245], off
	s_mov_b32 m0, s51
	s_nop 0
	global_load_lds_dwordx4 v[162:163], off
	v_lshl_add_u64 v[162:163], v[196:197], 0, s[8:9]
	s_mov_b32 m0, s54
	s_nop 0
	global_load_lds_dwordx4 v[162:163], off
	s_waitcnt vmcnt(8)
	s_waitcnt lgkmcnt(0)
	s_barrier
	s_setprio 1
	s_waitcnt lgkmcnt(0)
	v_mfma_f32_16x16x32_bf16 v[62:65], v[158:161], v[212:215], v[62:65]
	v_mfma_f32_16x16x32_bf16 v[58:61], v[184:187], v[212:215], v[58:61]
	v_mfma_f32_16x16x32_bf16 v[46:49], v[158:161], v[216:219], v[46:49]
	v_mfma_f32_16x16x32_bf16 v[42:45], v[184:187], v[216:219], v[42:45]
	v_mfma_f32_16x16x32_bf16 v[30:33], v[158:161], v[228:231], v[30:33]
	v_mfma_f32_16x16x32_bf16 v[26:29], v[184:187], v[228:231], v[26:29]
	v_mfma_f32_16x16x32_bf16 v[14:17], v[158:161], v[232:235], v[14:17]
	v_mfma_f32_16x16x32_bf16 v[10:13], v[184:187], v[232:235], v[10:13]
	v_mfma_f32_16x16x32_bf16 v[62:65], v[180:183], v[220:223], v[62:65]
	v_mfma_f32_16x16x32_bf16 v[58:61], v[188:191], v[220:223], v[58:61]
	v_mfma_f32_16x16x32_bf16 v[46:49], v[180:183], v[224:227], v[46:49]
	v_mfma_f32_16x16x32_bf16 v[42:45], v[188:191], v[224:227], v[42:45]
	v_mfma_f32_16x16x32_bf16 v[30:33], v[180:183], v[236:239], v[30:33]
	v_mfma_f32_16x16x32_bf16 v[26:29], v[188:191], v[236:239], v[26:29]
	v_mfma_f32_16x16x32_bf16 v[14:17], v[180:183], v[240:243], v[14:17]
	v_mfma_f32_16x16x32_bf16 v[10:13], v[188:191], v[240:243], v[10:13]
	v_mfma_f32_16x16x32_bf16 v[54:57], v[192:195], v[212:215], v[54:57]
	v_mfma_f32_16x16x32_bf16 v[50:53], v[204:207], v[212:215], v[50:53]
	v_mfma_f32_16x16x32_bf16 v[38:41], v[192:195], v[216:219], v[38:41]
	v_mfma_f32_16x16x32_bf16 v[34:37], v[204:207], v[216:219], v[34:37]
	v_mfma_f32_16x16x32_bf16 v[22:25], v[192:195], v[228:231], v[22:25]
	v_mfma_f32_16x16x32_bf16 v[18:21], v[204:207], v[228:231], v[18:21]
	v_mfma_f32_16x16x32_bf16 v[6:9], v[192:195], v[232:235], v[6:9]
	v_mfma_f32_16x16x32_bf16 v[2:5], v[204:207], v[232:235], v[2:5]
	v_mfma_f32_16x16x32_bf16 v[54:57], v[200:203], v[220:223], v[54:57]
	v_mfma_f32_16x16x32_bf16 v[50:53], v[208:211], v[220:223], v[50:53]
	v_mfma_f32_16x16x32_bf16 v[38:41], v[200:203], v[224:227], v[38:41]
	v_mfma_f32_16x16x32_bf16 v[34:37], v[208:211], v[224:227], v[34:37]
	v_mfma_f32_16x16x32_bf16 v[22:25], v[200:203], v[236:239], v[22:25]
	v_mfma_f32_16x16x32_bf16 v[18:21], v[208:211], v[236:239], v[18:21]
	v_mfma_f32_16x16x32_bf16 v[6:9], v[200:203], v[240:243], v[6:9]
	v_mfma_f32_16x16x32_bf16 v[2:5], v[208:211], v[240:243], v[2:5]
	s_setprio 0
	s_barrier
	s_setprio 3
	s_add_i32 s64, s64, 2
	s_add_u32 s62, s62, 0x8000
	s_addc_u32 s63, s63, 0
	s_add_u32 s4, s4, 0x100
	s_addc_u32 s5, s5, 0
	s_cmp_gt_u32 s64, 13
	s_cbranch_scc0 .LBB0_192
	s_and_b64 vcc, exec, s[12:13]
	s_cbranch_vccz .LBB0_195
	s_barrier

; #define PG8_STAGE(bufoff, gbase, voff) do { _Pragma("unroll") for (int _i = 0; _i < 2; ++_i) \
;         __builtin_amdgcn_global_load_lds((const unsigned*)((const char*)(gbase) + (voff)[_i]), (LAS unsigned*)(lds + (bufoff) + ldsw + _i * 8192), 16, 0, 0); } while (0)
; #define PG8_LDA(dst, b, h) do { _Pragma("unroll") for (int m = 0; m < 4; ++m) _Pragma("unroll") for (int k = 0; k < 2; ++k) dst[m][k] = *(const LAS bf16x8*)(lds + PG8_SA(b, h) + ((aoff ^ (k * 64)) + m * 2048)); } while (0)
; #define PG8_LDB(dst, b, h) do { _Pragma("unroll") for (int n = 0; n < 2; ++n) _Pragma("unroll") for (int k = 0; k < 2; ++k) dst[n][k] = *(const LAS bf16x8*)(lds + PG8_SB(b, h) + ((boff ^ (k * 64)) + n * 2048)); } while (0)
; #define PG8_WAIT_V(n) asm volatile("s_waitcnt vmcnt(" #n ")" ::: "memory")
; #define PG8_WAIT_L(n) asm volatile("s_waitcnt lgkmcnt(" #n ")" ::: "memory")
;     ...
;             const bool last = (t == nt - 2);
;             const char* a1 = cA + (size_t)(t + 1) * kstepA;
;             const char* a2 = last ? nA : cA + (size_t)(t + 2) * kstepA; const char* b2 = last ? nB : cB + (size_t)(t + 2) * kstepB;
;             const char* a3 = a2 + kstepA; const char* b3 = b2 + kstepB;
;             unsigned vs[2][2];
;             if constexpr (GATHER) {
;                 if (last && has_next) {
; #pragma unroll
;                     for (int hh = 0; hh < 2; ++hh)
; #pragma unroll
;                         for (int i = 0; i < 2; ++i) voffN[hh][i] = (unsigned)idxl[(ui + 1) * 256 + hh * HALF + sR[i]] * (unsigned)(K * 2) + (unsigned)sC[i] * 2u;
;                 }
; #pragma unroll
;                 for (int hh = 0; hh < 2; ++hh)
; #pragma unroll
;                     for (int i = 0; i < 2; ++i) vs[hh][i] = last ? voffN[hh][i] : voffA[hh][i];
;             } else {
; #pragma unroll
;                 for (int hh = 0; hh < 2; ++hh)
; #pragma unroll
;                     for (int i = 0; i < 2; ++i) vs[hh][i] = voffA[hh][i];
;             }
;             PG8_LDB(B0, 0, 0); PG8_LDB(B1, 0, 1); PG8_SCHED; PG8_LDA(At, 0, 0); PG8_STAGE(PG8_SA(1, 1), a1, voffA[1]);
;             PG8_WAIT_V(8); PG8_WAIT_L(0); PG8_BAR; if (do0) { PG8_MMA(0, 0, At, B0); PG8_MMA(0, 1, At, B1); } PG8_BAR; PG8_SCHED;
;             PG8_LDA(At, 0, 1); PG8_STAGE(PG8_SB(0, 0), b2, voffB); PG8_STAGE(PG8_SB(0, 1), b2 + hstep, voffB); PG8_STAGE(PG8_SA(0, 0), a2, vs[0]);
.LBB0_212:
	ds_read_b128 v[168:171], v153
	ds_read_b128 v[172:175], v154
	ds_read_b128 v[176:179], v155
	ds_read_b128 v[180:183], v156
	ds_read_b128 v[184:187], v157
	ds_read_b128 v[188:191], v158
	ds_read_b128 v[192:195], v159
	ds_read_b128 v[200:203], v160
	s_add_u32 s30, s4, 0x4000
	s_addc_u32 s31, s5, 0
	s_cmp_eq_u32 s64, 12
	s_cselect_b32 s36, s29, s30
	s_cselect_b32 s37, s17, s31
	s_cselect_b32 s34, s61, s62
	s_cselect_b32 s35, s19, s63
	s_add_u32 s30, s36, 0x4000
	s_addc_u32 s31, s37, 0
	v_lshl_add_u64 v[196:197], s[4:5], 0, v[148:149]
	s_add_i32 m0, s27, 0xc000
	ds_read_b128 v[204:207], v161
	ds_read_b128 v[208:211], v161 offset:2048
	ds_read_b128 v[212:215], v162
	ds_read_b128 v[216:219], v162 offset:2048
	ds_read_b128 v[220:223], v161 offset:4096
	ds_read_b128 v[224:227], v161 offset:6144
	ds_read_b128 v[228:231], v162 offset:4096
	ds_read_b128 v[232:235], v162 offset:6144
	global_load_lds_dwordx4 v[196:197], off
	v_lshl_add_u64 v[196:197], s[4:5], 0, v[150:151]
	s_add_i32 m0, s27, 0xe000
	s_nop 0
	global_load_lds_dwordx4 v[196:197], off
	s_waitcnt vmcnt(8)
	s_waitcnt lgkmcnt(0)
	s_barrier
	s_setprio 1
	s_waitcnt lgkmcnt(0)
	v_mfma_f32_16x16x32_bf16 v[126:129], v[168:171], v[204:207], v[126:129]
	v_mfma_f32_16x16x32_bf16 v[122:125], v[176:179], v[204:207], v[122:125]
	v_mfma_f32_16x16x32_bf16 v[110:113], v[168:171], v[208:211], v[110:113]
	v_mfma_f32_16x16x32_bf16 v[106:109], v[176:179], v[208:211], v[106:109]
	v_mfma_f32_16x16x32_bf16 v[94:97], v[168:171], v[220:223], v[94:97]
	v_mfma_f32_16x16x32_bf16 v[90:93], v[176:179], v[220:223], v[90:93]
	v_mfma_f32_16x16x32_bf16 v[78:81], v[168:171], v[224:227], v[78:81]
	v_mfma_f32_16x16x32_bf16 v[74:77], v[176:179], v[224:227], v[74:77]
	v_mfma_f32_16x16x32_bf16 v[126:129], v[172:175], v[212:215], v[126:129]
	v_mfma_f32_16x16x32_bf16 v[122:125], v[180:183], v[212:215], v[122:125]
	v_mfma_f32_16x16x32_bf16 v[110:113], v[172:175], v[216:219], v[110:113]
	v_mfma_f32_16x16x32_bf16 v[106:109], v[180:183], v[216:219], v[106:109]
	v_mfma_f32_16x16x32_bf16 v[94:97], v[172:175], v[228:231], v[94:97]
	v_mfma_f32_16x16x32_bf16 v[90:93], v[180:183], v[228:231], v[90:93]
	v_mfma_f32_16x16x32_bf16 v[78:81], v[172:175], v[232:235], v[78:81]
	v_mfma_f32_16x16x32_bf16 v[74:77], v[180:183], v[232:235], v[74:77]
	v_mfma_f32_16x16x32_bf16 v[118:121], v[184:187], v[204:207], v[118:121]
	v_mfma_f32_16x16x32_bf16 v[114:117], v[192:195], v[204:207], v[114:117]
	v_mfma_f32_16x16x32_bf16 v[102:105], v[184:187], v[208:211], v[102:105]
	v_mfma_f32_16x16x32_bf16 v[98:101], v[192:195], v[208:211], v[98:101]
	v_mfma_f32_16x16x32_bf16 v[86:89], v[184:187], v[220:223], v[86:89]
	v_mfma_f32_16x16x32_bf16 v[82:85], v[192:195], v[220:223], v[82:85]
	v_mfma_f32_16x16x32_bf16 v[70:73], v[184:187], v[224:227], v[70:73]
	v_mfma_f32_16x16x32_bf16 v[66:69], v[192:195], v[224:227], v[66:69]
	v_mfma_f32_16x16x32_bf16 v[118:121], v[188:191], v[212:215], v[118:121]
	v_mfma_f32_16x16x32_bf16 v[114:117], v[200:203], v[212:215], v[114:117]
	v_mfma_f32_16x16x32_bf16 v[102:105], v[188:191], v[216:219], v[102:105]
	v_mfma_f32_16x16x32_bf16 v[98:101], v[200:203], v[216:219], v[98:101]
	v_mfma_f32_16x16x32_bf16 v[86:89], v[188:191], v[228:231], v[86:89]
	v_mfma_f32_16x16x32_bf16 v[82:85], v[200:203], v[228:231], v[82:85]
	v_mfma_f32_16x16x32_bf16 v[70:73], v[188:191], v[232:235], v[70:73]
	v_mfma_f32_16x16x32_bf16 v[66:69], v[200:203], v[232:235], v[66:69]
	s_setprio 0
	s_barrier
	s_setprio 3
	s_add_i32 s65, s58, s39
	v_lshl_add_u64 v[196:197], s[34:35], 0, v[132:133]
	s_mov_b32 m0, s65
	ds_read_b128 v[204:207], v161 offset:16384
	ds_read_b128 v[208:211], v161 offset:18432
	ds_read_b128 v[212:215], v162 offset:16384
	ds_read_b128 v[216:219], v162 offset:18432
	ds_read_b128 v[220:223], v161 offset:20480
	ds_read_b128 v[224:227], v161 offset:22528
	ds_read_b128 v[228:231], v162 offset:20480
	ds_read_b128 v[232:235], v162 offset:22528
	global_load_lds_dwordx4 v[196:197], off
	s_add_i32 m0, s65, 0x2000
	s_add_u32 s66, s34, 0x40000
	v_lshl_add_u64 v[236:237], s[34:35], 0, v[130:131]
	s_addc_u32 s67, s35, 0
	s_add_i32 s65, s59, s39
	global_load_lds_dwordx4 v[236:237], off
	v_lshl_add_u64 v[238:239], s[66:67], 0, v[132:133]
	s_mov_b32 m0, s65
	s_nop 0
	global_load_lds_dwordx4 v[238:239], off
	v_lshl_add_u64 v[238:239], s[66:67], 0, v[130:131]
	s_add_i32 m0, s65, 0x2000
	s_nop 0
	global_load_lds_dwordx4 v[238:239], off
	v_lshl_add_u64 v[238:239], s[36:37], 0, v[134:135]
	s_mov_b32 m0, s27
	s_nop 0
	global_load_lds_dwordx4 v[238:239], off
	v_lshl_add_u64 v[238:239], s[36:37], 0, v[136:137]
	s_mov_b32 m0, s48
	s_nop 0
	global_load_lds_dwordx4 v[238:239], off
	s_waitcnt vmcnt(8)
	s_waitcnt lgkmcnt(0)
	s_barrier
; #define PG8_STAGE(bufoff, gbase, voff) do { _Pragma("unroll") for (int _i = 0; _i < 2; ++_i) \
;         __builtin_amdgcn_global_load_lds((const unsigned*)((const char*)(gbase) + (voff)[_i]), (LAS unsigned*)(lds + (bufoff) + ldsw + _i * 8192), 16, 0, 0); } while (0)
; #define PG8_LDA(dst, b, h) do { _Pragma("unroll") for (int m = 0; m < 4; ++m) _Pragma("unroll") for (int k = 0; k < 2; ++k) dst[m][k] = *(const LAS bf16x8*)(lds + PG8_SA(b, h) + ((aoff ^ (k * 64)) + m * 2048)); } while (0)
; #define PG8_LDB(dst, b, h) do { _Pragma("unroll") for (int n = 0; n < 2; ++n) _Pragma("unroll") for (int k = 0; k < 2; ++k) dst[n][k] = *(const LAS bf16x8*)(lds + PG8_SB(b, h) + ((boff ^ (k * 64)) + n * 2048)); } while (0)
; #define PG8_MMA(ai, bj, At, Bt) do { __builtin_amdgcn_s_setprio(1); _Pragma("unroll") for (int m = 0; m < 4; ++m) _Pragma("unroll") for (int n = 0; n < 2; ++n) _Pragma("unroll") for (int k = 0; k < 2; ++k) \
;         acc[ai][bj][m][n] = __builtin_amdgcn_mfma_f32_16x16x32_bf16(Bt[n][k], At[m][k], acc[ai][bj][m][n], 0, 0, 0); __builtin_amdgcn_s_setprio(0); } while (0)
; #define PG8_WAIT_V(n) asm volatile("s_waitcnt vmcnt(" #n ")" ::: "memory")
; #define PG8_WAIT_L(n) asm volatile("s_waitcnt lgkmcnt(" #n ")" ::: "memory")
; #define PG8_BAR __builtin_amdgcn_s_barrier()
; #define PG8_SCHED __builtin_amdgcn_sched_barrier(0)
;     ...
;             PG8_WAIT_V(8); PG8_WAIT_L(0); PG8_BAR; if (do1) { PG8_MMA(1, 0, At, B0); PG8_MMA(1, 1, At, B1); } PG8_BAR; PG8_SCHED;
;             PG8_LDB(B0, 1, 0); PG8_LDB(B1, 1, 1); PG8_SCHED; PG8_LDA(At, 1, 0); PG8_STAGE(PG8_SA(0, 1), a2, vs[1]);
;             PG8_WAIT_V(8); PG8_WAIT_L(0); PG8_BAR; if (do0) { PG8_MMA(0, 0, At, B0); PG8_MMA(0, 1, At, B1); } PG8_BAR; PG8_SCHED;
	s_setprio 1
	s_waitcnt lgkmcnt(0)
	v_mfma_f32_16x16x32_bf16 v[62:65], v[168:171], v[204:207], v[62:65]
	v_mfma_f32_16x16x32_bf16 v[58:61], v[176:179], v[204:207], v[58:61]
	v_mfma_f32_16x16x32_bf16 v[46:49], v[168:171], v[208:211], v[46:49]
	v_mfma_f32_16x16x32_bf16 v[42:45], v[176:179], v[208:211], v[42:45]
	v_mfma_f32_16x16x32_bf16 v[30:33], v[168:171], v[220:223], v[30:33]
	v_mfma_f32_16x16x32_bf16 v[26:29], v[176:179], v[220:223], v[26:29]
	v_mfma_f32_16x16x32_bf16 v[14:17], v[168:171], v[224:227], v[14:17]
	v_mfma_f32_16x16x32_bf16 v[10:13], v[176:179], v[224:227], v[10:13]
	v_mfma_f32_16x16x32_bf16 v[62:65], v[172:175], v[212:215], v[62:65]
	v_mfma_f32_16x16x32_bf16 v[58:61], v[180:183], v[212:215], v[58:61]
	v_mfma_f32_16x16x32_bf16 v[46:49], v[172:175], v[216:219], v[46:49]
	v_mfma_f32_16x16x32_bf16 v[42:45], v[180:183], v[216:219], v[42:45]
	v_mfma_f32_16x16x32_bf16 v[30:33], v[172:175], v[228:231], v[30:33]
	v_mfma_f32_16x16x32_bf16 v[26:29], v[180:183], v[228:231], v[26:29]
	v_mfma_f32_16x16x32_bf16 v[14:17], v[172:175], v[232:235], v[14:17]
	v_mfma_f32_16x16x32_bf16 v[10:13], v[180:183], v[232:235], v[10:13]
	v_mfma_f32_16x16x32_bf16 v[54:57], v[184:187], v[204:207], v[54:57]
	v_mfma_f32_16x16x32_bf16 v[50:53], v[192:195], v[204:207], v[50:53]
	v_mfma_f32_16x16x32_bf16 v[38:41], v[184:187], v[208:211], v[38:41]
	v_mfma_f32_16x16x32_bf16 v[34:37], v[192:195], v[208:211], v[34:37]
	v_mfma_f32_16x16x32_bf16 v[22:25], v[184:187], v[220:223], v[22:25]
	v_mfma_f32_16x16x32_bf16 v[18:21], v[192:195], v[220:223], v[18:21]
	v_mfma_f32_16x16x32_bf16 v[6:9], v[184:187], v[224:227], v[6:9]
	v_mfma_f32_16x16x32_bf16 v[2:5], v[192:195], v[224:227], v[2:5]
	v_mfma_f32_16x16x32_bf16 v[54:57], v[188:191], v[212:215], v[54:57]
	v_mfma_f32_16x16x32_bf16 v[50:53], v[200:203], v[212:215], v[50:53]
	v_mfma_f32_16x16x32_bf16 v[38:41], v[188:191], v[216:219], v[38:41]
	v_mfma_f32_16x16x32_bf16 v[34:37], v[200:203], v[216:219], v[34:37]
	v_mfma_f32_16x16x32_bf16 v[22:25], v[188:191], v[228:231], v[22:25]
	v_mfma_f32_16x16x32_bf16 v[18:21], v[200:203], v[228:231], v[18:21]
	v_mfma_f32_16x16x32_bf16 v[6:9], v[188:191], v[232:235], v[6:9]
	v_mfma_f32_16x16x32_bf16 v[2:5], v[200:203], v[232:235], v[2:5]
	s_setprio 0
	s_barrier
	s_setprio 3
	s_add_i32 s65, 0, 0x18000
	v_add_u32_e32 v167, s65, v143
	v_add_u32_e32 v172, s65, v152
	s_add_i32 s66, 0, 0x1c000
	ds_read_b128 v[168:171], v167
	ds_read_b128 v[172:175], v172
	ds_read_b128 v[176:179], v163
	ds_read_b128 v[180:183], v164
	v_add_u32_e32 v167, s66, v143
	v_add_u32_e32 v188, s66, v152
	ds_read_b128 v[184:187], v167
	ds_read_b128 v[188:191], v188
	ds_read_b128 v[192:195], v165
	ds_read_b128 v[200:203], v166
	s_mov_b32 m0, s49
	v_lshl_add_u64 v[238:239], s[36:37], 0, v[138:139]
	ds_read_b128 v[204:207], v161 offset:32768
	ds_read_b128 v[208:211], v161 offset:34816
	ds_read_b128 v[212:215], v162 offset:32768
	ds_read_b128 v[216:219], v162 offset:34816
	ds_read_b128 v[220:223], v161 offset:36864
	ds_read_b128 v[224:227], v161 offset:38912
	ds_read_b128 v[228:231], v162 offset:36864
	ds_read_b128 v[232:235], v162 offset:38912
	global_load_lds_dwordx4 v[238:239], off
	v_lshl_add_u64 v[238:239], s[36:37], 0, v[140:141]
	s_mov_b32 m0, s50
	s_nop 0
	global_load_lds_dwordx4 v[238:239], off
	s_waitcnt vmcnt(8)
	s_waitcnt lgkmcnt(0)
	s_barrier
	s_setprio 1
	s_waitcnt lgkmcnt(0)
	v_mfma_f32_16x16x32_bf16 v[126:129], v[168:171], v[204:207], v[126:129]
	v_mfma_f32_16x16x32_bf16 v[122:125], v[176:179], v[204:207], v[122:125]
	v_mfma_f32_16x16x32_bf16 v[110:113], v[168:171], v[208:211], v[110:113]
	v_mfma_f32_16x16x32_bf16 v[106:109], v[176:179], v[208:211], v[106:109]
	v_mfma_f32_16x16x32_bf16 v[94:97], v[168:171], v[220:223], v[94:97]
	v_mfma_f32_16x16x32_bf16 v[90:93], v[176:179], v[220:223], v[90:93]
	v_mfma_f32_16x16x32_bf16 v[78:81], v[168:171], v[224:227], v[78:81]
	v_mfma_f32_16x16x32_bf16 v[74:77], v[176:179], v[224:227], v[74:77]
	v_mfma_f32_16x16x32_bf16 v[126:129], v[172:175], v[212:215], v[126:129]
	v_mfma_f32_16x16x32_bf16 v[122:125], v[180:183], v[212:215], v[122:125]
	v_mfma_f32_16x16x32_bf16 v[110:113], v[172:175], v[216:219], v[110:113]
	v_mfma_f32_16x16x32_bf16 v[106:109], v[180:183], v[216:219], v[106:109]
	v_mfma_f32_16x16x32_bf16 v[94:97], v[172:175], v[228:231], v[94:97]
	v_mfma_f32_16x16x32_bf16 v[90:93], v[180:183], v[228:231], v[90:93]
	v_mfma_f32_16x16x32_bf16 v[78:81], v[172:175], v[232:235], v[78:81]
	v_mfma_f32_16x16x32_bf16 v[74:77], v[180:183], v[232:235], v[74:77]
	v_mfma_f32_16x16x32_bf16 v[118:121], v[184:187], v[204:207], v[118:121]
	v_mfma_f32_16x16x32_bf16 v[114:117], v[192:195], v[204:207], v[114:117]
	v_mfma_f32_16x16x32_bf16 v[102:105], v[184:187], v[208:211], v[102:105]
	v_mfma_f32_16x16x32_bf16 v[98:101], v[192:195], v[208:211], v[98:101]
	v_mfma_f32_16x16x32_bf16 v[86:89], v[184:187], v[220:223], v[86:89]
	v_mfma_f32_16x16x32_bf16 v[82:85], v[192:195], v[220:223], v[82:85]
	v_mfma_f32_16x16x32_bf16 v[70:73], v[184:187], v[224:227], v[70:73]
	v_mfma_f32_16x16x32_bf16 v[66:69], v[192:195], v[224:227], v[66:69]
	v_mfma_f32_16x16x32_bf16 v[118:121], v[188:191], v[212:215], v[118:121]
	v_mfma_f32_16x16x32_bf16 v[114:117], v[200:203], v[212:215], v[114:117]
	v_mfma_f32_16x16x32_bf16 v[102:105], v[188:191], v[216:219], v[102:105]
	v_mfma_f32_16x16x32_bf16 v[98:101], v[200:203], v[216:219], v[98:101]
	v_mfma_f32_16x16x32_bf16 v[86:89], v[188:191], v[228:231], v[86:89]
	v_mfma_f32_16x16x32_bf16 v[82:85], v[200:203], v[228:231], v[82:85]
	v_mfma_f32_16x16x32_bf16 v[70:73], v[188:191], v[232:235], v[70:73]
	v_mfma_f32_16x16x32_bf16 v[66:69], v[200:203], v[232:235], v[66:69]
	s_setprio 0
	s_barrier
; #define PG8_STAGE(bufoff, gbase, voff) do { _Pragma("unroll") for (int _i = 0; _i < 2; ++_i) \
;         __builtin_amdgcn_global_load_lds((const unsigned*)((const char*)(gbase) + (voff)[_i]), (LAS unsigned*)(lds + (bufoff) + ldsw + _i * 8192), 16, 0, 0); } while (0)
; #define PG8_LDA(dst, b, h) do { _Pragma("unroll") for (int m = 0; m < 4; ++m) _Pragma("unroll") for (int k = 0; k < 2; ++k) dst[m][k] = *(const LAS bf16x8*)(lds + PG8_SA(b, h) + ((aoff ^ (k * 64)) + m * 2048)); } while (0)
; #define PG8_MMA(ai, bj, At, Bt) do { __builtin_amdgcn_s_setprio(1); _Pragma("unroll") for (int m = 0; m < 4; ++m) _Pragma("unroll") for (int n = 0; n < 2; ++n) _Pragma("unroll") for (int k = 0; k < 2; ++k) \
;         acc[ai][bj][m][n] = __builtin_amdgcn_mfma_f32_16x16x32_bf16(Bt[n][k], At[m][k], acc[ai][bj][m][n], 0, 0, 0); __builtin_amdgcn_s_setprio(0); } while (0)
; #define PG8_WAIT_V(n) asm volatile("s_waitcnt vmcnt(" #n ")" ::: "memory")
; #define PG8_WAIT_L(n) asm volatile("s_waitcnt lgkmcnt(" #n ")" ::: "memory")
; #define PG8_BAR __builtin_amdgcn_s_barrier()
; #define PG8_SCHED __builtin_amdgcn_sched_barrier(0)
;     ...
;             PG8_LDA(At, 1, 1); PG8_STAGE(PG8_SB(1, 0), b3, voffB); PG8_STAGE(PG8_SB(1, 1), b3 + hstep, voffB); PG8_STAGE(PG8_SA(1, 0), a3, vs[0]);
;             PG8_WAIT_V(8); PG8_WAIT_L(0); PG8_BAR; if (do1) { PG8_MMA(1, 0, At, B0); PG8_MMA(1, 1, At, B1); } PG8_BAR; PG8_SCHED;
;         }
;         if (wr == 0) PG8_BAR;
	s_setprio 3
	s_add_i32 s36, s65, s39
	v_lshl_add_u64 v[196:197], v[196:197], 0, s[12:13]
	s_mov_b32 m0, s36
	ds_read_b128 v[204:207], v161 offset:49152
	ds_read_b128 v[208:211], v161 offset:51200
	ds_read_b128 v[212:215], v162 offset:49152
	ds_read_b128 v[216:219], v162 offset:51200
	ds_read_b128 v[220:223], v161 offset:53248
	ds_read_b128 v[224:227], v161 offset:55296
	ds_read_b128 v[228:231], v162 offset:53248
	ds_read_b128 v[232:235], v162 offset:55296
	global_load_lds_dwordx4 v[196:197], off
	s_add_i32 m0, s36, 0x2000
	s_add_u32 s34, s34, 0x40080
	v_lshl_add_u64 v[196:197], v[236:237], 0, s[12:13]
	s_addc_u32 s35, s35, 0
	s_add_i32 s36, s66, s39
	global_load_lds_dwordx4 v[196:197], off
	v_lshl_add_u64 v[196:197], s[34:35], 0, v[132:133]
	s_mov_b32 m0, s36
	s_nop 0
	global_load_lds_dwordx4 v[196:197], off
	v_lshl_add_u64 v[196:197], s[34:35], 0, v[130:131]
	s_add_i32 m0, s36, 0x2000
	s_nop 0
	global_load_lds_dwordx4 v[196:197], off
	v_lshl_add_u64 v[196:197], s[30:31], 0, v[134:135]
	s_mov_b32 m0, s55
	s_nop 0
	global_load_lds_dwordx4 v[196:197], off
	v_lshl_add_u64 v[196:197], s[30:31], 0, v[136:137]
	s_mov_b32 m0, s56
	s_nop 0
	global_load_lds_dwordx4 v[196:197], off
	s_waitcnt vmcnt(8)
	s_waitcnt lgkmcnt(0)
	s_barrier
	s_setprio 1
	s_waitcnt lgkmcnt(0)
	v_mfma_f32_16x16x32_bf16 v[62:65], v[168:171], v[204:207], v[62:65]
	v_mfma_f32_16x16x32_bf16 v[58:61], v[176:179], v[204:207], v[58:61]
	v_mfma_f32_16x16x32_bf16 v[46:49], v[168:171], v[208:211], v[46:49]
	v_mfma_f32_16x16x32_bf16 v[42:45], v[176:179], v[208:211], v[42:45]
	v_mfma_f32_16x16x32_bf16 v[30:33], v[168:171], v[220:223], v[30:33]
	v_mfma_f32_16x16x32_bf16 v[26:29], v[176:179], v[220:223], v[26:29]
	v_mfma_f32_16x16x32_bf16 v[14:17], v[168:171], v[224:227], v[14:17]
	v_mfma_f32_16x16x32_bf16 v[10:13], v[176:179], v[224:227], v[10:13]
	v_mfma_f32_16x16x32_bf16 v[62:65], v[172:175], v[212:215], v[62:65]
	v_mfma_f32_16x16x32_bf16 v[58:61], v[180:183], v[212:215], v[58:61]
	v_mfma_f32_16x16x32_bf16 v[46:49], v[172:175], v[216:219], v[46:49]
	v_mfma_f32_16x16x32_bf16 v[42:45], v[180:183], v[216:219], v[42:45]
	v_mfma_f32_16x16x32_bf16 v[30:33], v[172:175], v[228:231], v[30:33]
	v_mfma_f32_16x16x32_bf16 v[26:29], v[180:183], v[228:231], v[26:29]
	v_mfma_f32_16x16x32_bf16 v[14:17], v[172:175], v[232:235], v[14:17]
	v_mfma_f32_16x16x32_bf16 v[10:13], v[180:183], v[232:235], v[10:13]
	v_mfma_f32_16x16x32_bf16 v[54:57], v[184:187], v[204:207], v[54:57]
	v_mfma_f32_16x16x32_bf16 v[50:53], v[192:195], v[204:207], v[50:53]
	v_mfma_f32_16x16x32_bf16 v[38:41], v[184:187], v[208:211], v[38:41]
	v_mfma_f32_16x16x32_bf16 v[34:37], v[192:195], v[208:211], v[34:37]
	v_mfma_f32_16x16x32_bf16 v[22:25], v[184:187], v[220:223], v[22:25]
	v_mfma_f32_16x16x32_bf16 v[18:21], v[192:195], v[220:223], v[18:21]
	v_mfma_f32_16x16x32_bf16 v[6:9], v[184:187], v[224:227], v[6:9]
	v_mfma_f32_16x16x32_bf16 v[2:5], v[192:195], v[224:227], v[2:5]
	v_mfma_f32_16x16x32_bf16 v[54:57], v[188:191], v[212:215], v[54:57]
	v_mfma_f32_16x16x32_bf16 v[50:53], v[200:203], v[212:215], v[50:53]
	v_mfma_f32_16x16x32_bf16 v[38:41], v[188:191], v[216:219], v[38:41]
	v_mfma_f32_16x16x32_bf16 v[34:37], v[200:203], v[216:219], v[34:37]
	v_mfma_f32_16x16x32_bf16 v[22:25], v[188:191], v[228:231], v[22:25]
	v_mfma_f32_16x16x32_bf16 v[18:21], v[200:203], v[228:231], v[18:21]
	v_mfma_f32_16x16x32_bf16 v[6:9], v[188:191], v[232:235], v[6:9]
	v_mfma_f32_16x16x32_bf16 v[2:5], v[200:203], v[232:235], v[2:5]
	s_setprio 0
	s_barrier
	s_setprio 3
	s_add_i32 s64, s64, 2
	s_add_u32 s62, s62, 0x100
	s_addc_u32 s63, s63, 0
	s_add_u32 s4, s4, 0x8000
	s_addc_u32 s5, s5, 0
	s_cmp_gt_u32 s64, 13
	s_cbranch_scc0 .LBB0_212
	s_and_b64 vcc, exec, s[14:15]
	s_cbranch_vccz .LBB0_215
	s_barrier

; #define PG8_STAGE(bufoff, gbase, voff) do { _Pragma("unroll") for (int _i = 0; _i < 2; ++_i) \
;         __builtin_amdgcn_global_load_lds((const unsigned*)((const char*)(gbase) + (voff)[_i]), (LAS unsigned*)(lds + (bufoff) + ldsw + _i * 8192), 16, 0, 0); } while (0)
; #define PG8_LDA(dst, b, h) do { _Pragma("unroll") for (int m = 0; m < 4; ++m) _Pragma("unroll") for (int k = 0; k < 2; ++k) dst[m][k] = *(const LAS bf16x8*)(lds + PG8_SA(b, h) + ((aoff ^ (k * 64)) + m * 2048)); } while (0)
; #define PG8_LDB(dst, b, h) do { _Pragma("unroll") for (int n = 0; n < 2; ++n) _Pragma("unroll") for (int k = 0; k < 2; ++k) dst[n][k] = *(const LAS bf16x8*)(lds + PG8_SB(b, h) + ((boff ^ (k * 64)) + n * 2048)); } while (0)
; #define PG8_WAIT_V(n) asm volatile("s_waitcnt vmcnt(" #n ")" ::: "memory")
; #define PG8_WAIT_L(n) asm volatile("s_waitcnt lgkmcnt(" #n ")" ::: "memory")
;     ...
;             const bool last = (t == nt - 2);
;             const char* a1 = cA + (size_t)(t + 1) * kstepA;
;             const char* a2 = last ? nA : cA + (size_t)(t + 2) * kstepA; const char* b2 = last ? nB : cB + (size_t)(t + 2) * kstepB;
;             const char* a3 = a2 + kstepA; const char* b3 = b2 + kstepB;
;             unsigned vs[2][2];
;             if constexpr (GATHER) {
;                 if (last && has_next) {
; #pragma unroll
;                     for (int hh = 0; hh < 2; ++hh)
; #pragma unroll
;                         for (int i = 0; i < 2; ++i) voffN[hh][i] = (unsigned)idxl[(ui + 1) * 256 + hh * HALF + sR[i]] * (unsigned)(K * 2) + (unsigned)sC[i] * 2u;
;                 }
; #pragma unroll
;                 for (int hh = 0; hh < 2; ++hh)
; #pragma unroll
;                     for (int i = 0; i < 2; ++i) vs[hh][i] = last ? voffN[hh][i] : voffA[hh][i];
;             } else {
; #pragma unroll
;                 for (int hh = 0; hh < 2; ++hh)
; #pragma unroll
;                     for (int i = 0; i < 2; ++i) vs[hh][i] = voffA[hh][i];
;             }
;             PG8_LDB(B0, 0, 0); PG8_LDB(B1, 0, 1); PG8_SCHED; PG8_LDA(At, 0, 0); PG8_STAGE(PG8_SA(1, 1), a1, voffA[1]);
;             PG8_WAIT_V(8); PG8_WAIT_L(0); PG8_BAR; if (do0) { PG8_MMA(0, 0, At, B0); PG8_MMA(0, 1, At, B1); } PG8_BAR; PG8_SCHED;
;             PG8_LDA(At, 0, 1); PG8_STAGE(PG8_SB(0, 0), b2, voffB); PG8_STAGE(PG8_SB(0, 1), b2 + hstep, voffB); PG8_STAGE(PG8_SA(0, 0), a2, vs[0]);
.LBB0_460:
	ds_read_b128 v[130:133], v203
	ds_read_b128 v[134:137], v204
	ds_read_b128 v[138:141], v205
	ds_read_b128 v[142:145], v206
	ds_read_b128 v[168:171], v207
	ds_read_b128 v[172:175], v208
	ds_read_b128 v[176:179], v209
	ds_read_b128 v[180:183], v210
	s_add_u32 s4, s2, 0x80
	s_addc_u32 s5, s3, 0
	s_cmp_eq_u32 s41, 12
	s_cselect_b32 s39, s9, s5
	s_cselect_b32 s38, s12, s4
	s_cselect_b32 s5, s27, s40
	s_cselect_b32 s4, s29, s37
	v_lshl_add_u64 v[196:197], s[2:3], 0, v[162:163]
	s_add_i32 m0, s50, 0xc000
	ds_read_b128 v[184:187], v211
	ds_read_b128 v[188:191], v211 offset:2048
	ds_read_b128 v[192:195], v212
	ds_read_b128 v[220:223], v212 offset:2048
	ds_read_b128 v[224:227], v211 offset:4096
	ds_read_b128 v[228:231], v211 offset:6144
	ds_read_b128 v[232:235], v212 offset:4096
	ds_read_b128 v[236:239], v212 offset:6144
	global_load_lds_dwordx4 v[196:197], off
	v_lshl_add_u64 v[196:197], s[2:3], 0, v[160:161]
	s_add_i32 m0, s50, 0xe000
	s_add_u32 s6, s4, 0x4000
	global_load_lds_dwordx4 v[196:197], off
	s_waitcnt vmcnt(8)
	s_waitcnt lgkmcnt(0)
	s_addc_u32 s7, s5, 0
	s_barrier
	s_setprio 1
	s_waitcnt lgkmcnt(0)
	v_mfma_f32_16x16x32_bf16 v[126:129], v[130:133], v[184:187], v[126:129]
	v_mfma_f32_16x16x32_bf16 v[58:61], v[138:141], v[184:187], v[58:61]
	v_mfma_f32_16x16x32_bf16 v[122:125], v[130:133], v[188:191], v[122:125]
	v_mfma_f32_16x16x32_bf16 v[118:121], v[138:141], v[188:191], v[118:121]
	v_mfma_f32_16x16x32_bf16 v[114:117], v[130:133], v[224:227], v[114:117]
	v_mfma_f32_16x16x32_bf16 v[110:113], v[138:141], v[224:227], v[110:113]
	v_mfma_f32_16x16x32_bf16 v[106:109], v[130:133], v[228:231], v[106:109]
	v_mfma_f32_16x16x32_bf16 v[102:105], v[138:141], v[228:231], v[102:105]
	v_mfma_f32_16x16x32_bf16 v[126:129], v[134:137], v[192:195], v[126:129]
	v_mfma_f32_16x16x32_bf16 v[58:61], v[142:145], v[192:195], v[58:61]
	v_mfma_f32_16x16x32_bf16 v[122:125], v[134:137], v[220:223], v[122:125]
	v_mfma_f32_16x16x32_bf16 v[118:121], v[142:145], v[220:223], v[118:121]
	v_mfma_f32_16x16x32_bf16 v[114:117], v[134:137], v[232:235], v[114:117]
	v_mfma_f32_16x16x32_bf16 v[110:113], v[142:145], v[232:235], v[110:113]
	v_mfma_f32_16x16x32_bf16 v[106:109], v[134:137], v[236:239], v[106:109]
	v_mfma_f32_16x16x32_bf16 v[102:105], v[142:145], v[236:239], v[102:105]
	v_mfma_f32_16x16x32_bf16 v[66:69], v[168:171], v[184:187], v[66:69]
	v_mfma_f32_16x16x32_bf16 v[50:53], v[176:179], v[184:187], v[50:53]
	v_mfma_f32_16x16x32_bf16 v[54:57], v[168:171], v[188:191], v[54:57]
	v_mfma_f32_16x16x32_bf16 v[42:45], v[176:179], v[188:191], v[42:45]
	v_mfma_f32_16x16x32_bf16 v[46:49], v[168:171], v[224:227], v[46:49]
	v_mfma_f32_16x16x32_bf16 v[34:37], v[176:179], v[224:227], v[34:37]
	v_mfma_f32_16x16x32_bf16 v[98:101], v[168:171], v[228:231], v[98:101]
	v_mfma_f32_16x16x32_bf16 v[38:41], v[176:179], v[228:231], v[38:41]
	v_mfma_f32_16x16x32_bf16 v[66:69], v[172:175], v[192:195], v[66:69]
	v_mfma_f32_16x16x32_bf16 v[50:53], v[180:183], v[192:195], v[50:53]
	v_mfma_f32_16x16x32_bf16 v[54:57], v[172:175], v[220:223], v[54:57]
	v_mfma_f32_16x16x32_bf16 v[42:45], v[180:183], v[220:223], v[42:45]
	v_mfma_f32_16x16x32_bf16 v[46:49], v[172:175], v[232:235], v[46:49]
	v_mfma_f32_16x16x32_bf16 v[34:37], v[180:183], v[232:235], v[34:37]
	v_mfma_f32_16x16x32_bf16 v[98:101], v[172:175], v[236:239], v[98:101]
	v_mfma_f32_16x16x32_bf16 v[38:41], v[180:183], v[236:239], v[38:41]
	s_setprio 0
	s_barrier
	s_setprio 3
	s_add_i32 s42, s65, s49
	v_lshl_add_u64 v[196:197], s[4:5], 0, v[146:147]
	s_mov_b32 m0, s42
	ds_read_b128 v[184:187], v211 offset:16384
	ds_read_b128 v[188:191], v211 offset:18432
	ds_read_b128 v[192:195], v212 offset:16384
	ds_read_b128 v[220:223], v212 offset:18432
	ds_read_b128 v[224:227], v211 offset:20480
	ds_read_b128 v[228:231], v211 offset:22528
	ds_read_b128 v[232:235], v212 offset:20480
	ds_read_b128 v[236:239], v212 offset:22528
	global_load_lds_dwordx4 v[196:197], off
	s_add_i32 m0, s42, 0x2000
	s_add_u32 s42, s4, 0x40000
	v_lshl_add_u64 v[196:197], s[4:5], 0, v[148:149]
	s_addc_u32 s43, s5, 0
	s_add_i32 s74, s66, s49
	global_load_lds_dwordx4 v[196:197], off
	v_lshl_add_u64 v[196:197], s[42:43], 0, v[146:147]
	s_mov_b32 m0, s74
	v_lshl_add_u64 v[240:241], s[38:39], 0, v[152:153]
	global_load_lds_dwordx4 v[196:197], off
	v_lshl_add_u64 v[196:197], s[42:43], 0, v[148:149]
	s_add_i32 m0, s74, 0x2000
	s_nop 0
	global_load_lds_dwordx4 v[196:197], off
	v_lshl_add_u64 v[196:197], s[38:39], 0, v[150:151]
	s_mov_b32 m0, s50
	s_nop 0
	global_load_lds_dwordx4 v[196:197], off
	s_mov_b32 m0, s51
	s_nop 0
	global_load_lds_dwordx4 v[240:241], off
	s_waitcnt vmcnt(8)
	s_waitcnt lgkmcnt(0)
	s_barrier
; #define PG8_STAGE(bufoff, gbase, voff) do { _Pragma("unroll") for (int _i = 0; _i < 2; ++_i) \
;         __builtin_amdgcn_global_load_lds((const unsigned*)((const char*)(gbase) + (voff)[_i]), (LAS unsigned*)(lds + (bufoff) + ldsw + _i * 8192), 16, 0, 0); } while (0)
; #define PG8_LDA(dst, b, h) do { _Pragma("unroll") for (int m = 0; m < 4; ++m) _Pragma("unroll") for (int k = 0; k < 2; ++k) dst[m][k] = *(const LAS bf16x8*)(lds + PG8_SA(b, h) + ((aoff ^ (k * 64)) + m * 2048)); } while (0)
; #define PG8_LDB(dst, b, h) do { _Pragma("unroll") for (int n = 0; n < 2; ++n) _Pragma("unroll") for (int k = 0; k < 2; ++k) dst[n][k] = *(const LAS bf16x8*)(lds + PG8_SB(b, h) + ((boff ^ (k * 64)) + n * 2048)); } while (0)
; #define PG8_MMA(ai, bj, At, Bt) do { __builtin_amdgcn_s_setprio(1); _Pragma("unroll") for (int m = 0; m < 4; ++m) _Pragma("unroll") for (int n = 0; n < 2; ++n) _Pragma("unroll") for (int k = 0; k < 2; ++k) \
;         acc[ai][bj][m][n] = __builtin_amdgcn_mfma_f32_16x16x32_bf16(Bt[n][k], At[m][k], acc[ai][bj][m][n], 0, 0, 0); __builtin_amdgcn_s_setprio(0); } while (0)
; #define PG8_WAIT_V(n) asm volatile("s_waitcnt vmcnt(" #n ")" ::: "memory")
; #define PG8_WAIT_L(n) asm volatile("s_waitcnt lgkmcnt(" #n ")" ::: "memory")
; #define PG8_BAR __builtin_amdgcn_s_barrier()
; #define PG8_SCHED __builtin_amdgcn_sched_barrier(0)
;     ...
;             PG8_WAIT_V(8); PG8_WAIT_L(0); PG8_BAR; if (do1) { PG8_MMA(1, 0, At, B0); PG8_MMA(1, 1, At, B1); } PG8_BAR; PG8_SCHED;
;             PG8_LDB(B0, 1, 0); PG8_LDB(B1, 1, 1); PG8_SCHED; PG8_LDA(At, 1, 0); PG8_STAGE(PG8_SA(0, 1), a2, vs[1]);
;             PG8_WAIT_V(8); PG8_WAIT_L(0); PG8_BAR; if (do0) { PG8_MMA(0, 0, At, B0); PG8_MMA(0, 1, At, B1); } PG8_BAR; PG8_SCHED;
	s_setprio 1
	s_waitcnt lgkmcnt(0)
	v_mfma_f32_16x16x32_bf16 v[94:97], v[130:133], v[184:187], v[94:97]
	v_mfma_f32_16x16x32_bf16 v[26:29], v[138:141], v[184:187], v[26:29]
	v_mfma_f32_16x16x32_bf16 v[90:93], v[130:133], v[188:191], v[90:93]
	v_mfma_f32_16x16x32_bf16 v[86:89], v[138:141], v[188:191], v[86:89]
	v_mfma_f32_16x16x32_bf16 v[82:85], v[130:133], v[224:227], v[82:85]
	v_mfma_f32_16x16x32_bf16 v[78:81], v[138:141], v[224:227], v[78:81]
	v_mfma_f32_16x16x32_bf16 v[74:77], v[130:133], v[228:231], v[74:77]
	v_mfma_f32_16x16x32_bf16 v[70:73], v[138:141], v[228:231], v[70:73]
	v_mfma_f32_16x16x32_bf16 v[94:97], v[134:137], v[192:195], v[94:97]
	v_mfma_f32_16x16x32_bf16 v[26:29], v[142:145], v[192:195], v[26:29]
	v_mfma_f32_16x16x32_bf16 v[90:93], v[134:137], v[220:223], v[90:93]
	v_mfma_f32_16x16x32_bf16 v[86:89], v[142:145], v[220:223], v[86:89]
	v_mfma_f32_16x16x32_bf16 v[82:85], v[134:137], v[232:235], v[82:85]
	v_mfma_f32_16x16x32_bf16 v[78:81], v[142:145], v[232:235], v[78:81]
	v_mfma_f32_16x16x32_bf16 v[74:77], v[134:137], v[236:239], v[74:77]
	v_mfma_f32_16x16x32_bf16 v[70:73], v[142:145], v[236:239], v[70:73]
	v_mfma_f32_16x16x32_bf16 v[30:33], v[168:171], v[184:187], v[30:33]
	v_mfma_f32_16x16x32_bf16 v[18:21], v[176:179], v[184:187], v[18:21]
	v_mfma_f32_16x16x32_bf16 v[22:25], v[168:171], v[188:191], v[22:25]
	v_mfma_f32_16x16x32_bf16 v[10:13], v[176:179], v[188:191], v[10:13]
	v_mfma_f32_16x16x32_bf16 v[14:17], v[168:171], v[224:227], v[14:17]
	v_mfma_f32_16x16x32_bf16 v[2:5], v[176:179], v[224:227], v[2:5]
	v_mfma_f32_16x16x32_bf16 v[62:65], v[168:171], v[228:231], v[62:65]
	v_mfma_f32_16x16x32_bf16 v[6:9], v[176:179], v[228:231], v[6:9]
	v_mfma_f32_16x16x32_bf16 v[30:33], v[172:175], v[192:195], v[30:33]
	v_mfma_f32_16x16x32_bf16 v[18:21], v[180:183], v[192:195], v[18:21]
	v_mfma_f32_16x16x32_bf16 v[22:25], v[172:175], v[220:223], v[22:25]
	v_mfma_f32_16x16x32_bf16 v[10:13], v[180:183], v[220:223], v[10:13]
	v_mfma_f32_16x16x32_bf16 v[14:17], v[172:175], v[232:235], v[14:17]
	v_mfma_f32_16x16x32_bf16 v[2:5], v[180:183], v[232:235], v[2:5]
	v_mfma_f32_16x16x32_bf16 v[62:65], v[172:175], v[236:239], v[62:65]
	v_mfma_f32_16x16x32_bf16 v[6:9], v[180:183], v[236:239], v[6:9]
	s_setprio 0
	s_barrier
	s_setprio 3
	s_add_i32 s42, 0, 0x18000
	s_add_i32 s43, 0, 0x1c000
	v_add_u32_e32 v130, s42, v201
	v_add_u32_e32 v134, s42, v202
	v_add_u32_e32 v158, s43, v201
	v_add_u32_e32 v172, s43, v202
	ds_read_b128 v[130:133], v130
	ds_read_b128 v[134:137], v134
	ds_read_b128 v[138:141], v213
	ds_read_b128 v[142:145], v214
	ds_read_b128 v[168:171], v158
	ds_read_b128 v[172:175], v172
	ds_read_b128 v[176:179], v215
	ds_read_b128 v[180:183], v216
	s_mov_b32 m0, s52
	v_lshl_add_u64 v[242:243], s[38:39], 0, v[154:155]
	ds_read_b128 v[184:187], v211 offset:32768
	ds_read_b128 v[188:191], v211 offset:34816
	ds_read_b128 v[192:195], v212 offset:32768
	ds_read_b128 v[220:223], v212 offset:34816
	ds_read_b128 v[224:227], v211 offset:36864
	ds_read_b128 v[228:231], v211 offset:38912
	ds_read_b128 v[232:235], v212 offset:36864
	ds_read_b128 v[236:239], v212 offset:38912
	global_load_lds_dwordx4 v[242:243], off
	v_lshl_add_u64 v[242:243], s[38:39], 0, v[156:157]
	s_mov_b32 m0, s53
	s_nop 0
	global_load_lds_dwordx4 v[242:243], off
	s_waitcnt vmcnt(8)
	s_waitcnt lgkmcnt(0)
	s_barrier
	s_setprio 1
	s_waitcnt lgkmcnt(0)
	v_mfma_f32_16x16x32_bf16 v[126:129], v[130:133], v[184:187], v[126:129]
	v_mfma_f32_16x16x32_bf16 v[58:61], v[138:141], v[184:187], v[58:61]
	v_mfma_f32_16x16x32_bf16 v[122:125], v[130:133], v[188:191], v[122:125]
	v_mfma_f32_16x16x32_bf16 v[118:121], v[138:141], v[188:191], v[118:121]
	v_mfma_f32_16x16x32_bf16 v[114:117], v[130:133], v[224:227], v[114:117]
	v_mfma_f32_16x16x32_bf16 v[110:113], v[138:141], v[224:227], v[110:113]
	v_mfma_f32_16x16x32_bf16 v[106:109], v[130:133], v[228:231], v[106:109]
	v_mfma_f32_16x16x32_bf16 v[102:105], v[138:141], v[228:231], v[102:105]
	v_mfma_f32_16x16x32_bf16 v[126:129], v[134:137], v[192:195], v[126:129]
	v_mfma_f32_16x16x32_bf16 v[58:61], v[142:145], v[192:195], v[58:61]
	v_mfma_f32_16x16x32_bf16 v[122:125], v[134:137], v[220:223], v[122:125]
	v_mfma_f32_16x16x32_bf16 v[118:121], v[142:145], v[220:223], v[118:121]
	v_mfma_f32_16x16x32_bf16 v[114:117], v[134:137], v[232:235], v[114:117]
	v_mfma_f32_16x16x32_bf16 v[110:113], v[142:145], v[232:235], v[110:113]
	v_mfma_f32_16x16x32_bf16 v[106:109], v[134:137], v[236:239], v[106:109]
	v_mfma_f32_16x16x32_bf16 v[102:105], v[142:145], v[236:239], v[102:105]
	v_mfma_f32_16x16x32_bf16 v[66:69], v[168:171], v[184:187], v[66:69]
	v_mfma_f32_16x16x32_bf16 v[50:53], v[176:179], v[184:187], v[50:53]
	v_mfma_f32_16x16x32_bf16 v[54:57], v[168:171], v[188:191], v[54:57]
	v_mfma_f32_16x16x32_bf16 v[42:45], v[176:179], v[188:191], v[42:45]
	v_mfma_f32_16x16x32_bf16 v[46:49], v[168:171], v[224:227], v[46:49]
	v_mfma_f32_16x16x32_bf16 v[34:37], v[176:179], v[224:227], v[34:37]
	v_mfma_f32_16x16x32_bf16 v[98:101], v[168:171], v[228:231], v[98:101]
	v_mfma_f32_16x16x32_bf16 v[38:41], v[176:179], v[228:231], v[38:41]
	v_mfma_f32_16x16x32_bf16 v[66:69], v[172:175], v[192:195], v[66:69]
	v_mfma_f32_16x16x32_bf16 v[50:53], v[180:183], v[192:195], v[50:53]
	v_mfma_f32_16x16x32_bf16 v[54:57], v[172:175], v[220:223], v[54:57]
	v_mfma_f32_16x16x32_bf16 v[42:45], v[180:183], v[220:223], v[42:45]
	v_mfma_f32_16x16x32_bf16 v[46:49], v[172:175], v[232:235], v[46:49]
	v_mfma_f32_16x16x32_bf16 v[34:37], v[180:183], v[232:235], v[34:37]
	v_mfma_f32_16x16x32_bf16 v[98:101], v[172:175], v[236:239], v[98:101]
	v_mfma_f32_16x16x32_bf16 v[38:41], v[180:183], v[236:239], v[38:41]
	s_setprio 0
	s_barrier
; #define PG8_STAGE(bufoff, gbase, voff) do { _Pragma("unroll") for (int _i = 0; _i < 2; ++_i) \
;         __builtin_amdgcn_global_load_lds((const unsigned*)((const char*)(gbase) + (voff)[_i]), (LAS unsigned*)(lds + (bufoff) + ldsw + _i * 8192), 16, 0, 0); } while (0)
; #define PG8_LDA(dst, b, h) do { _Pragma("unroll") for (int m = 0; m < 4; ++m) _Pragma("unroll") for (int k = 0; k < 2; ++k) dst[m][k] = *(const LAS bf16x8*)(lds + PG8_SA(b, h) + ((aoff ^ (k * 64)) + m * 2048)); } while (0)
; #define PG8_MMA(ai, bj, At, Bt) do { __builtin_amdgcn_s_setprio(1); _Pragma("unroll") for (int m = 0; m < 4; ++m) _Pragma("unroll") for (int n = 0; n < 2; ++n) _Pragma("unroll") for (int k = 0; k < 2; ++k) \
;         acc[ai][bj][m][n] = __builtin_amdgcn_mfma_f32_16x16x32_bf16(Bt[n][k], At[m][k], acc[ai][bj][m][n], 0, 0, 0); __builtin_amdgcn_s_setprio(0); } while (0)
; #define PG8_WAIT_V(n) asm volatile("s_waitcnt vmcnt(" #n ")" ::: "memory")
; #define PG8_WAIT_L(n) asm volatile("s_waitcnt lgkmcnt(" #n ")" ::: "memory")
; #define PG8_BAR __builtin_amdgcn_s_barrier()
; #define PG8_SCHED __builtin_amdgcn_sched_barrier(0)
;     ...
;             PG8_LDA(At, 1, 1); PG8_STAGE(PG8_SB(1, 0), b3, voffB); PG8_STAGE(PG8_SB(1, 1), b3 + hstep, voffB); PG8_STAGE(PG8_SA(1, 0), a3, vs[0]);
;             PG8_WAIT_V(8); PG8_WAIT_L(0); PG8_BAR; if (do1) { PG8_MMA(1, 0, At, B0); PG8_MMA(1, 1, At, B1); } PG8_BAR; PG8_SCHED;
;         }
;         if (wr == 0) PG8_BAR;
	s_setprio 3
	s_add_i32 s38, s42, s49
	v_lshl_add_u64 v[242:243], s[6:7], 0, v[146:147]
	s_mov_b32 m0, s38
	ds_read_b128 v[184:187], v211 offset:49152
	ds_read_b128 v[188:191], v211 offset:51200
	ds_read_b128 v[192:195], v212 offset:49152
	ds_read_b128 v[220:223], v212 offset:51200
	ds_read_b128 v[224:227], v211 offset:53248
	ds_read_b128 v[228:231], v211 offset:55296
	ds_read_b128 v[232:235], v212 offset:53248
	ds_read_b128 v[236:239], v212 offset:55296
	global_load_lds_dwordx4 v[242:243], off
	s_add_i32 m0, s38, 0x2000
	s_add_u32 s4, s4, 0x44000
	v_lshl_add_u64 v[242:243], s[6:7], 0, v[148:149]
	s_addc_u32 s5, s5, 0
	s_add_i32 s6, s43, s49
	global_load_lds_dwordx4 v[242:243], off
	v_lshl_add_u64 v[242:243], s[4:5], 0, v[146:147]
	s_mov_b32 m0, s6
	v_lshl_add_u64 v[196:197], v[196:197], 0, s[92:93]
	global_load_lds_dwordx4 v[242:243], off
	v_lshl_add_u64 v[242:243], s[4:5], 0, v[148:149]
	s_add_i32 m0, s6, 0x2000
	s_nop 0
	global_load_lds_dwordx4 v[242:243], off
	s_mov_b32 m0, s55
	s_nop 0
	global_load_lds_dwordx4 v[196:197], off
	v_lshl_add_u64 v[196:197], v[240:241], 0, s[92:93]
	s_mov_b32 m0, s56
	s_nop 0
	global_load_lds_dwordx4 v[196:197], off
	s_waitcnt vmcnt(8)
	s_waitcnt lgkmcnt(0)
	s_barrier
	s_setprio 1
	s_waitcnt lgkmcnt(0)
	v_mfma_f32_16x16x32_bf16 v[94:97], v[130:133], v[184:187], v[94:97]
	v_mfma_f32_16x16x32_bf16 v[26:29], v[138:141], v[184:187], v[26:29]
	v_mfma_f32_16x16x32_bf16 v[90:93], v[130:133], v[188:191], v[90:93]
	v_mfma_f32_16x16x32_bf16 v[86:89], v[138:141], v[188:191], v[86:89]
	v_mfma_f32_16x16x32_bf16 v[82:85], v[130:133], v[224:227], v[82:85]
	v_mfma_f32_16x16x32_bf16 v[78:81], v[138:141], v[224:227], v[78:81]
	v_mfma_f32_16x16x32_bf16 v[74:77], v[130:133], v[228:231], v[74:77]
	v_mfma_f32_16x16x32_bf16 v[70:73], v[138:141], v[228:231], v[70:73]
	v_mfma_f32_16x16x32_bf16 v[94:97], v[134:137], v[192:195], v[94:97]
	v_mfma_f32_16x16x32_bf16 v[26:29], v[142:145], v[192:195], v[26:29]
	v_mfma_f32_16x16x32_bf16 v[90:93], v[134:137], v[220:223], v[90:93]
	v_mfma_f32_16x16x32_bf16 v[86:89], v[142:145], v[220:223], v[86:89]
	v_mfma_f32_16x16x32_bf16 v[82:85], v[134:137], v[232:235], v[82:85]
	v_mfma_f32_16x16x32_bf16 v[78:81], v[142:145], v[232:235], v[78:81]
	v_mfma_f32_16x16x32_bf16 v[74:77], v[134:137], v[236:239], v[74:77]
	v_mfma_f32_16x16x32_bf16 v[70:73], v[142:145], v[236:239], v[70:73]
	v_mfma_f32_16x16x32_bf16 v[30:33], v[168:171], v[184:187], v[30:33]
	v_mfma_f32_16x16x32_bf16 v[18:21], v[176:179], v[184:187], v[18:21]
	v_mfma_f32_16x16x32_bf16 v[22:25], v[168:171], v[188:191], v[22:25]
	v_mfma_f32_16x16x32_bf16 v[10:13], v[176:179], v[188:191], v[10:13]
	v_mfma_f32_16x16x32_bf16 v[14:17], v[168:171], v[224:227], v[14:17]
	v_mfma_f32_16x16x32_bf16 v[2:5], v[176:179], v[224:227], v[2:5]
	v_mfma_f32_16x16x32_bf16 v[62:65], v[168:171], v[228:231], v[62:65]
	v_mfma_f32_16x16x32_bf16 v[6:9], v[176:179], v[228:231], v[6:9]
	v_mfma_f32_16x16x32_bf16 v[30:33], v[172:175], v[192:195], v[30:33]
	v_mfma_f32_16x16x32_bf16 v[18:21], v[180:183], v[192:195], v[18:21]
	v_mfma_f32_16x16x32_bf16 v[22:25], v[172:175], v[220:223], v[22:25]
	v_mfma_f32_16x16x32_bf16 v[10:13], v[180:183], v[220:223], v[10:13]
	v_mfma_f32_16x16x32_bf16 v[14:17], v[172:175], v[232:235], v[14:17]
	v_mfma_f32_16x16x32_bf16 v[2:5], v[180:183], v[232:235], v[2:5]
	v_mfma_f32_16x16x32_bf16 v[62:65], v[172:175], v[236:239], v[62:65]
	v_mfma_f32_16x16x32_bf16 v[6:9], v[180:183], v[236:239], v[6:9]
	s_setprio 0
	s_barrier
	s_setprio 3
	s_add_i32 s41, s41, 2
	s_add_u32 s37, s37, 0x8000
	s_addc_u32 s40, s40, 0
	s_add_u32 s2, s2, 0x100
	s_addc_u32 s3, s3, 0
	s_cmp_gt_u32 s41, 13
	s_cbranch_scc0 .LBB0_460
	s_and_b64 vcc, exec, s[24:25]
	s_cbranch_vccz .LBB0_463
	s_barrier

; #define PG8_STAGE(bufoff, gbase, voff) do { _Pragma("unroll") for (int _i = 0; _i < 2; ++_i) \
;         __builtin_amdgcn_global_load_lds((const unsigned*)((const char*)(gbase) + (voff)[_i]), (LAS unsigned*)(lds + (bufoff) + ldsw + _i * 8192), 16, 0, 0); } while (0)
; #define PG8_LDA(dst, b, h) do { _Pragma("unroll") for (int m = 0; m < 4; ++m) _Pragma("unroll") for (int k = 0; k < 2; ++k) dst[m][k] = *(const LAS bf16x8*)(lds + PG8_SA(b, h) + ((aoff ^ (k * 64)) + m * 2048)); } while (0)
; #define PG8_LDB(dst, b, h) do { _Pragma("unroll") for (int n = 0; n < 2; ++n) _Pragma("unroll") for (int k = 0; k < 2; ++k) dst[n][k] = *(const LAS bf16x8*)(lds + PG8_SB(b, h) + ((boff ^ (k * 64)) + n * 2048)); } while (0)
; #define PG8_WAIT_V(n) asm volatile("s_waitcnt vmcnt(" #n ")" ::: "memory")
; #define PG8_BAR __builtin_amdgcn_s_barrier()
;     ...
;         for (int t = 0; t < nt; t += 2) {
;             const bool last = (t == nt - 2);
;             const char* a1 = cA + (size_t)(t + 1) * kstepA;
;             const char* a2 = last ? nA : cA + (size_t)(t + 2) * kstepA; const char* b2 = last ? nB : cB + (size_t)(t + 2) * kstepB;
;             const char* a3 = a2 + kstepA; const char* b3 = b2 + kstepB;
;             unsigned vs[2][2];
;             if constexpr (GATHER) {
;                 if (last && has_next) {
; #pragma unroll
;                     for (int hh = 0; hh < 2; ++hh)
; #pragma unroll
;                         for (int i = 0; i < 2; ++i) voffN[hh][i] = (unsigned)idxl[(ui + 1) * 256 + hh * HALF + sR[i]] * (unsigned)(K * 2) + (unsigned)sC[i] * 2u;
;                 }
; #pragma unroll
;                 for (int hh = 0; hh < 2; ++hh)
; #pragma unroll
;                     for (int i = 0; i < 2; ++i) vs[hh][i] = last ? voffN[hh][i] : voffA[hh][i];
;             } else {
; #pragma unroll
;                 for (int hh = 0; hh < 2; ++hh)
; #pragma unroll
;                     for (int i = 0; i < 2; ++i) vs[hh][i] = voffA[hh][i];
;             }
;             PG8_LDB(B0, 0, 0); PG8_LDB(B1, 0, 1); PG8_SCHED; PG8_LDA(At, 0, 0); PG8_STAGE(PG8_SA(1, 1), a1, voffA[1]);
;             PG8_WAIT_V(8); PG8_WAIT_L(0); PG8_BAR; if (do0) { PG8_MMA(0, 0, At, B0); PG8_MMA(0, 1, At, B1); } PG8_BAR; PG8_SCHED;
;             PG8_LDA(At, 0, 1); PG8_STAGE(PG8_SB(0, 0), b2, voffB); PG8_STAGE(PG8_SB(0, 1), b2 + hstep, voffB); PG8_STAGE(PG8_SA(0, 0), a2, vs[0]);
.LBB0_557:
	ds_read_b128 v[130:133], v199
	ds_read_b128 v[134:137], v200
	ds_read_b128 v[138:141], v201
	ds_read_b128 v[142:145], v202
	ds_read_b128 v[164:167], v203
	ds_read_b128 v[168:171], v204
	ds_read_b128 v[172:175], v205
	ds_read_b128 v[176:179], v206
	s_add_u32 s2, s0, 0x80
	s_addc_u32 s3, s1, 0
	s_cmp_eq_u32 s41, 12
	s_cselect_b32 s39, s7, s3
	s_cselect_b32 s38, s8, s2
	s_cselect_b32 s3, s25, s40
	s_cselect_b32 s2, s27, s37
	v_lshl_add_u64 v[192:193], s[0:1], 0, v[162:163]
	s_add_i32 m0, s50, 0xc000
	ds_read_b128 v[180:183], v207
	ds_read_b128 v[184:187], v207 offset:2048
	ds_read_b128 v[188:191], v208
	ds_read_b128 v[216:219], v208 offset:2048
	ds_read_b128 v[220:223], v207 offset:4096
	ds_read_b128 v[224:227], v207 offset:6144
	ds_read_b128 v[228:231], v208 offset:4096
	ds_read_b128 v[232:235], v208 offset:6144
	global_load_lds_dwordx4 v[192:193], off
	v_lshl_add_u64 v[192:193], s[0:1], 0, v[160:161]
	s_add_i32 m0, s50, 0xe000
	s_add_u32 s4, s2, 0x4000
	global_load_lds_dwordx4 v[192:193], off
	s_waitcnt vmcnt(8)
	s_waitcnt lgkmcnt(0)
	s_addc_u32 s5, s3, 0
	s_barrier
	s_setprio 1
	s_waitcnt lgkmcnt(0)
	v_mfma_f32_16x16x32_bf16 v[126:129], v[130:133], v[180:183], v[126:129]
	v_mfma_f32_16x16x32_bf16 v[58:61], v[138:141], v[180:183], v[58:61]
	v_mfma_f32_16x16x32_bf16 v[122:125], v[130:133], v[184:187], v[122:125]
	v_mfma_f32_16x16x32_bf16 v[118:121], v[138:141], v[184:187], v[118:121]
	v_mfma_f32_16x16x32_bf16 v[114:117], v[130:133], v[220:223], v[114:117]
	v_mfma_f32_16x16x32_bf16 v[110:113], v[138:141], v[220:223], v[110:113]
	v_mfma_f32_16x16x32_bf16 v[106:109], v[130:133], v[224:227], v[106:109]
	v_mfma_f32_16x16x32_bf16 v[102:105], v[138:141], v[224:227], v[102:105]
	v_mfma_f32_16x16x32_bf16 v[126:129], v[134:137], v[188:191], v[126:129]
	v_mfma_f32_16x16x32_bf16 v[58:61], v[142:145], v[188:191], v[58:61]
	v_mfma_f32_16x16x32_bf16 v[122:125], v[134:137], v[216:219], v[122:125]
	v_mfma_f32_16x16x32_bf16 v[118:121], v[142:145], v[216:219], v[118:121]
	v_mfma_f32_16x16x32_bf16 v[114:117], v[134:137], v[228:231], v[114:117]
	v_mfma_f32_16x16x32_bf16 v[110:113], v[142:145], v[228:231], v[110:113]
	v_mfma_f32_16x16x32_bf16 v[106:109], v[134:137], v[232:235], v[106:109]
	v_mfma_f32_16x16x32_bf16 v[102:105], v[142:145], v[232:235], v[102:105]
	v_mfma_f32_16x16x32_bf16 v[66:69], v[164:167], v[180:183], v[66:69]
	v_mfma_f32_16x16x32_bf16 v[50:53], v[172:175], v[180:183], v[50:53]
	v_mfma_f32_16x16x32_bf16 v[54:57], v[164:167], v[184:187], v[54:57]
	v_mfma_f32_16x16x32_bf16 v[42:45], v[172:175], v[184:187], v[42:45]
	v_mfma_f32_16x16x32_bf16 v[46:49], v[164:167], v[220:223], v[46:49]
	v_mfma_f32_16x16x32_bf16 v[34:37], v[172:175], v[220:223], v[34:37]
	v_mfma_f32_16x16x32_bf16 v[98:101], v[164:167], v[224:227], v[98:101]
	v_mfma_f32_16x16x32_bf16 v[38:41], v[172:175], v[224:227], v[38:41]
	v_mfma_f32_16x16x32_bf16 v[66:69], v[168:171], v[188:191], v[66:69]
	v_mfma_f32_16x16x32_bf16 v[50:53], v[176:179], v[188:191], v[50:53]
	v_mfma_f32_16x16x32_bf16 v[54:57], v[168:171], v[216:219], v[54:57]
	v_mfma_f32_16x16x32_bf16 v[42:45], v[176:179], v[216:219], v[42:45]
	v_mfma_f32_16x16x32_bf16 v[46:49], v[168:171], v[228:231], v[46:49]
	v_mfma_f32_16x16x32_bf16 v[34:37], v[176:179], v[228:231], v[34:37]
	v_mfma_f32_16x16x32_bf16 v[98:101], v[168:171], v[232:235], v[98:101]
	v_mfma_f32_16x16x32_bf16 v[38:41], v[176:179], v[232:235], v[38:41]
	s_setprio 0
	s_barrier
	s_setprio 3
	s_add_i32 s42, s63, s49
	v_lshl_add_u64 v[192:193], s[2:3], 0, v[146:147]
	s_mov_b32 m0, s42
	ds_read_b128 v[180:183], v207 offset:16384
	ds_read_b128 v[184:187], v207 offset:18432
	ds_read_b128 v[188:191], v208 offset:16384
	ds_read_b128 v[216:219], v208 offset:18432
	ds_read_b128 v[220:223], v207 offset:20480
	ds_read_b128 v[224:227], v207 offset:22528
	ds_read_b128 v[228:231], v208 offset:20480
	ds_read_b128 v[232:235], v208 offset:22528
	global_load_lds_dwordx4 v[192:193], off
	s_add_i32 m0, s42, 0x2000
	s_add_u32 s42, s2, 0x40000
	v_lshl_add_u64 v[192:193], s[2:3], 0, v[148:149]
	s_addc_u32 s43, s3, 0
	s_add_i32 s73, s64, s49
	global_load_lds_dwordx4 v[192:193], off
	v_lshl_add_u64 v[192:193], s[42:43], 0, v[146:147]
	s_mov_b32 m0, s73
	v_lshl_add_u64 v[236:237], s[38:39], 0, v[152:153]
	global_load_lds_dwordx4 v[192:193], off
	v_lshl_add_u64 v[192:193], s[42:43], 0, v[148:149]
	s_add_i32 m0, s73, 0x2000
	s_nop 0
	global_load_lds_dwordx4 v[192:193], off
	v_lshl_add_u64 v[192:193], s[38:39], 0, v[150:151]
	s_mov_b32 m0, s50
	s_nop 0
	global_load_lds_dwordx4 v[192:193], off
	s_mov_b32 m0, s51
	s_nop 0
	global_load_lds_dwordx4 v[236:237], off
	s_waitcnt vmcnt(8)
	s_waitcnt lgkmcnt(0)
	s_barrier
; #define PG8_STAGE(bufoff, gbase, voff) do { _Pragma("unroll") for (int _i = 0; _i < 2; ++_i) \
;         __builtin_amdgcn_global_load_lds((const unsigned*)((const char*)(gbase) + (voff)[_i]), (LAS unsigned*)(lds + (bufoff) + ldsw + _i * 8192), 16, 0, 0); } while (0)
; #define PG8_LDA(dst, b, h) do { _Pragma("unroll") for (int m = 0; m < 4; ++m) _Pragma("unroll") for (int k = 0; k < 2; ++k) dst[m][k] = *(const LAS bf16x8*)(lds + PG8_SA(b, h) + ((aoff ^ (k * 64)) + m * 2048)); } while (0)
; #define PG8_LDB(dst, b, h) do { _Pragma("unroll") for (int n = 0; n < 2; ++n) _Pragma("unroll") for (int k = 0; k < 2; ++k) dst[n][k] = *(const LAS bf16x8*)(lds + PG8_SB(b, h) + ((boff ^ (k * 64)) + n * 2048)); } while (0)
; #define PG8_MMA(ai, bj, At, Bt) do { __builtin_amdgcn_s_setprio(1); _Pragma("unroll") for (int m = 0; m < 4; ++m) _Pragma("unroll") for (int n = 0; n < 2; ++n) _Pragma("unroll") for (int k = 0; k < 2; ++k) \
;         acc[ai][bj][m][n] = __builtin_amdgcn_mfma_f32_16x16x32_bf16(Bt[n][k], At[m][k], acc[ai][bj][m][n], 0, 0, 0); __builtin_amdgcn_s_setprio(0); } while (0)
; #define PG8_WAIT_V(n) asm volatile("s_waitcnt vmcnt(" #n ")" ::: "memory")
; #define PG8_WAIT_L(n) asm volatile("s_waitcnt lgkmcnt(" #n ")" ::: "memory")
; #define PG8_BAR __builtin_amdgcn_s_barrier()
; #define PG8_SCHED __builtin_amdgcn_sched_barrier(0)
;     ...
;             PG8_WAIT_V(8); PG8_WAIT_L(0); PG8_BAR; if (do1) { PG8_MMA(1, 0, At, B0); PG8_MMA(1, 1, At, B1); } PG8_BAR; PG8_SCHED;
;             PG8_LDB(B0, 1, 0); PG8_LDB(B1, 1, 1); PG8_SCHED; PG8_LDA(At, 1, 0); PG8_STAGE(PG8_SA(0, 1), a2, vs[1]);
;             PG8_WAIT_V(8); PG8_WAIT_L(0); PG8_BAR; if (do0) { PG8_MMA(0, 0, At, B0); PG8_MMA(0, 1, At, B1); } PG8_BAR; PG8_SCHED;
	s_setprio 1
	s_waitcnt lgkmcnt(0)
	v_mfma_f32_16x16x32_bf16 v[94:97], v[130:133], v[180:183], v[94:97]
	v_mfma_f32_16x16x32_bf16 v[26:29], v[138:141], v[180:183], v[26:29]
	v_mfma_f32_16x16x32_bf16 v[90:93], v[130:133], v[184:187], v[90:93]
	v_mfma_f32_16x16x32_bf16 v[86:89], v[138:141], v[184:187], v[86:89]
	v_mfma_f32_16x16x32_bf16 v[82:85], v[130:133], v[220:223], v[82:85]
	v_mfma_f32_16x16x32_bf16 v[78:81], v[138:141], v[220:223], v[78:81]
	v_mfma_f32_16x16x32_bf16 v[74:77], v[130:133], v[224:227], v[74:77]
	v_mfma_f32_16x16x32_bf16 v[70:73], v[138:141], v[224:227], v[70:73]
	v_mfma_f32_16x16x32_bf16 v[94:97], v[134:137], v[188:191], v[94:97]
	v_mfma_f32_16x16x32_bf16 v[26:29], v[142:145], v[188:191], v[26:29]
	v_mfma_f32_16x16x32_bf16 v[90:93], v[134:137], v[216:219], v[90:93]
	v_mfma_f32_16x16x32_bf16 v[86:89], v[142:145], v[216:219], v[86:89]
	v_mfma_f32_16x16x32_bf16 v[82:85], v[134:137], v[228:231], v[82:85]
	v_mfma_f32_16x16x32_bf16 v[78:81], v[142:145], v[228:231], v[78:81]
	v_mfma_f32_16x16x32_bf16 v[74:77], v[134:137], v[232:235], v[74:77]
	v_mfma_f32_16x16x32_bf16 v[70:73], v[142:145], v[232:235], v[70:73]
	v_mfma_f32_16x16x32_bf16 v[30:33], v[164:167], v[180:183], v[30:33]
	v_mfma_f32_16x16x32_bf16 v[18:21], v[172:175], v[180:183], v[18:21]
	v_mfma_f32_16x16x32_bf16 v[22:25], v[164:167], v[184:187], v[22:25]
	v_mfma_f32_16x16x32_bf16 v[10:13], v[172:175], v[184:187], v[10:13]
	v_mfma_f32_16x16x32_bf16 v[14:17], v[164:167], v[220:223], v[14:17]
	v_mfma_f32_16x16x32_bf16 v[2:5], v[172:175], v[220:223], v[2:5]
	v_mfma_f32_16x16x32_bf16 v[62:65], v[164:167], v[224:227], v[62:65]
	v_mfma_f32_16x16x32_bf16 v[6:9], v[172:175], v[224:227], v[6:9]
	v_mfma_f32_16x16x32_bf16 v[30:33], v[168:171], v[188:191], v[30:33]
	v_mfma_f32_16x16x32_bf16 v[18:21], v[176:179], v[188:191], v[18:21]
	v_mfma_f32_16x16x32_bf16 v[22:25], v[168:171], v[216:219], v[22:25]
	v_mfma_f32_16x16x32_bf16 v[10:13], v[176:179], v[216:219], v[10:13]
	v_mfma_f32_16x16x32_bf16 v[14:17], v[168:171], v[228:231], v[14:17]
	v_mfma_f32_16x16x32_bf16 v[2:5], v[176:179], v[228:231], v[2:5]
	v_mfma_f32_16x16x32_bf16 v[62:65], v[168:171], v[232:235], v[62:65]
	v_mfma_f32_16x16x32_bf16 v[6:9], v[176:179], v[232:235], v[6:9]
	s_setprio 0
	s_barrier
	s_setprio 3
	s_add_i32 s42, 0, 0x18000
	s_add_i32 s43, 0, 0x1c000
	v_add_u32_e32 v130, s42, v196
	v_add_u32_e32 v134, s42, v197
	v_add_u32_e32 v158, s43, v196
	v_add_u32_e32 v168, s43, v197
	ds_read_b128 v[130:133], v130
	ds_read_b128 v[134:137], v134
	ds_read_b128 v[138:141], v209
	ds_read_b128 v[142:145], v210
	ds_read_b128 v[164:167], v158
	ds_read_b128 v[168:171], v168
	ds_read_b128 v[172:175], v211
	ds_read_b128 v[176:179], v212
	s_mov_b32 m0, s52
	v_lshl_add_u64 v[238:239], s[38:39], 0, v[154:155]
	ds_read_b128 v[180:183], v207 offset:32768
	ds_read_b128 v[184:187], v207 offset:34816
	ds_read_b128 v[188:191], v208 offset:32768
	ds_read_b128 v[216:219], v208 offset:34816
	ds_read_b128 v[220:223], v207 offset:36864
	ds_read_b128 v[224:227], v207 offset:38912
	ds_read_b128 v[228:231], v208 offset:36864
	ds_read_b128 v[232:235], v208 offset:38912
	global_load_lds_dwordx4 v[238:239], off
	v_lshl_add_u64 v[238:239], s[38:39], 0, v[156:157]
	s_mov_b32 m0, s53
	s_nop 0
	global_load_lds_dwordx4 v[238:239], off
	s_waitcnt vmcnt(8)
	s_waitcnt lgkmcnt(0)
	s_barrier
	s_setprio 1
	s_waitcnt lgkmcnt(0)
	v_mfma_f32_16x16x32_bf16 v[126:129], v[130:133], v[180:183], v[126:129]
	v_mfma_f32_16x16x32_bf16 v[58:61], v[138:141], v[180:183], v[58:61]
	v_mfma_f32_16x16x32_bf16 v[122:125], v[130:133], v[184:187], v[122:125]
	v_mfma_f32_16x16x32_bf16 v[118:121], v[138:141], v[184:187], v[118:121]
	v_mfma_f32_16x16x32_bf16 v[114:117], v[130:133], v[220:223], v[114:117]
	v_mfma_f32_16x16x32_bf16 v[110:113], v[138:141], v[220:223], v[110:113]
	v_mfma_f32_16x16x32_bf16 v[106:109], v[130:133], v[224:227], v[106:109]
	v_mfma_f32_16x16x32_bf16 v[102:105], v[138:141], v[224:227], v[102:105]
	v_mfma_f32_16x16x32_bf16 v[126:129], v[134:137], v[188:191], v[126:129]
	v_mfma_f32_16x16x32_bf16 v[58:61], v[142:145], v[188:191], v[58:61]
	v_mfma_f32_16x16x32_bf16 v[122:125], v[134:137], v[216:219], v[122:125]
	v_mfma_f32_16x16x32_bf16 v[118:121], v[142:145], v[216:219], v[118:121]
	v_mfma_f32_16x16x32_bf16 v[114:117], v[134:137], v[228:231], v[114:117]
	v_mfma_f32_16x16x32_bf16 v[110:113], v[142:145], v[228:231], v[110:113]
	v_mfma_f32_16x16x32_bf16 v[106:109], v[134:137], v[232:235], v[106:109]
	v_mfma_f32_16x16x32_bf16 v[102:105], v[142:145], v[232:235], v[102:105]
	v_mfma_f32_16x16x32_bf16 v[66:69], v[164:167], v[180:183], v[66:69]
	v_mfma_f32_16x16x32_bf16 v[50:53], v[172:175], v[180:183], v[50:53]
	v_mfma_f32_16x16x32_bf16 v[54:57], v[164:167], v[184:187], v[54:57]
	v_mfma_f32_16x16x32_bf16 v[42:45], v[172:175], v[184:187], v[42:45]
	v_mfma_f32_16x16x32_bf16 v[46:49], v[164:167], v[220:223], v[46:49]
	v_mfma_f32_16x16x32_bf16 v[34:37], v[172:175], v[220:223], v[34:37]
	v_mfma_f32_16x16x32_bf16 v[98:101], v[164:167], v[224:227], v[98:101]
	v_mfma_f32_16x16x32_bf16 v[38:41], v[172:175], v[224:227], v[38:41]
	v_mfma_f32_16x16x32_bf16 v[66:69], v[168:171], v[188:191], v[66:69]
	v_mfma_f32_16x16x32_bf16 v[50:53], v[176:179], v[188:191], v[50:53]
	v_mfma_f32_16x16x32_bf16 v[54:57], v[168:171], v[216:219], v[54:57]
	v_mfma_f32_16x16x32_bf16 v[42:45], v[176:179], v[216:219], v[42:45]
	v_mfma_f32_16x16x32_bf16 v[46:49], v[168:171], v[228:231], v[46:49]
	v_mfma_f32_16x16x32_bf16 v[34:37], v[176:179], v[228:231], v[34:37]
	v_mfma_f32_16x16x32_bf16 v[98:101], v[168:171], v[232:235], v[98:101]
	v_mfma_f32_16x16x32_bf16 v[38:41], v[176:179], v[232:235], v[38:41]
	s_setprio 0
	s_barrier
; #define PG8_STAGE(bufoff, gbase, voff) do { _Pragma("unroll") for (int _i = 0; _i < 2; ++_i) \
;         __builtin_amdgcn_global_load_lds((const unsigned*)((const char*)(gbase) + (voff)[_i]), (LAS unsigned*)(lds + (bufoff) + ldsw + _i * 8192), 16, 0, 0); } while (0)
; #define PG8_LDA(dst, b, h) do { _Pragma("unroll") for (int m = 0; m < 4; ++m) _Pragma("unroll") for (int k = 0; k < 2; ++k) dst[m][k] = *(const LAS bf16x8*)(lds + PG8_SA(b, h) + ((aoff ^ (k * 64)) + m * 2048)); } while (0)
; #define PG8_MMA(ai, bj, At, Bt) do { __builtin_amdgcn_s_setprio(1); _Pragma("unroll") for (int m = 0; m < 4; ++m) _Pragma("unroll") for (int n = 0; n < 2; ++n) _Pragma("unroll") for (int k = 0; k < 2; ++k) \
;         acc[ai][bj][m][n] = __builtin_amdgcn_mfma_f32_16x16x32_bf16(Bt[n][k], At[m][k], acc[ai][bj][m][n], 0, 0, 0); __builtin_amdgcn_s_setprio(0); } while (0)
; #define PG8_WAIT_V(n) asm volatile("s_waitcnt vmcnt(" #n ")" ::: "memory")
; #define PG8_WAIT_L(n) asm volatile("s_waitcnt lgkmcnt(" #n ")" ::: "memory")
; #define PG8_BAR __builtin_amdgcn_s_barrier()
; #define PG8_SCHED __builtin_amdgcn_sched_barrier(0)
;     ...
;             PG8_LDA(At, 1, 1); PG8_STAGE(PG8_SB(1, 0), b3, voffB); PG8_STAGE(PG8_SB(1, 1), b3 + hstep, voffB); PG8_STAGE(PG8_SA(1, 0), a3, vs[0]);
;             PG8_WAIT_V(8); PG8_WAIT_L(0); PG8_BAR; if (do1) { PG8_MMA(1, 0, At, B0); PG8_MMA(1, 1, At, B1); } PG8_BAR; PG8_SCHED;
;         }
;         if (wr == 0) PG8_BAR;
	s_setprio 3
	s_add_i32 s38, s42, s49
	v_lshl_add_u64 v[238:239], s[4:5], 0, v[146:147]
	s_mov_b32 m0, s38
	ds_read_b128 v[180:183], v207 offset:49152
	ds_read_b128 v[184:187], v207 offset:51200
	ds_read_b128 v[188:191], v208 offset:49152
	ds_read_b128 v[216:219], v208 offset:51200
	ds_read_b128 v[220:223], v207 offset:53248
	ds_read_b128 v[224:227], v207 offset:55296
	ds_read_b128 v[228:231], v208 offset:53248
	ds_read_b128 v[232:235], v208 offset:55296
	global_load_lds_dwordx4 v[238:239], off
	s_add_i32 m0, s38, 0x2000
	s_add_u32 s2, s2, 0x44000
	v_lshl_add_u64 v[238:239], s[4:5], 0, v[148:149]
	s_addc_u32 s3, s3, 0
	s_add_i32 s4, s43, s49
	global_load_lds_dwordx4 v[238:239], off
	v_lshl_add_u64 v[238:239], s[2:3], 0, v[146:147]
	s_mov_b32 m0, s4
	v_lshl_add_u64 v[192:193], v[192:193], 0, s[92:93]
	global_load_lds_dwordx4 v[238:239], off
	v_lshl_add_u64 v[238:239], s[2:3], 0, v[148:149]
	s_add_i32 m0, s4, 0x2000
	s_nop 0
	global_load_lds_dwordx4 v[238:239], off
	s_mov_b32 m0, s55
	s_nop 0
	global_load_lds_dwordx4 v[192:193], off
	v_lshl_add_u64 v[192:193], v[236:237], 0, s[92:93]
	s_mov_b32 m0, s56
	s_nop 0
	global_load_lds_dwordx4 v[192:193], off
	s_waitcnt vmcnt(8)
	s_waitcnt lgkmcnt(0)
	s_barrier
	s_setprio 1
	s_waitcnt lgkmcnt(0)
	v_mfma_f32_16x16x32_bf16 v[94:97], v[130:133], v[180:183], v[94:97]
	v_mfma_f32_16x16x32_bf16 v[26:29], v[138:141], v[180:183], v[26:29]
	v_mfma_f32_16x16x32_bf16 v[90:93], v[130:133], v[184:187], v[90:93]
	v_mfma_f32_16x16x32_bf16 v[86:89], v[138:141], v[184:187], v[86:89]
	v_mfma_f32_16x16x32_bf16 v[82:85], v[130:133], v[220:223], v[82:85]
	v_mfma_f32_16x16x32_bf16 v[78:81], v[138:141], v[220:223], v[78:81]
	v_mfma_f32_16x16x32_bf16 v[74:77], v[130:133], v[224:227], v[74:77]
	v_mfma_f32_16x16x32_bf16 v[70:73], v[138:141], v[224:227], v[70:73]
	v_mfma_f32_16x16x32_bf16 v[94:97], v[134:137], v[188:191], v[94:97]
	v_mfma_f32_16x16x32_bf16 v[26:29], v[142:145], v[188:191], v[26:29]
	v_mfma_f32_16x16x32_bf16 v[90:93], v[134:137], v[216:219], v[90:93]
	v_mfma_f32_16x16x32_bf16 v[86:89], v[142:145], v[216:219], v[86:89]
	v_mfma_f32_16x16x32_bf16 v[82:85], v[134:137], v[228:231], v[82:85]
	v_mfma_f32_16x16x32_bf16 v[78:81], v[142:145], v[228:231], v[78:81]
	v_mfma_f32_16x16x32_bf16 v[74:77], v[134:137], v[232:235], v[74:77]
	v_mfma_f32_16x16x32_bf16 v[70:73], v[142:145], v[232:235], v[70:73]
	v_mfma_f32_16x16x32_bf16 v[30:33], v[164:167], v[180:183], v[30:33]
	v_mfma_f32_16x16x32_bf16 v[18:21], v[172:175], v[180:183], v[18:21]
	v_mfma_f32_16x16x32_bf16 v[22:25], v[164:167], v[184:187], v[22:25]
	v_mfma_f32_16x16x32_bf16 v[10:13], v[172:175], v[184:187], v[10:13]
	v_mfma_f32_16x16x32_bf16 v[14:17], v[164:167], v[220:223], v[14:17]
	v_mfma_f32_16x16x32_bf16 v[2:5], v[172:175], v[220:223], v[2:5]
	v_mfma_f32_16x16x32_bf16 v[62:65], v[164:167], v[224:227], v[62:65]
	v_mfma_f32_16x16x32_bf16 v[6:9], v[172:175], v[224:227], v[6:9]
	v_mfma_f32_16x16x32_bf16 v[30:33], v[168:171], v[188:191], v[30:33]
	v_mfma_f32_16x16x32_bf16 v[18:21], v[176:179], v[188:191], v[18:21]
	v_mfma_f32_16x16x32_bf16 v[22:25], v[168:171], v[216:219], v[22:25]
	v_mfma_f32_16x16x32_bf16 v[10:13], v[176:179], v[216:219], v[10:13]
	v_mfma_f32_16x16x32_bf16 v[14:17], v[168:171], v[228:231], v[14:17]
	v_mfma_f32_16x16x32_bf16 v[2:5], v[176:179], v[228:231], v[2:5]
	v_mfma_f32_16x16x32_bf16 v[62:65], v[168:171], v[232:235], v[62:65]
	v_mfma_f32_16x16x32_bf16 v[6:9], v[176:179], v[232:235], v[6:9]
	s_setprio 0
	s_barrier
	s_setprio 3
	s_add_i32 s41, s41, 2
	s_add_u32 s37, s37, 0x8000
	s_addc_u32 s40, s40, 0
	s_add_u32 s0, s0, 0x100
	s_addc_u32 s1, s1, 0
	s_cmp_gt_u32 s41, 13
	s_cbranch_scc0 .LBB0_557
	s_and_b64 vcc, exec, s[80:81]
	s_cbranch_vccz .LBB0_560
	s_barrier

; #define PG8_STAGE(bufoff, gbase, voff) do { _Pragma("unroll") for (int _i = 0; _i < 2; ++_i) \
;         __builtin_amdgcn_global_load_lds((const unsigned*)((const char*)(gbase) + (voff)[_i]), (LAS unsigned*)(lds + (bufoff) + ldsw + _i * 8192), 16, 0, 0); } while (0)
; #define PG8_LDA(dst, b, h) do { _Pragma("unroll") for (int m = 0; m < 4; ++m) _Pragma("unroll") for (int k = 0; k < 2; ++k) dst[m][k] = *(const LAS bf16x8*)(lds + PG8_SA(b, h) + ((aoff ^ (k * 64)) + m * 2048)); } while (0)
; #define PG8_LDB(dst, b, h) do { _Pragma("unroll") for (int n = 0; n < 2; ++n) _Pragma("unroll") for (int k = 0; k < 2; ++k) dst[n][k] = *(const LAS bf16x8*)(lds + PG8_SB(b, h) + ((boff ^ (k * 64)) + n * 2048)); } while (0)
; #define PG8_MMA(ai, bj, At, Bt) do { __builtin_amdgcn_s_setprio(1); _Pragma("unroll") for (int m = 0; m < 4; ++m) _Pragma("unroll") for (int n = 0; n < 2; ++n) _Pragma("unroll") for (int k = 0; k < 2; ++k) \
;         acc[ai][bj][m][n] = __builtin_amdgcn_mfma_f32_16x16x32_bf16(Bt[n][k], At[m][k], acc[ai][bj][m][n], 0, 0, 0); __builtin_amdgcn_s_setprio(0); } while (0)
; #define PG8_WAIT_V(n) asm volatile("s_waitcnt vmcnt(" #n ")" ::: "memory")
; #define PG8_WAIT_L(n) asm volatile("s_waitcnt lgkmcnt(" #n ")" ::: "memory")
; #define PG8_BAR __builtin_amdgcn_s_barrier()
; #define PG8_SCHED __builtin_amdgcn_sched_barrier(0)
;     ...
;             PG8_LDB(B0, 1, 0); PG8_LDB(B1, 1, 1); PG8_SCHED; PG8_LDA(At, 1, 0); PG8_STAGE(PG8_SA(0, 1), a2, vs[1]);
;             PG8_WAIT_V(8); PG8_WAIT_L(0); PG8_BAR; if (do0) { PG8_MMA(0, 0, At, B0); PG8_MMA(0, 1, At, B1); } PG8_BAR; PG8_SCHED;
.LBB0_1012:
	v_cndmask_b32_e64 v213, v214, v215, s[6:7]
	v_cndmask_b32_e64 v225, v216, v217, s[6:7]
	s_barrier
	s_setprio 3
	s_add_i32 s6, 0, 0x18000
	v_add_u32_e32 v134, s6, v226
	v_add_u32_e32 v135, s6, v227
	ds_read_b128 v[150:153], v134
	ds_read_b128 v[154:157], v135
	v_add_u32_e32 v134, s58, v226
	s_add_i32 s6, 0, 0x1c000
	v_add_u32_e32 v135, s58, v227
	ds_read_b128 v[158:161], v134
	ds_read_b128 v[162:165], v135
	v_add_u32_e32 v134, s6, v226
	v_add_u32_e32 v138, s6, v227
	v_add_u32_e32 v142, s59, v226
	v_add_u32_e32 v146, s59, v227
	ds_read_b128 v[134:137], v134
	ds_read_b128 v[138:141], v138
	ds_read_b128 v[142:145], v142
	ds_read_b128 v[146:149], v146
	s_mov_b32 m0, s42
	s_waitcnt lgkmcnt(0)
	ds_read_b128 v[190:193], v228 offset:32768
	ds_read_b128 v[178:181], v228 offset:34816
	ds_read_b128 v[194:197], v229 offset:32768
	ds_read_b128 v[182:185], v229 offset:34816
	ds_read_b128 v[174:177], v228 offset:36864
	ds_read_b128 v[166:169], v228 offset:38912
	ds_read_b128 v[186:189], v229 offset:36864
	ds_read_b128 v[170:173], v229 offset:38912
	global_load_lds_dwordx4 v213, s[34:35]
	s_mov_b32 m0, s43
	s_and_b64 vcc, exec, s[8:9]
	global_load_lds_dwordx4 v225, s[34:35]
	s_waitcnt vmcnt(8)
	s_waitcnt lgkmcnt(0)
	s_barrier
	s_cbranch_vccnz .LBB0_1014
	s_setprio 1
	s_waitcnt lgkmcnt(0)
	v_mfma_f32_16x16x32_bf16 v[130:133], v[150:153], v[190:193], v[130:133]
	v_mfma_f32_16x16x32_bf16 v[126:129], v[158:161], v[190:193], v[126:129]
	v_mfma_f32_16x16x32_bf16 v[114:117], v[150:153], v[178:181], v[114:117]
	v_mfma_f32_16x16x32_bf16 v[110:113], v[158:161], v[178:181], v[110:113]
	v_mfma_f32_16x16x32_bf16 v[98:101], v[150:153], v[174:177], v[98:101]
	v_mfma_f32_16x16x32_bf16 v[94:97], v[158:161], v[174:177], v[94:97]
	v_mfma_f32_16x16x32_bf16 v[82:85], v[150:153], v[166:169], v[82:85]
	v_mfma_f32_16x16x32_bf16 v[78:81], v[158:161], v[166:169], v[78:81]
	v_mfma_f32_16x16x32_bf16 v[130:133], v[154:157], v[194:197], v[130:133]
	v_mfma_f32_16x16x32_bf16 v[126:129], v[162:165], v[194:197], v[126:129]
	v_mfma_f32_16x16x32_bf16 v[114:117], v[154:157], v[182:185], v[114:117]
	v_mfma_f32_16x16x32_bf16 v[110:113], v[162:165], v[182:185], v[110:113]
	v_mfma_f32_16x16x32_bf16 v[98:101], v[154:157], v[186:189], v[98:101]
	v_mfma_f32_16x16x32_bf16 v[94:97], v[162:165], v[186:189], v[94:97]
	v_mfma_f32_16x16x32_bf16 v[82:85], v[154:157], v[170:173], v[82:85]
	v_mfma_f32_16x16x32_bf16 v[78:81], v[162:165], v[170:173], v[78:81]
	v_mfma_f32_16x16x32_bf16 v[122:125], v[134:137], v[190:193], v[122:125]
	v_mfma_f32_16x16x32_bf16 v[118:121], v[142:145], v[190:193], v[118:121]
	v_mfma_f32_16x16x32_bf16 v[106:109], v[134:137], v[178:181], v[106:109]
	v_mfma_f32_16x16x32_bf16 v[102:105], v[142:145], v[178:181], v[102:105]
	v_mfma_f32_16x16x32_bf16 v[90:93], v[134:137], v[174:177], v[90:93]
	v_mfma_f32_16x16x32_bf16 v[86:89], v[142:145], v[174:177], v[86:89]
	v_mfma_f32_16x16x32_bf16 v[74:77], v[134:137], v[166:169], v[74:77]
	v_mfma_f32_16x16x32_bf16 v[70:73], v[142:145], v[166:169], v[70:73]
	v_mfma_f32_16x16x32_bf16 v[122:125], v[138:141], v[194:197], v[122:125]
	v_mfma_f32_16x16x32_bf16 v[118:121], v[146:149], v[194:197], v[118:121]
	v_mfma_f32_16x16x32_bf16 v[106:109], v[138:141], v[182:185], v[106:109]
	v_mfma_f32_16x16x32_bf16 v[102:105], v[146:149], v[182:185], v[102:105]
	v_mfma_f32_16x16x32_bf16 v[90:93], v[138:141], v[186:189], v[90:93]
	v_mfma_f32_16x16x32_bf16 v[86:89], v[146:149], v[186:189], v[86:89]
	v_mfma_f32_16x16x32_bf16 v[74:77], v[138:141], v[170:173], v[74:77]
	v_mfma_f32_16x16x32_bf16 v[70:73], v[146:149], v[170:173], v[70:73]
	s_setprio 0
; #define PG8_STAGE(bufoff, gbase, voff) do { _Pragma("unroll") for (int _i = 0; _i < 2; ++_i) \
;         __builtin_amdgcn_global_load_lds((const unsigned*)((const char*)(gbase) + (voff)[_i]), (LAS unsigned*)(lds + (bufoff) + ldsw + _i * 8192), 16, 0, 0); } while (0)
; #define PG8_LDA(dst, b, h) do { _Pragma("unroll") for (int m = 0; m < 4; ++m) _Pragma("unroll") for (int k = 0; k < 2; ++k) dst[m][k] = *(const LAS bf16x8*)(lds + PG8_SA(b, h) + ((aoff ^ (k * 64)) + m * 2048)); } while (0)
; #define PG8_MMA(ai, bj, At, Bt) do { __builtin_amdgcn_s_setprio(1); _Pragma("unroll") for (int m = 0; m < 4; ++m) _Pragma("unroll") for (int n = 0; n < 2; ++n) _Pragma("unroll") for (int k = 0; k < 2; ++k) \
;         acc[ai][bj][m][n] = __builtin_amdgcn_mfma_f32_16x16x32_bf16(Bt[n][k], At[m][k], acc[ai][bj][m][n], 0, 0, 0); __builtin_amdgcn_s_setprio(0); } while (0)
; #define PG8_WAIT_V(n) asm volatile("s_waitcnt vmcnt(" #n ")" ::: "memory")
; #define PG8_WAIT_L(n) asm volatile("s_waitcnt lgkmcnt(" #n ")" ::: "memory")
; #define PG8_BAR __builtin_amdgcn_s_barrier()
; #define PG8_SCHED __builtin_amdgcn_sched_barrier(0)
;     ...
;             PG8_LDA(At, 1, 1); PG8_STAGE(PG8_SB(1, 0), b3, voffB); PG8_STAGE(PG8_SB(1, 1), b3 + hstep, voffB); PG8_STAGE(PG8_SA(1, 0), a3, vs[0]);
;             PG8_WAIT_V(8); PG8_WAIT_L(0); PG8_BAR; if (do1) { PG8_MMA(1, 0, At, B0); PG8_MMA(1, 1, At, B1); } PG8_BAR; PG8_SCHED;
;         }
;     ...
;         if (wr == 1) PG8_BAR;
.LBB0_1014:
	v_mov_b32_e32 v225, v3
	s_add_u32 s6, s30, 0x4000
	v_lshl_add_u64 v[232:233], s[34:35], 0, v[2:3]
	v_lshl_add_u64 v[224:225], s[34:35], 0, v[224:225]
	s_addc_u32 s7, s31, 0
	s_barrier
	s_setprio 3
	s_mov_b32 m0, s47
	v_lshl_add_u64 v[234:235], s[6:7], 0, v[202:203]
	s_waitcnt lgkmcnt(0)
	ds_read_b128 v[190:193], v228 offset:49152
	ds_read_b128 v[178:181], v228 offset:51200
	ds_read_b128 v[194:197], v229 offset:49152
	ds_read_b128 v[182:185], v229 offset:51200
	ds_read_b128 v[174:177], v228 offset:53248
	ds_read_b128 v[166:169], v228 offset:55296
	ds_read_b128 v[186:189], v229 offset:53248
	ds_read_b128 v[170:173], v229 offset:55296
	global_load_lds_dwordx4 v[234:235], off
	v_lshl_add_u64 v[234:235], s[6:7], 0, v[204:205]
	s_add_u32 s6, s30, 0x44000
	s_mov_b32 m0, s48
	s_addc_u32 s7, s31, 0
	global_load_lds_dwordx4 v[234:235], off
	v_lshl_add_u64 v[234:235], s[6:7], 0, v[202:203]
	s_mov_b32 m0, s51
	v_lshl_add_u64 v[232:233], v[232:233], 0, s[16:17]
	global_load_lds_dwordx4 v[234:235], off
	v_lshl_add_u64 v[234:235], s[6:7], 0, v[204:205]
	s_mov_b32 m0, s52
	v_lshl_add_u64 v[224:225], v[224:225], 0, s[16:17]
	global_load_lds_dwordx4 v[234:235], off
	s_mov_b32 m0, s49
	s_and_b64 vcc, exec, s[10:11]
	global_load_lds_dwordx4 v[232:233], off
	s_mov_b32 m0, s50
	s_nop 0
	global_load_lds_dwordx4 v[224:225], off
	s_waitcnt vmcnt(8)
	s_waitcnt lgkmcnt(0)
	s_barrier
	s_cbranch_vccnz .LBB0_1005
	s_setprio 1
	s_waitcnt lgkmcnt(0)
	v_mfma_f32_16x16x32_bf16 v[66:69], v[150:153], v[190:193], v[66:69]
	v_mfma_f32_16x16x32_bf16 v[62:65], v[158:161], v[190:193], v[62:65]
	v_mfma_f32_16x16x32_bf16 v[50:53], v[150:153], v[178:181], v[50:53]
	v_mfma_f32_16x16x32_bf16 v[46:49], v[158:161], v[178:181], v[46:49]
	v_mfma_f32_16x16x32_bf16 v[34:37], v[150:153], v[174:177], v[34:37]
	v_mfma_f32_16x16x32_bf16 v[30:33], v[158:161], v[174:177], v[30:33]
	v_mfma_f32_16x16x32_bf16 v[18:21], v[150:153], v[166:169], v[18:21]
	v_mfma_f32_16x16x32_bf16 v[14:17], v[158:161], v[166:169], v[14:17]
	v_mfma_f32_16x16x32_bf16 v[66:69], v[154:157], v[194:197], v[66:69]
	v_mfma_f32_16x16x32_bf16 v[62:65], v[162:165], v[194:197], v[62:65]
	v_mfma_f32_16x16x32_bf16 v[50:53], v[154:157], v[182:185], v[50:53]
	v_mfma_f32_16x16x32_bf16 v[46:49], v[162:165], v[182:185], v[46:49]
	v_mfma_f32_16x16x32_bf16 v[34:37], v[154:157], v[186:189], v[34:37]
	v_mfma_f32_16x16x32_bf16 v[30:33], v[162:165], v[186:189], v[30:33]
	v_mfma_f32_16x16x32_bf16 v[18:21], v[154:157], v[170:173], v[18:21]
	v_mfma_f32_16x16x32_bf16 v[14:17], v[162:165], v[170:173], v[14:17]
	v_mfma_f32_16x16x32_bf16 v[58:61], v[134:137], v[190:193], v[58:61]
	v_mfma_f32_16x16x32_bf16 v[54:57], v[142:145], v[190:193], v[54:57]
	v_mfma_f32_16x16x32_bf16 v[42:45], v[134:137], v[178:181], v[42:45]
	v_mfma_f32_16x16x32_bf16 v[38:41], v[142:145], v[178:181], v[38:41]
	v_mfma_f32_16x16x32_bf16 v[26:29], v[134:137], v[174:177], v[26:29]
	v_mfma_f32_16x16x32_bf16 v[22:25], v[142:145], v[174:177], v[22:25]
	v_mfma_f32_16x16x32_bf16 v[10:13], v[134:137], v[166:169], v[10:13]
	v_mfma_f32_16x16x32_bf16 v[6:9], v[142:145], v[166:169], v[6:9]
	v_mfma_f32_16x16x32_bf16 v[58:61], v[138:141], v[194:197], v[58:61]
	v_mfma_f32_16x16x32_bf16 v[54:57], v[146:149], v[194:197], v[54:57]
	v_mfma_f32_16x16x32_bf16 v[42:45], v[138:141], v[182:185], v[42:45]
	v_mfma_f32_16x16x32_bf16 v[38:41], v[146:149], v[182:185], v[38:41]
	v_mfma_f32_16x16x32_bf16 v[26:29], v[138:141], v[186:189], v[26:29]
	v_mfma_f32_16x16x32_bf16 v[22:25], v[146:149], v[186:189], v[22:25]
	v_mfma_f32_16x16x32_bf16 v[10:13], v[138:141], v[170:173], v[10:13]
	v_mfma_f32_16x16x32_bf16 v[6:9], v[146:149], v[170:173], v[6:9]
	s_setprio 0
	s_branch .LBB0_1005
.LBB0_1016:
	s_and_b64 vcc, exec, s[14:15]
	s_cbranch_vccz .LBB0_1018
	s_barrier
	s_setprio 3

; #define PG8_STAGE(bufoff, gbase, voff) do { _Pragma("unroll") for (int _i = 0; _i < 2; ++_i) \
;         __builtin_amdgcn_global_load_lds((const unsigned*)((const char*)(gbase) + (voff)[_i]), (LAS unsigned*)(lds + (bufoff) + ldsw + _i * 8192), 16, 0, 0); } while (0)
; #define PG8_LDA(dst, b, h) do { _Pragma("unroll") for (int m = 0; m < 4; ++m) _Pragma("unroll") for (int k = 0; k < 2; ++k) dst[m][k] = *(const LAS bf16x8*)(lds + PG8_SA(b, h) + ((aoff ^ (k * 64)) + m * 2048)); } while (0)
; #define PG8_LDB(dst, b, h) do { _Pragma("unroll") for (int n = 0; n < 2; ++n) _Pragma("unroll") for (int k = 0; k < 2; ++k) dst[n][k] = *(const LAS bf16x8*)(lds + PG8_SB(b, h) + ((boff ^ (k * 64)) + n * 2048)); } while (0)
; #define PG8_MMA(ai, bj, At, Bt) do { __builtin_amdgcn_s_setprio(1); _Pragma("unroll") for (int m = 0; m < 4; ++m) _Pragma("unroll") for (int n = 0; n < 2; ++n) _Pragma("unroll") for (int k = 0; k < 2; ++k) \
;         acc[ai][bj][m][n] = __builtin_amdgcn_mfma_f32_16x16x32_bf16(Bt[n][k], At[m][k], acc[ai][bj][m][n], 0, 0, 0); __builtin_amdgcn_s_setprio(0); } while (0)
; #define PG8_WAIT_V(n) asm volatile("s_waitcnt vmcnt(" #n ")" ::: "memory")
; #define PG8_WAIT_L(n) asm volatile("s_waitcnt lgkmcnt(" #n ")" ::: "memory")
; #define PG8_BAR __builtin_amdgcn_s_barrier()
; #define PG8_SCHED __builtin_amdgcn_sched_barrier(0)
;     ...
;             PG8_LDB(B0, 1, 0); PG8_LDB(B1, 1, 1); PG8_SCHED; PG8_LDA(At, 1, 0); PG8_STAGE(PG8_SA(0, 1), a2, vs[1]);
;             PG8_WAIT_V(8); PG8_WAIT_L(0); PG8_BAR; if (do0) { PG8_MMA(0, 0, At, B0); PG8_MMA(0, 1, At, B1); } PG8_BAR; PG8_SCHED;
.LBB0_1104:
	s_barrier
	s_setprio 3
	s_add_i32 s64, 0, 0x18000
	v_add_u32_e32 v3, s64, v199
	v_add_u32_e32 v4, s64, v216
	ds_read_b128 v[150:153], v3
	ds_read_b128 v[154:157], v4
	v_add_u32_e32 v3, s48, v199
	s_add_i32 s64, 0, 0x1c000
	v_add_u32_e32 v4, s48, v216
	ds_read_b128 v[158:161], v3
	ds_read_b128 v[162:165], v4
	v_add_u32_e32 v3, s64, v199
	v_add_u32_e32 v4, s64, v216
	ds_read_b128 v[134:137], v3
	ds_read_b128 v[138:141], v4
	v_add_u32_e32 v3, s49, v199
	v_add_u32_e32 v4, s49, v216
	ds_read_b128 v[142:145], v3
	ds_read_b128 v[146:149], v4
	s_mov_b32 m0, s36
	v_lshl_add_u64 v[4:5], s[26:27], 0, v[204:205]
	s_waitcnt lgkmcnt(0)
	ds_read_b128 v[190:193], v226 offset:32768
	ds_read_b128 v[178:181], v226 offset:34816
	ds_read_b128 v[194:197], v227 offset:32768
	ds_read_b128 v[182:185], v227 offset:34816
	ds_read_b128 v[174:177], v226 offset:36864
	ds_read_b128 v[166:169], v226 offset:38912
	ds_read_b128 v[186:189], v227 offset:36864
	ds_read_b128 v[170:173], v227 offset:38912
	global_load_lds_dwordx4 v[4:5], off
	v_lshl_add_u64 v[4:5], s[26:27], 0, v[206:207]
	s_mov_b32 m0, s37
	s_and_b64 vcc, exec, s[6:7]
	global_load_lds_dwordx4 v[4:5], off
	s_waitcnt vmcnt(8)
	s_waitcnt lgkmcnt(0)
	s_barrier
	s_cbranch_vccnz .LBB0_1106
	s_setprio 1
	s_waitcnt lgkmcnt(0)
	v_mfma_f32_16x16x32_bf16 v[66:69], v[150:153], v[190:193], v[66:69]
	v_mfma_f32_16x16x32_bf16 v[62:65], v[158:161], v[190:193], v[62:65]
	v_mfma_f32_16x16x32_bf16 v[50:53], v[150:153], v[178:181], v[50:53]
	v_mfma_f32_16x16x32_bf16 v[46:49], v[158:161], v[178:181], v[46:49]
	v_mfma_f32_16x16x32_bf16 v[34:37], v[150:153], v[174:177], v[34:37]
	v_mfma_f32_16x16x32_bf16 v[30:33], v[158:161], v[174:177], v[30:33]
	v_mfma_f32_16x16x32_bf16 v[18:21], v[150:153], v[166:169], v[18:21]
	v_mfma_f32_16x16x32_bf16 v[14:17], v[158:161], v[166:169], v[14:17]
	v_mfma_f32_16x16x32_bf16 v[66:69], v[154:157], v[194:197], v[66:69]
	v_mfma_f32_16x16x32_bf16 v[62:65], v[162:165], v[194:197], v[62:65]
	v_mfma_f32_16x16x32_bf16 v[50:53], v[154:157], v[182:185], v[50:53]
	v_mfma_f32_16x16x32_bf16 v[46:49], v[162:165], v[182:185], v[46:49]
	v_mfma_f32_16x16x32_bf16 v[34:37], v[154:157], v[186:189], v[34:37]
	v_mfma_f32_16x16x32_bf16 v[30:33], v[162:165], v[186:189], v[30:33]
	v_mfma_f32_16x16x32_bf16 v[18:21], v[154:157], v[170:173], v[18:21]
	v_mfma_f32_16x16x32_bf16 v[14:17], v[162:165], v[170:173], v[14:17]
	v_mfma_f32_16x16x32_bf16 v[58:61], v[134:137], v[190:193], v[58:61]
	v_mfma_f32_16x16x32_bf16 v[54:57], v[142:145], v[190:193], v[54:57]
	v_mfma_f32_16x16x32_bf16 v[42:45], v[134:137], v[178:181], v[42:45]
	v_mfma_f32_16x16x32_bf16 v[38:41], v[142:145], v[178:181], v[38:41]
	v_mfma_f32_16x16x32_bf16 v[26:29], v[134:137], v[174:177], v[26:29]
	v_mfma_f32_16x16x32_bf16 v[22:25], v[142:145], v[174:177], v[22:25]
	v_mfma_f32_16x16x32_bf16 v[10:13], v[134:137], v[166:169], v[10:13]
	v_mfma_f32_16x16x32_bf16 v[4:7], v[142:145], v[166:169], v[6:9]
	v_mfma_f32_16x16x32_bf16 v[58:61], v[138:141], v[194:197], v[58:61]
	v_mfma_f32_16x16x32_bf16 v[54:57], v[146:149], v[194:197], v[54:57]
	v_mfma_f32_16x16x32_bf16 v[42:45], v[138:141], v[182:185], v[42:45]
	v_mfma_f32_16x16x32_bf16 v[38:41], v[146:149], v[182:185], v[38:41]
	v_mfma_f32_16x16x32_bf16 v[26:29], v[138:141], v[186:189], v[26:29]
	v_mfma_f32_16x16x32_bf16 v[22:25], v[146:149], v[186:189], v[22:25]
	v_mfma_f32_16x16x32_bf16 v[10:13], v[138:141], v[170:173], v[10:13]
	v_mfma_f32_16x16x32_bf16 v[6:9], v[146:149], v[170:173], v[4:7]
	s_setprio 0
; #define PG8_STAGE(bufoff, gbase, voff) do { _Pragma("unroll") for (int _i = 0; _i < 2; ++_i) \
;         __builtin_amdgcn_global_load_lds((const unsigned*)((const char*)(gbase) + (voff)[_i]), (LAS unsigned*)(lds + (bufoff) + ldsw + _i * 8192), 16, 0, 0); } while (0)
; #define PG8_LDA(dst, b, h) do { _Pragma("unroll") for (int m = 0; m < 4; ++m) _Pragma("unroll") for (int k = 0; k < 2; ++k) dst[m][k] = *(const LAS bf16x8*)(lds + PG8_SA(b, h) + ((aoff ^ (k * 64)) + m * 2048)); } while (0)
; #define PG8_MMA(ai, bj, At, Bt) do { __builtin_amdgcn_s_setprio(1); _Pragma("unroll") for (int m = 0; m < 4; ++m) _Pragma("unroll") for (int n = 0; n < 2; ++n) _Pragma("unroll") for (int k = 0; k < 2; ++k) \
;         acc[ai][bj][m][n] = __builtin_amdgcn_mfma_f32_16x16x32_bf16(Bt[n][k], At[m][k], acc[ai][bj][m][n], 0, 0, 0); __builtin_amdgcn_s_setprio(0); } while (0)
; #define PG8_WAIT_V(n) asm volatile("s_waitcnt vmcnt(" #n ")" ::: "memory")
; #define PG8_WAIT_L(n) asm volatile("s_waitcnt lgkmcnt(" #n ")" ::: "memory")
; #define PG8_BAR __builtin_amdgcn_s_barrier()
; #define PG8_SCHED __builtin_amdgcn_sched_barrier(0)
;     ...
;             PG8_LDA(At, 1, 1); PG8_STAGE(PG8_SB(1, 0), b3, voffB); PG8_STAGE(PG8_SB(1, 1), b3 + hstep, voffB); PG8_STAGE(PG8_SA(1, 0), a3, vs[0]);
;             PG8_WAIT_V(8); PG8_WAIT_L(0); PG8_BAR; if (do1) { PG8_MMA(1, 0, At, B0); PG8_MMA(1, 1, At, B1); } PG8_BAR; PG8_SCHED;
;         }
;     ...
;         if (wr == 1) PG8_BAR;
.LBB0_1106:
	s_add_u32 s6, s26, 0x4000
	s_addc_u32 s7, s27, 0
	s_add_u32 s26, s24, 0x4000
	s_addc_u32 s27, s25, 0
	s_barrier
	s_setprio 3
	s_mov_b32 m0, s39
	v_lshl_add_u64 v[4:5], s[26:27], 0, v[208:209]
	s_add_u32 s24, s24, 0xb4000
	s_waitcnt lgkmcnt(0)
	ds_read_b128 v[190:193], v226 offset:49152
	ds_read_b128 v[178:181], v226 offset:51200
	ds_read_b128 v[194:197], v227 offset:49152
	ds_read_b128 v[182:185], v227 offset:51200
	ds_read_b128 v[174:177], v226 offset:53248
	ds_read_b128 v[166:169], v226 offset:55296
	ds_read_b128 v[186:189], v227 offset:53248
	ds_read_b128 v[170:173], v227 offset:55296
	global_load_lds_dwordx4 v[4:5], off
	v_lshl_add_u64 v[4:5], s[26:27], 0, v[210:211]
	s_mov_b32 m0, s40
	s_addc_u32 s25, s25, 0
	global_load_lds_dwordx4 v[4:5], off
	v_lshl_add_u64 v[4:5], s[24:25], 0, v[208:209]
	s_mov_b32 m0, s43
	s_and_b64 vcc, exec, s[8:9]
	global_load_lds_dwordx4 v[4:5], off
	v_lshl_add_u64 v[4:5], s[24:25], 0, v[210:211]
	s_mov_b32 m0, s44
	s_nop 0
	global_load_lds_dwordx4 v[4:5], off
	v_lshl_add_u64 v[4:5], s[6:7], 0, v[200:201]
	s_mov_b32 m0, s41
	s_nop 0
	global_load_lds_dwordx4 v[4:5], off
	v_lshl_add_u64 v[4:5], s[6:7], 0, v[202:203]
	s_mov_b32 m0, s42
	s_nop 0
	global_load_lds_dwordx4 v[4:5], off
	s_waitcnt vmcnt(8)
	s_waitcnt lgkmcnt(0)
	s_barrier
	s_cbranch_vccnz .LBB0_1099
	s_setprio 1
	s_waitcnt lgkmcnt(0)
	v_mfma_f32_16x16x32_bf16 v[130:133], v[150:153], v[190:193], v[130:133]
	v_mfma_f32_16x16x32_bf16 v[126:129], v[158:161], v[190:193], v[126:129]
	v_mfma_f32_16x16x32_bf16 v[114:117], v[150:153], v[178:181], v[114:117]
	v_mfma_f32_16x16x32_bf16 v[110:113], v[158:161], v[178:181], v[110:113]
	v_mfma_f32_16x16x32_bf16 v[98:101], v[150:153], v[174:177], v[98:101]
	v_mfma_f32_16x16x32_bf16 v[94:97], v[158:161], v[174:177], v[94:97]
	v_mfma_f32_16x16x32_bf16 v[82:85], v[150:153], v[166:169], v[82:85]
	v_mfma_f32_16x16x32_bf16 v[78:81], v[158:161], v[166:169], v[78:81]
	v_mfma_f32_16x16x32_bf16 v[130:133], v[154:157], v[194:197], v[130:133]
	v_mfma_f32_16x16x32_bf16 v[126:129], v[162:165], v[194:197], v[126:129]
	v_mfma_f32_16x16x32_bf16 v[114:117], v[154:157], v[182:185], v[114:117]
	v_mfma_f32_16x16x32_bf16 v[110:113], v[162:165], v[182:185], v[110:113]
	v_mfma_f32_16x16x32_bf16 v[98:101], v[154:157], v[186:189], v[98:101]
	v_mfma_f32_16x16x32_bf16 v[94:97], v[162:165], v[186:189], v[94:97]
	v_mfma_f32_16x16x32_bf16 v[82:85], v[154:157], v[170:173], v[82:85]
	v_mfma_f32_16x16x32_bf16 v[78:81], v[162:165], v[170:173], v[78:81]
	v_mfma_f32_16x16x32_bf16 v[122:125], v[134:137], v[190:193], v[122:125]
	v_mfma_f32_16x16x32_bf16 v[118:121], v[142:145], v[190:193], v[118:121]
	v_mfma_f32_16x16x32_bf16 v[106:109], v[134:137], v[178:181], v[106:109]
	v_mfma_f32_16x16x32_bf16 v[102:105], v[142:145], v[178:181], v[102:105]
	v_mfma_f32_16x16x32_bf16 v[90:93], v[134:137], v[174:177], v[90:93]
	v_mfma_f32_16x16x32_bf16 v[86:89], v[142:145], v[174:177], v[86:89]
	v_mfma_f32_16x16x32_bf16 v[74:77], v[134:137], v[166:169], v[74:77]
	v_mfma_f32_16x16x32_bf16 v[70:73], v[142:145], v[166:169], v[70:73]
	v_mfma_f32_16x16x32_bf16 v[122:125], v[138:141], v[194:197], v[122:125]
	v_mfma_f32_16x16x32_bf16 v[118:121], v[146:149], v[194:197], v[118:121]
	v_mfma_f32_16x16x32_bf16 v[106:109], v[138:141], v[182:185], v[106:109]
	v_mfma_f32_16x16x32_bf16 v[102:105], v[146:149], v[182:185], v[102:105]
	v_mfma_f32_16x16x32_bf16 v[90:93], v[138:141], v[186:189], v[90:93]
	v_mfma_f32_16x16x32_bf16 v[86:89], v[146:149], v[186:189], v[86:89]
	v_mfma_f32_16x16x32_bf16 v[74:77], v[138:141], v[170:173], v[74:77]
	v_mfma_f32_16x16x32_bf16 v[70:73], v[146:149], v[170:173], v[70:73]
	s_setprio 0
	s_branch .LBB0_1099
.LBB0_1108:
	s_and_b64 vcc, exec, s[10:11]
	s_cbranch_vccz .LBB0_1110
	s_barrier
	s_setprio 3

; #define PG8_STAGE(bufoff, gbase, voff) do { _Pragma("unroll") for (int _i = 0; _i < 2; ++_i) \
;         __builtin_amdgcn_global_load_lds((const unsigned*)((const char*)(gbase) + (voff)[_i]), (LAS unsigned*)(lds + (bufoff) + ldsw + _i * 8192), 16, 0, 0); } while (0)
; #define PG8_LDA(dst, b, h) do { _Pragma("unroll") for (int m = 0; m < 4; ++m) _Pragma("unroll") for (int k = 0; k < 2; ++k) dst[m][k] = *(const LAS bf16x8*)(lds + PG8_SA(b, h) + ((aoff ^ (k * 64)) + m * 2048)); } while (0)
; #define PG8_LDB(dst, b, h) do { _Pragma("unroll") for (int n = 0; n < 2; ++n) _Pragma("unroll") for (int k = 0; k < 2; ++k) dst[n][k] = *(const LAS bf16x8*)(lds + PG8_SB(b, h) + ((boff ^ (k * 64)) + n * 2048)); } while (0)
; #define PG8_WAIT_V(n) asm volatile("s_waitcnt vmcnt(" #n ")" ::: "memory")
; #define PG8_BAR __builtin_amdgcn_s_barrier()
;     ...
;         for (int t = 0; t < nt; t += 2) {
;             const bool last = (t == nt - 2);
;             const char* a1 = cA + (size_t)(t + 1) * kstepA;
;             const char* a2 = last ? nA : cA + (size_t)(t + 2) * kstepA; const char* b2 = last ? nB : cB + (size_t)(t + 2) * kstepB;
;             const char* a3 = a2 + kstepA; const char* b3 = b2 + kstepB;
;             unsigned vs[2][2];
;             if constexpr (GATHER) {
;                 if (last && has_next) {
; #pragma unroll
;                     for (int hh = 0; hh < 2; ++hh)
; #pragma unroll
;                         for (int i = 0; i < 2; ++i) voffN[hh][i] = (unsigned)idxl[(ui + 1) * 256 + hh * HALF + sR[i]] * (unsigned)(K * 2) + (unsigned)sC[i] * 2u;
;                 }
; #pragma unroll
;                 for (int hh = 0; hh < 2; ++hh)
; #pragma unroll
;                     for (int i = 0; i < 2; ++i) vs[hh][i] = last ? voffN[hh][i] : voffA[hh][i];
;             } else {
; #pragma unroll
;                 for (int hh = 0; hh < 2; ++hh)
; #pragma unroll
;                     for (int i = 0; i < 2; ++i) vs[hh][i] = voffA[hh][i];
;             }
;             PG8_LDB(B0, 0, 0); PG8_LDB(B1, 0, 1); PG8_SCHED; PG8_LDA(At, 0, 0); PG8_STAGE(PG8_SA(1, 1), a1, voffA[1]);
;             PG8_WAIT_V(8); PG8_WAIT_L(0); PG8_BAR; if (do0) { PG8_MMA(0, 0, At, B0); PG8_MMA(0, 1, At, B1); } PG8_BAR; PG8_SCHED;
;             PG8_LDA(At, 0, 1); PG8_STAGE(PG8_SB(0, 0), b2, voffB); PG8_STAGE(PG8_SB(0, 1), b2 + hstep, voffB); PG8_STAGE(PG8_SA(0, 0), a2, vs[0]);
.LBB0_1257:
	ds_read_b128 v[156:159], v176
	ds_read_b128 v[160:163], v177
	ds_read_b128 v[164:167], v178
	ds_read_b128 v[192:195], v179
	ds_read_b128 v[200:203], v180
	ds_read_b128 v[204:207], v181
	ds_read_b128 v[208:211], v182
	ds_read_b128 v[212:215], v183
	s_add_u32 s40, s38, 0x80
	s_addc_u32 s41, s39, 0
	s_cmp_eq_u32 s63, 12
	s_cselect_b32 s45, s3, s41
	s_cselect_b32 s44, s11, s40
	s_cselect_b32 s41, s12, s62
	s_cselect_b32 s40, s29, s31
	v_lshl_add_u64 v[168:169], s[38:39], 0, v[150:151]
	s_add_i32 m0, s47, 0xc000
	ds_read_b128 v[216:219], v184
	ds_read_b128 v[220:223], v184 offset:2048
	ds_read_b128 v[224:227], v185
	ds_read_b128 v[228:231], v185 offset:2048
	ds_read_b128 v[232:235], v184 offset:4096
	ds_read_b128 v[236:239], v184 offset:6144
	ds_read_b128 v[240:243], v185 offset:4096
	ds_read_b128 v[244:247], v185 offset:6144
	global_load_lds_dwordx4 v[168:169], off
	v_lshl_add_u64 v[168:169], s[38:39], 0, v[148:149]
	s_add_i32 m0, s47, 0xe000
	s_add_u32 s42, s40, 0x4000
	global_load_lds_dwordx4 v[168:169], off
	s_waitcnt vmcnt(8)
	s_waitcnt lgkmcnt(0)
	s_addc_u32 s43, s41, 0
	s_barrier
	s_setprio 1
	s_waitcnt lgkmcnt(0)
	v_mfma_f32_16x16x32_bf16 v[126:129], v[156:159], v[216:219], v[126:129]
	v_mfma_f32_16x16x32_bf16 v[118:121], v[164:167], v[216:219], v[118:121]
	v_mfma_f32_16x16x32_bf16 v[110:113], v[156:159], v[220:223], v[110:113]
	v_mfma_f32_16x16x32_bf16 v[102:105], v[164:167], v[220:223], v[102:105]
	v_mfma_f32_16x16x32_bf16 v[94:97], v[156:159], v[232:235], v[94:97]
	v_mfma_f32_16x16x32_bf16 v[86:89], v[164:167], v[232:235], v[86:89]
	v_mfma_f32_16x16x32_bf16 v[78:81], v[156:159], v[236:239], v[78:81]
	v_mfma_f32_16x16x32_bf16 v[70:73], v[164:167], v[236:239], v[70:73]
	v_mfma_f32_16x16x32_bf16 v[126:129], v[160:163], v[224:227], v[126:129]
	v_mfma_f32_16x16x32_bf16 v[118:121], v[192:195], v[224:227], v[118:121]
	v_mfma_f32_16x16x32_bf16 v[110:113], v[160:163], v[228:231], v[110:113]
	v_mfma_f32_16x16x32_bf16 v[102:105], v[192:195], v[228:231], v[102:105]
	v_mfma_f32_16x16x32_bf16 v[94:97], v[160:163], v[240:243], v[94:97]
	v_mfma_f32_16x16x32_bf16 v[86:89], v[192:195], v[240:243], v[86:89]
	v_mfma_f32_16x16x32_bf16 v[78:81], v[160:163], v[244:247], v[78:81]
	v_mfma_f32_16x16x32_bf16 v[70:73], v[192:195], v[244:247], v[70:73]
	v_mfma_f32_16x16x32_bf16 v[122:125], v[200:203], v[216:219], v[122:125]
	v_mfma_f32_16x16x32_bf16 v[114:117], v[208:211], v[216:219], v[114:117]
	v_mfma_f32_16x16x32_bf16 v[106:109], v[200:203], v[220:223], v[106:109]
	v_mfma_f32_16x16x32_bf16 v[98:101], v[208:211], v[220:223], v[98:101]
	v_mfma_f32_16x16x32_bf16 v[90:93], v[200:203], v[232:235], v[90:93]
	v_mfma_f32_16x16x32_bf16 v[82:85], v[208:211], v[232:235], v[82:85]
	v_mfma_f32_16x16x32_bf16 v[74:77], v[200:203], v[236:239], v[74:77]
	v_mfma_f32_16x16x32_bf16 v[66:69], v[208:211], v[236:239], v[66:69]
	v_mfma_f32_16x16x32_bf16 v[122:125], v[204:207], v[224:227], v[122:125]
	v_mfma_f32_16x16x32_bf16 v[114:117], v[212:215], v[224:227], v[114:117]
	v_mfma_f32_16x16x32_bf16 v[106:109], v[204:207], v[228:231], v[106:109]
	v_mfma_f32_16x16x32_bf16 v[98:101], v[212:215], v[228:231], v[98:101]
	v_mfma_f32_16x16x32_bf16 v[90:93], v[204:207], v[240:243], v[90:93]
	v_mfma_f32_16x16x32_bf16 v[82:85], v[212:215], v[240:243], v[82:85]
	v_mfma_f32_16x16x32_bf16 v[74:77], v[204:207], v[244:247], v[74:77]
	v_mfma_f32_16x16x32_bf16 v[66:69], v[212:215], v[244:247], v[66:69]
	s_setprio 0
	s_barrier
	s_setprio 3
	s_add_i32 s64, s56, s46
	v_lshl_add_u64 v[168:169], s[40:41], 0, v[130:131]
	s_mov_b32 m0, s64
	ds_read_b128 v[216:219], v184 offset:16384
	ds_read_b128 v[220:223], v184 offset:18432
	ds_read_b128 v[224:227], v185 offset:16384
	ds_read_b128 v[228:231], v185 offset:18432
	ds_read_b128 v[232:235], v184 offset:20480
	ds_read_b128 v[236:239], v184 offset:22528
	ds_read_b128 v[240:243], v185 offset:20480
	ds_read_b128 v[244:247], v185 offset:22528
	global_load_lds_dwordx4 v[168:169], off
	s_add_i32 m0, s64, 0x2000
	s_add_u32 s64, s40, 0x40000
	v_lshl_add_u64 v[168:169], s[40:41], 0, v[132:133]
	s_addc_u32 s65, s41, 0
	s_add_i32 s66, s57, s46
	global_load_lds_dwordx4 v[168:169], off
	v_lshl_add_u64 v[168:169], s[64:65], 0, v[130:131]
	s_mov_b32 m0, s66
	v_lshl_add_u64 v[196:197], s[44:45], 0, v[136:137]
	global_load_lds_dwordx4 v[168:169], off
	v_lshl_add_u64 v[168:169], s[64:65], 0, v[132:133]
	s_add_i32 m0, s66, 0x2000
	s_nop 0
	global_load_lds_dwordx4 v[168:169], off
	v_lshl_add_u64 v[168:169], s[44:45], 0, v[134:135]
	s_mov_b32 m0, s47
	s_nop 0
	global_load_lds_dwordx4 v[168:169], off
	s_mov_b32 m0, s48
	s_nop 0
	global_load_lds_dwordx4 v[196:197], off
	s_waitcnt vmcnt(8)
	s_waitcnt lgkmcnt(0)
	s_barrier
; #define PG8_STAGE(bufoff, gbase, voff) do { _Pragma("unroll") for (int _i = 0; _i < 2; ++_i) \
;         __builtin_amdgcn_global_load_lds((const unsigned*)((const char*)(gbase) + (voff)[_i]), (LAS unsigned*)(lds + (bufoff) + ldsw + _i * 8192), 16, 0, 0); } while (0)
; #define PG8_LDA(dst, b, h) do { _Pragma("unroll") for (int m = 0; m < 4; ++m) _Pragma("unroll") for (int k = 0; k < 2; ++k) dst[m][k] = *(const LAS bf16x8*)(lds + PG8_SA(b, h) + ((aoff ^ (k * 64)) + m * 2048)); } while (0)
; #define PG8_LDB(dst, b, h) do { _Pragma("unroll") for (int n = 0; n < 2; ++n) _Pragma("unroll") for (int k = 0; k < 2; ++k) dst[n][k] = *(const LAS bf16x8*)(lds + PG8_SB(b, h) + ((boff ^ (k * 64)) + n * 2048)); } while (0)
; #define PG8_MMA(ai, bj, At, Bt) do { __builtin_amdgcn_s_setprio(1); _Pragma("unroll") for (int m = 0; m < 4; ++m) _Pragma("unroll") for (int n = 0; n < 2; ++n) _Pragma("unroll") for (int k = 0; k < 2; ++k) \
;         acc[ai][bj][m][n] = __builtin_amdgcn_mfma_f32_16x16x32_bf16(Bt[n][k], At[m][k], acc[ai][bj][m][n], 0, 0, 0); __builtin_amdgcn_s_setprio(0); } while (0)
; #define PG8_WAIT_V(n) asm volatile("s_waitcnt vmcnt(" #n ")" ::: "memory")
; #define PG8_WAIT_L(n) asm volatile("s_waitcnt lgkmcnt(" #n ")" ::: "memory")
; #define PG8_BAR __builtin_amdgcn_s_barrier()
; #define PG8_SCHED __builtin_amdgcn_sched_barrier(0)
;     ...
;             PG8_WAIT_V(8); PG8_WAIT_L(0); PG8_BAR; if (do1) { PG8_MMA(1, 0, At, B0); PG8_MMA(1, 1, At, B1); } PG8_BAR; PG8_SCHED;
;             PG8_LDB(B0, 1, 0); PG8_LDB(B1, 1, 1); PG8_SCHED; PG8_LDA(At, 1, 0); PG8_STAGE(PG8_SA(0, 1), a2, vs[1]);
;             PG8_WAIT_V(8); PG8_WAIT_L(0); PG8_BAR; if (do0) { PG8_MMA(0, 0, At, B0); PG8_MMA(0, 1, At, B1); } PG8_BAR; PG8_SCHED;
	s_setprio 1
	s_waitcnt lgkmcnt(0)
	v_mfma_f32_16x16x32_bf16 v[62:65], v[156:159], v[216:219], v[62:65]
	v_mfma_f32_16x16x32_bf16 v[54:57], v[164:167], v[216:219], v[54:57]
	v_mfma_f32_16x16x32_bf16 v[46:49], v[156:159], v[220:223], v[46:49]
	v_mfma_f32_16x16x32_bf16 v[38:41], v[164:167], v[220:223], v[38:41]
	v_mfma_f32_16x16x32_bf16 v[30:33], v[156:159], v[232:235], v[30:33]
	v_mfma_f32_16x16x32_bf16 v[22:25], v[164:167], v[232:235], v[22:25]
	v_mfma_f32_16x16x32_bf16 v[14:17], v[156:159], v[236:239], v[14:17]
	v_mfma_f32_16x16x32_bf16 v[6:9], v[164:167], v[236:239], v[6:9]
	v_mfma_f32_16x16x32_bf16 v[62:65], v[160:163], v[224:227], v[62:65]
	v_mfma_f32_16x16x32_bf16 v[54:57], v[192:195], v[224:227], v[54:57]
	v_mfma_f32_16x16x32_bf16 v[46:49], v[160:163], v[228:231], v[46:49]
	v_mfma_f32_16x16x32_bf16 v[38:41], v[192:195], v[228:231], v[38:41]
	v_mfma_f32_16x16x32_bf16 v[30:33], v[160:163], v[240:243], v[30:33]
	v_mfma_f32_16x16x32_bf16 v[22:25], v[192:195], v[240:243], v[22:25]
	v_mfma_f32_16x16x32_bf16 v[14:17], v[160:163], v[244:247], v[14:17]
	v_mfma_f32_16x16x32_bf16 v[6:9], v[192:195], v[244:247], v[6:9]
	v_mfma_f32_16x16x32_bf16 v[58:61], v[200:203], v[216:219], v[58:61]
	v_mfma_f32_16x16x32_bf16 v[50:53], v[208:211], v[216:219], v[50:53]
	v_mfma_f32_16x16x32_bf16 v[42:45], v[200:203], v[220:223], v[42:45]
	v_mfma_f32_16x16x32_bf16 v[34:37], v[208:211], v[220:223], v[34:37]
	v_mfma_f32_16x16x32_bf16 v[26:29], v[200:203], v[232:235], v[26:29]
	v_mfma_f32_16x16x32_bf16 v[18:21], v[208:211], v[232:235], v[18:21]
	v_mfma_f32_16x16x32_bf16 v[10:13], v[200:203], v[236:239], v[10:13]
	v_mfma_f32_16x16x32_bf16 v[2:5], v[208:211], v[236:239], v[2:5]
	v_mfma_f32_16x16x32_bf16 v[58:61], v[204:207], v[224:227], v[58:61]
	v_mfma_f32_16x16x32_bf16 v[50:53], v[212:215], v[224:227], v[50:53]
	v_mfma_f32_16x16x32_bf16 v[42:45], v[204:207], v[228:231], v[42:45]
	v_mfma_f32_16x16x32_bf16 v[34:37], v[212:215], v[228:231], v[34:37]
	v_mfma_f32_16x16x32_bf16 v[26:29], v[204:207], v[240:243], v[26:29]
	v_mfma_f32_16x16x32_bf16 v[18:21], v[212:215], v[240:243], v[18:21]
	v_mfma_f32_16x16x32_bf16 v[10:13], v[204:207], v[244:247], v[10:13]
	v_mfma_f32_16x16x32_bf16 v[2:5], v[212:215], v[244:247], v[2:5]
	s_setprio 0
	s_barrier
	s_setprio 3
	s_add_i32 s64, 0, 0x18000
	v_add_u32_e32 v142, s64, v170
	v_add_u32_e32 v160, s64, v174
	s_add_i32 s65, 0, 0x1c000
	ds_read_b128 v[156:159], v142
	ds_read_b128 v[160:163], v160
	ds_read_b128 v[164:167], v186
	ds_read_b128 v[192:195], v187
	v_add_u32_e32 v142, s65, v170
	v_add_u32_e32 v191, s65, v174
	ds_read_b128 v[200:203], v142
	ds_read_b128 v[204:207], v191
	ds_read_b128 v[208:211], v188
	ds_read_b128 v[212:215], v189
	s_mov_b32 m0, s49
	v_lshl_add_u64 v[248:249], s[44:45], 0, v[138:139]
	ds_read_b128 v[216:219], v184 offset:32768
	ds_read_b128 v[220:223], v184 offset:34816
	ds_read_b128 v[224:227], v185 offset:32768
	ds_read_b128 v[228:231], v185 offset:34816
	ds_read_b128 v[232:235], v184 offset:36864
	ds_read_b128 v[236:239], v184 offset:38912
	ds_read_b128 v[240:243], v185 offset:36864
	ds_read_b128 v[244:247], v185 offset:38912
	global_load_lds_dwordx4 v[248:249], off
	v_lshl_add_u64 v[248:249], s[44:45], 0, v[140:141]
	s_mov_b32 m0, s50
	s_nop 0
	global_load_lds_dwordx4 v[248:249], off
	s_waitcnt vmcnt(8)
	s_waitcnt lgkmcnt(0)
	s_barrier
	s_setprio 1
	s_waitcnt lgkmcnt(0)
	v_mfma_f32_16x16x32_bf16 v[126:129], v[156:159], v[216:219], v[126:129]
	v_mfma_f32_16x16x32_bf16 v[118:121], v[164:167], v[216:219], v[118:121]
	v_mfma_f32_16x16x32_bf16 v[110:113], v[156:159], v[220:223], v[110:113]
	v_mfma_f32_16x16x32_bf16 v[102:105], v[164:167], v[220:223], v[102:105]
	v_mfma_f32_16x16x32_bf16 v[94:97], v[156:159], v[232:235], v[94:97]
	v_mfma_f32_16x16x32_bf16 v[86:89], v[164:167], v[232:235], v[86:89]
	v_mfma_f32_16x16x32_bf16 v[78:81], v[156:159], v[236:239], v[78:81]
	v_mfma_f32_16x16x32_bf16 v[70:73], v[164:167], v[236:239], v[70:73]
	v_mfma_f32_16x16x32_bf16 v[126:129], v[160:163], v[224:227], v[126:129]
	v_mfma_f32_16x16x32_bf16 v[118:121], v[192:195], v[224:227], v[118:121]
	v_mfma_f32_16x16x32_bf16 v[110:113], v[160:163], v[228:231], v[110:113]
	v_mfma_f32_16x16x32_bf16 v[102:105], v[192:195], v[228:231], v[102:105]
	v_mfma_f32_16x16x32_bf16 v[94:97], v[160:163], v[240:243], v[94:97]
	v_mfma_f32_16x16x32_bf16 v[86:89], v[192:195], v[240:243], v[86:89]
	v_mfma_f32_16x16x32_bf16 v[78:81], v[160:163], v[244:247], v[78:81]
	v_mfma_f32_16x16x32_bf16 v[70:73], v[192:195], v[244:247], v[70:73]
	v_mfma_f32_16x16x32_bf16 v[122:125], v[200:203], v[216:219], v[122:125]
	v_mfma_f32_16x16x32_bf16 v[114:117], v[208:211], v[216:219], v[114:117]
	v_mfma_f32_16x16x32_bf16 v[106:109], v[200:203], v[220:223], v[106:109]
	v_mfma_f32_16x16x32_bf16 v[98:101], v[208:211], v[220:223], v[98:101]
	v_mfma_f32_16x16x32_bf16 v[90:93], v[200:203], v[232:235], v[90:93]
	v_mfma_f32_16x16x32_bf16 v[82:85], v[208:211], v[232:235], v[82:85]
	v_mfma_f32_16x16x32_bf16 v[74:77], v[200:203], v[236:239], v[74:77]
	v_mfma_f32_16x16x32_bf16 v[66:69], v[208:211], v[236:239], v[66:69]
	v_mfma_f32_16x16x32_bf16 v[122:125], v[204:207], v[224:227], v[122:125]
	v_mfma_f32_16x16x32_bf16 v[114:117], v[212:215], v[224:227], v[114:117]
	v_mfma_f32_16x16x32_bf16 v[106:109], v[204:207], v[228:231], v[106:109]
	v_mfma_f32_16x16x32_bf16 v[98:101], v[212:215], v[228:231], v[98:101]
	v_mfma_f32_16x16x32_bf16 v[90:93], v[204:207], v[240:243], v[90:93]
	v_mfma_f32_16x16x32_bf16 v[82:85], v[212:215], v[240:243], v[82:85]
	v_mfma_f32_16x16x32_bf16 v[74:77], v[204:207], v[244:247], v[74:77]
	v_mfma_f32_16x16x32_bf16 v[66:69], v[212:215], v[244:247], v[66:69]
	s_setprio 0
	s_barrier
; #define PG8_STAGE(bufoff, gbase, voff) do { _Pragma("unroll") for (int _i = 0; _i < 2; ++_i) \
;         __builtin_amdgcn_global_load_lds((const unsigned*)((const char*)(gbase) + (voff)[_i]), (LAS unsigned*)(lds + (bufoff) + ldsw + _i * 8192), 16, 0, 0); } while (0)
; #define PG8_LDA(dst, b, h) do { _Pragma("unroll") for (int m = 0; m < 4; ++m) _Pragma("unroll") for (int k = 0; k < 2; ++k) dst[m][k] = *(const LAS bf16x8*)(lds + PG8_SA(b, h) + ((aoff ^ (k * 64)) + m * 2048)); } while (0)
; #define PG8_MMA(ai, bj, At, Bt) do { __builtin_amdgcn_s_setprio(1); _Pragma("unroll") for (int m = 0; m < 4; ++m) _Pragma("unroll") for (int n = 0; n < 2; ++n) _Pragma("unroll") for (int k = 0; k < 2; ++k) \
;         acc[ai][bj][m][n] = __builtin_amdgcn_mfma_f32_16x16x32_bf16(Bt[n][k], At[m][k], acc[ai][bj][m][n], 0, 0, 0); __builtin_amdgcn_s_setprio(0); } while (0)
; #define PG8_WAIT_V(n) asm volatile("s_waitcnt vmcnt(" #n ")" ::: "memory")
; #define PG8_WAIT_L(n) asm volatile("s_waitcnt lgkmcnt(" #n ")" ::: "memory")
; #define PG8_BAR __builtin_amdgcn_s_barrier()
; #define PG8_SCHED __builtin_amdgcn_sched_barrier(0)
;     ...
;             PG8_LDA(At, 1, 1); PG8_STAGE(PG8_SB(1, 0), b3, voffB); PG8_STAGE(PG8_SB(1, 1), b3 + hstep, voffB); PG8_STAGE(PG8_SA(1, 0), a3, vs[0]);
;             PG8_WAIT_V(8); PG8_WAIT_L(0); PG8_BAR; if (do1) { PG8_MMA(1, 0, At, B0); PG8_MMA(1, 1, At, B1); } PG8_BAR; PG8_SCHED;
;         }
;         if (wr == 0) PG8_BAR;
	s_setprio 3
	s_add_i32 s44, s64, s46
	v_lshl_add_u64 v[248:249], s[42:43], 0, v[130:131]
	s_mov_b32 m0, s44
	ds_read_b128 v[216:219], v184 offset:49152
	ds_read_b128 v[220:223], v184 offset:51200
	ds_read_b128 v[224:227], v185 offset:49152
	ds_read_b128 v[228:231], v185 offset:51200
	ds_read_b128 v[232:235], v184 offset:53248
	ds_read_b128 v[236:239], v184 offset:55296
	ds_read_b128 v[240:243], v185 offset:53248
	ds_read_b128 v[244:247], v185 offset:55296
	global_load_lds_dwordx4 v[248:249], off
	s_add_i32 m0, s44, 0x2000
	s_add_u32 s40, s40, 0x44000
	v_lshl_add_u64 v[248:249], s[42:43], 0, v[132:133]
	s_addc_u32 s41, s41, 0
	s_add_i32 s42, s65, s46
	global_load_lds_dwordx4 v[248:249], off
	v_lshl_add_u64 v[248:249], s[40:41], 0, v[130:131]
	s_mov_b32 m0, s42
	v_lshl_add_u64 v[168:169], v[168:169], 0, s[20:21]
	global_load_lds_dwordx4 v[248:249], off
	v_lshl_add_u64 v[248:249], s[40:41], 0, v[132:133]
	s_add_i32 m0, s42, 0x2000
	s_nop 0
	global_load_lds_dwordx4 v[248:249], off
	s_mov_b32 m0, s52
	s_nop 0
	global_load_lds_dwordx4 v[168:169], off
	v_lshl_add_u64 v[168:169], v[196:197], 0, s[20:21]
	s_mov_b32 m0, s53
	s_nop 0
	global_load_lds_dwordx4 v[168:169], off
	s_waitcnt vmcnt(8)
	s_waitcnt lgkmcnt(0)
	s_barrier
	s_setprio 1
	s_waitcnt lgkmcnt(0)
	v_mfma_f32_16x16x32_bf16 v[62:65], v[156:159], v[216:219], v[62:65]
	v_mfma_f32_16x16x32_bf16 v[54:57], v[164:167], v[216:219], v[54:57]
	v_mfma_f32_16x16x32_bf16 v[46:49], v[156:159], v[220:223], v[46:49]
	v_mfma_f32_16x16x32_bf16 v[38:41], v[164:167], v[220:223], v[38:41]
	v_mfma_f32_16x16x32_bf16 v[30:33], v[156:159], v[232:235], v[30:33]
	v_mfma_f32_16x16x32_bf16 v[22:25], v[164:167], v[232:235], v[22:25]
	v_mfma_f32_16x16x32_bf16 v[14:17], v[156:159], v[236:239], v[14:17]
	v_mfma_f32_16x16x32_bf16 v[6:9], v[164:167], v[236:239], v[6:9]
	v_mfma_f32_16x16x32_bf16 v[62:65], v[160:163], v[224:227], v[62:65]
	v_mfma_f32_16x16x32_bf16 v[54:57], v[192:195], v[224:227], v[54:57]
	v_mfma_f32_16x16x32_bf16 v[46:49], v[160:163], v[228:231], v[46:49]
	v_mfma_f32_16x16x32_bf16 v[38:41], v[192:195], v[228:231], v[38:41]
	v_mfma_f32_16x16x32_bf16 v[30:33], v[160:163], v[240:243], v[30:33]
	v_mfma_f32_16x16x32_bf16 v[22:25], v[192:195], v[240:243], v[22:25]
	v_mfma_f32_16x16x32_bf16 v[14:17], v[160:163], v[244:247], v[14:17]
	v_mfma_f32_16x16x32_bf16 v[6:9], v[192:195], v[244:247], v[6:9]
	v_mfma_f32_16x16x32_bf16 v[58:61], v[200:203], v[216:219], v[58:61]
	v_mfma_f32_16x16x32_bf16 v[50:53], v[208:211], v[216:219], v[50:53]
	v_mfma_f32_16x16x32_bf16 v[42:45], v[200:203], v[220:223], v[42:45]
	v_mfma_f32_16x16x32_bf16 v[34:37], v[208:211], v[220:223], v[34:37]
	v_mfma_f32_16x16x32_bf16 v[26:29], v[200:203], v[232:235], v[26:29]
	v_mfma_f32_16x16x32_bf16 v[18:21], v[208:211], v[232:235], v[18:21]
	v_mfma_f32_16x16x32_bf16 v[10:13], v[200:203], v[236:239], v[10:13]
	v_mfma_f32_16x16x32_bf16 v[2:5], v[208:211], v[236:239], v[2:5]
	v_mfma_f32_16x16x32_bf16 v[58:61], v[204:207], v[224:227], v[58:61]
	v_mfma_f32_16x16x32_bf16 v[50:53], v[212:215], v[224:227], v[50:53]
	v_mfma_f32_16x16x32_bf16 v[42:45], v[204:207], v[228:231], v[42:45]
	v_mfma_f32_16x16x32_bf16 v[34:37], v[212:215], v[228:231], v[34:37]
	v_mfma_f32_16x16x32_bf16 v[26:29], v[204:207], v[240:243], v[26:29]
	v_mfma_f32_16x16x32_bf16 v[18:21], v[212:215], v[240:243], v[18:21]
	v_mfma_f32_16x16x32_bf16 v[10:13], v[204:207], v[244:247], v[10:13]
	v_mfma_f32_16x16x32_bf16 v[2:5], v[212:215], v[244:247], v[2:5]
	s_setprio 0
	s_barrier
	s_setprio 3
	s_add_i32 s63, s63, 2
	s_add_u32 s31, s31, 0x8000
	s_addc_u32 s62, s62, 0
	s_add_u32 s38, s38, 0x100
	s_addc_u32 s39, s39, 0
	s_cmp_gt_u32 s63, 13
	s_cbranch_scc0 .LBB0_1257
	s_and_b64 vcc, exec, s[22:23]
	s_cbranch_vccz .LBB0_1260
	s_barrier

; #define PG8_STAGE(bufoff, gbase, voff) do { _Pragma("unroll") for (int _i = 0; _i < 2; ++_i) \
;         __builtin_amdgcn_global_load_lds((const unsigned*)((const char*)(gbase) + (voff)[_i]), (LAS unsigned*)(lds + (bufoff) + ldsw + _i * 8192), 16, 0, 0); } while (0)
; #define PG8_LDA(dst, b, h) do { _Pragma("unroll") for (int m = 0; m < 4; ++m) _Pragma("unroll") for (int k = 0; k < 2; ++k) dst[m][k] = *(const LAS bf16x8*)(lds + PG8_SA(b, h) + ((aoff ^ (k * 64)) + m * 2048)); } while (0)
; #define PG8_LDB(dst, b, h) do { _Pragma("unroll") for (int n = 0; n < 2; ++n) _Pragma("unroll") for (int k = 0; k < 2; ++k) dst[n][k] = *(const LAS bf16x8*)(lds + PG8_SB(b, h) + ((boff ^ (k * 64)) + n * 2048)); } while (0)
; #define PG8_WAIT_V(n) asm volatile("s_waitcnt vmcnt(" #n ")" ::: "memory")
; #define PG8_BAR __builtin_amdgcn_s_barrier()
;     ...
;         for (int t = 0; t < nt; t += 2) {
;             const bool last = (t == nt - 2);
;             const char* a1 = cA + (size_t)(t + 1) * kstepA;
;             const char* a2 = last ? nA : cA + (size_t)(t + 2) * kstepA; const char* b2 = last ? nB : cB + (size_t)(t + 2) * kstepB;
;             const char* a3 = a2 + kstepA; const char* b3 = b2 + kstepB;
;             unsigned vs[2][2];
;             if constexpr (GATHER) {
;                 if (last && has_next) {
; #pragma unroll
;                     for (int hh = 0; hh < 2; ++hh)
; #pragma unroll
;                         for (int i = 0; i < 2; ++i) voffN[hh][i] = (unsigned)idxl[(ui + 1) * 256 + hh * HALF + sR[i]] * (unsigned)(K * 2) + (unsigned)sC[i] * 2u;
;                 }
; #pragma unroll
;                 for (int hh = 0; hh < 2; ++hh)
; #pragma unroll
;                     for (int i = 0; i < 2; ++i) vs[hh][i] = last ? voffN[hh][i] : voffA[hh][i];
;             } else {
; #pragma unroll
;                 for (int hh = 0; hh < 2; ++hh)
; #pragma unroll
;                     for (int i = 0; i < 2; ++i) vs[hh][i] = voffA[hh][i];
;             }
;             PG8_LDB(B0, 0, 0); PG8_LDB(B1, 0, 1); PG8_SCHED; PG8_LDA(At, 0, 0); PG8_STAGE(PG8_SA(1, 1), a1, voffA[1]);
;             PG8_WAIT_V(8); PG8_WAIT_L(0); PG8_BAR; if (do0) { PG8_MMA(0, 0, At, B0); PG8_MMA(0, 1, At, B1); } PG8_BAR; PG8_SCHED;
;             PG8_LDA(At, 0, 1); PG8_STAGE(PG8_SB(0, 0), b2, voffB); PG8_STAGE(PG8_SB(0, 1), b2 + hstep, voffB); PG8_STAGE(PG8_SA(0, 0), a2, vs[0]);
.LBB0_1343:
	v_add_u32_e32 v130, s92, v161
	v_add_u32_e32 v134, s92, v188
	v_add_u32_e32 v138, s93, v161
	v_add_u32_e32 v142, s93, v188
	v_add_u32_e32 v158, s62, v161
	ds_read_b128 v[130:133], v130
	ds_read_b128 v[134:137], v134
	ds_read_b128 v[138:141], v138
	ds_read_b128 v[142:145], v142
	v_add_u32_e32 v184, s62, v188
	ds_read_b128 v[180:183], v158
	ds_read_b128 v[200:203], v184
	v_add_u32_e32 v158, s63, v161
	s_add_u32 s56, s0, 0x4000
	v_add_u32_e32 v184, s63, v188
	ds_read_b128 v[204:207], v158
	ds_read_b128 v[208:211], v184
	s_addc_u32 s57, s1, 0
	s_cmp_eq_u32 s95, 12
	s_cselect_b32 s60, s23, s56
	s_cselect_b32 s61, s3, s57
	s_cselect_b32 s58, s47, s74
	s_cselect_b32 s59, s45, s94
	s_add_u32 s56, s60, 0x4000
	s_addc_u32 s57, s61, 0
	v_lshl_add_u64 v[184:185], s[0:1], 0, v[176:177]
	s_add_i32 m0, s55, 0xc000
	ds_read_b128 v[212:215], v193
	ds_read_b128 v[216:219], v193 offset:2048
	ds_read_b128 v[220:223], v194
	ds_read_b128 v[224:227], v194 offset:2048
	ds_read_b128 v[228:231], v193 offset:4096
	ds_read_b128 v[232:235], v193 offset:6144
	ds_read_b128 v[236:239], v194 offset:4096
	ds_read_b128 v[240:243], v194 offset:6144
	global_load_lds_dwordx4 v[184:185], off
	v_lshl_add_u64 v[184:185], s[0:1], 0, v[178:179]
	s_add_i32 m0, s55, 0xe000
	s_nop 0
	global_load_lds_dwordx4 v[184:185], off
	s_waitcnt vmcnt(8)
	s_waitcnt lgkmcnt(0)
	s_barrier
	s_setprio 1
	s_waitcnt lgkmcnt(0)
	v_mfma_f32_16x16x32_bf16 v[126:129], v[130:133], v[212:215], v[126:129]
	v_mfma_f32_16x16x32_bf16 v[122:125], v[138:141], v[212:215], v[122:125]
	v_mfma_f32_16x16x32_bf16 v[94:97], v[130:133], v[216:219], v[94:97]
	v_mfma_f32_16x16x32_bf16 v[90:93], v[138:141], v[216:219], v[90:93]
	v_mfma_f32_16x16x32_bf16 v[62:65], v[130:133], v[228:231], v[62:65]
	v_mfma_f32_16x16x32_bf16 v[58:61], v[138:141], v[228:231], v[58:61]
	v_mfma_f32_16x16x32_bf16 v[30:33], v[130:133], v[232:235], v[30:33]
	v_mfma_f32_16x16x32_bf16 v[26:29], v[138:141], v[232:235], v[26:29]
	v_mfma_f32_16x16x32_bf16 v[126:129], v[134:137], v[220:223], v[126:129]
	v_mfma_f32_16x16x32_bf16 v[122:125], v[142:145], v[220:223], v[122:125]
	v_mfma_f32_16x16x32_bf16 v[94:97], v[134:137], v[224:227], v[94:97]
	v_mfma_f32_16x16x32_bf16 v[90:93], v[142:145], v[224:227], v[90:93]
	v_mfma_f32_16x16x32_bf16 v[62:65], v[134:137], v[236:239], v[62:65]
	v_mfma_f32_16x16x32_bf16 v[58:61], v[142:145], v[236:239], v[58:61]
	v_mfma_f32_16x16x32_bf16 v[30:33], v[134:137], v[240:243], v[30:33]
	v_mfma_f32_16x16x32_bf16 v[26:29], v[142:145], v[240:243], v[26:29]
	v_mfma_f32_16x16x32_bf16 v[110:113], v[180:183], v[212:215], v[110:113]
	v_mfma_f32_16x16x32_bf16 v[106:109], v[204:207], v[212:215], v[106:109]
	v_mfma_f32_16x16x32_bf16 v[78:81], v[180:183], v[216:219], v[78:81]
	v_mfma_f32_16x16x32_bf16 v[74:77], v[204:207], v[216:219], v[74:77]
	v_mfma_f32_16x16x32_bf16 v[46:49], v[180:183], v[228:231], v[46:49]
	v_mfma_f32_16x16x32_bf16 v[42:45], v[204:207], v[228:231], v[42:45]
	v_mfma_f32_16x16x32_bf16 v[14:17], v[180:183], v[232:235], v[14:17]
	v_mfma_f32_16x16x32_bf16 v[10:13], v[204:207], v[232:235], v[10:13]
	v_mfma_f32_16x16x32_bf16 v[110:113], v[200:203], v[220:223], v[110:113]
	v_mfma_f32_16x16x32_bf16 v[106:109], v[208:211], v[220:223], v[106:109]
	v_mfma_f32_16x16x32_bf16 v[78:81], v[200:203], v[224:227], v[78:81]
	v_mfma_f32_16x16x32_bf16 v[74:77], v[208:211], v[224:227], v[74:77]
	v_mfma_f32_16x16x32_bf16 v[46:49], v[200:203], v[236:239], v[46:49]
	v_mfma_f32_16x16x32_bf16 v[42:45], v[208:211], v[236:239], v[42:45]
	v_mfma_f32_16x16x32_bf16 v[14:17], v[200:203], v[240:243], v[14:17]
	v_mfma_f32_16x16x32_bf16 v[10:13], v[208:211], v[240:243], v[10:13]
	s_setprio 0
	s_barrier
	s_setprio 3
	s_add_i32 vcc_lo, s92, s64
	v_lshl_add_u64 v[184:185], s[58:59], 0, v[146:147]
	s_mov_b32 m0, vcc_lo
	ds_read_b128 v[212:215], v193 offset:16384
	ds_read_b128 v[216:219], v193 offset:18432
	ds_read_b128 v[220:223], v194 offset:16384
	ds_read_b128 v[224:227], v194 offset:18432
	ds_read_b128 v[228:231], v193 offset:20480
	ds_read_b128 v[232:235], v193 offset:22528
	ds_read_b128 v[236:239], v194 offset:20480
	ds_read_b128 v[240:243], v194 offset:22528
	global_load_lds_dwordx4 v[184:185], off
	s_add_i32 m0, vcc_lo, 0x2000
	s_add_u32 vcc_lo, s58, 0x40000
	v_lshl_add_u64 v[196:197], s[58:59], 0, v[148:149]
	s_addc_u32 vcc_hi, s59, 0
	s_add_i32 s18, s62, s64
	global_load_lds_dwordx4 v[196:197], off
	v_lshl_add_u64 v[244:245], vcc, 0, v[146:147]
	s_mov_b32 m0, s18
	s_nop 0
	global_load_lds_dwordx4 v[244:245], off
	v_lshl_add_u64 v[244:245], vcc, 0, v[148:149]
	s_add_i32 m0, s18, 0x2000
	s_nop 0
	global_load_lds_dwordx4 v[244:245], off
	v_lshl_add_u64 v[244:245], s[60:61], 0, v[150:151]
	s_mov_b32 m0, s55
	s_nop 0
	global_load_lds_dwordx4 v[244:245], off
	v_lshl_add_u64 v[244:245], s[60:61], 0, v[152:153]
	s_mov_b32 m0, s65
	s_nop 0
	global_load_lds_dwordx4 v[244:245], off
	s_waitcnt vmcnt(8)
	s_waitcnt lgkmcnt(0)
	s_barrier
; #define PG8_STAGE(bufoff, gbase, voff) do { _Pragma("unroll") for (int _i = 0; _i < 2; ++_i) \
;         __builtin_amdgcn_global_load_lds((const unsigned*)((const char*)(gbase) + (voff)[_i]), (LAS unsigned*)(lds + (bufoff) + ldsw + _i * 8192), 16, 0, 0); } while (0)
; #define PG8_LDA(dst, b, h) do { _Pragma("unroll") for (int m = 0; m < 4; ++m) _Pragma("unroll") for (int k = 0; k < 2; ++k) dst[m][k] = *(const LAS bf16x8*)(lds + PG8_SA(b, h) + ((aoff ^ (k * 64)) + m * 2048)); } while (0)
; #define PG8_LDB(dst, b, h) do { _Pragma("unroll") for (int n = 0; n < 2; ++n) _Pragma("unroll") for (int k = 0; k < 2; ++k) dst[n][k] = *(const LAS bf16x8*)(lds + PG8_SB(b, h) + ((boff ^ (k * 64)) + n * 2048)); } while (0)
; #define PG8_MMA(ai, bj, At, Bt) do { __builtin_amdgcn_s_setprio(1); _Pragma("unroll") for (int m = 0; m < 4; ++m) _Pragma("unroll") for (int n = 0; n < 2; ++n) _Pragma("unroll") for (int k = 0; k < 2; ++k) \
;         acc[ai][bj][m][n] = __builtin_amdgcn_mfma_f32_16x16x32_bf16(Bt[n][k], At[m][k], acc[ai][bj][m][n], 0, 0, 0); __builtin_amdgcn_s_setprio(0); } while (0)
; #define PG8_WAIT_V(n) asm volatile("s_waitcnt vmcnt(" #n ")" ::: "memory")
; #define PG8_WAIT_L(n) asm volatile("s_waitcnt lgkmcnt(" #n ")" ::: "memory")
; #define PG8_BAR __builtin_amdgcn_s_barrier()
; #define PG8_SCHED __builtin_amdgcn_sched_barrier(0)
;     ...
;             PG8_WAIT_V(8); PG8_WAIT_L(0); PG8_BAR; if (do1) { PG8_MMA(1, 0, At, B0); PG8_MMA(1, 1, At, B1); } PG8_BAR; PG8_SCHED;
;             PG8_LDB(B0, 1, 0); PG8_LDB(B1, 1, 1); PG8_SCHED; PG8_LDA(At, 1, 0); PG8_STAGE(PG8_SA(0, 1), a2, vs[1]);
;             PG8_WAIT_V(8); PG8_WAIT_L(0); PG8_BAR; if (do0) { PG8_MMA(0, 0, At, B0); PG8_MMA(0, 1, At, B1); } PG8_BAR; PG8_SCHED;
	s_setprio 1
	s_waitcnt lgkmcnt(0)
	v_mfma_f32_16x16x32_bf16 v[118:121], v[130:133], v[212:215], v[118:121]
	v_mfma_f32_16x16x32_bf16 v[114:117], v[138:141], v[212:215], v[114:117]
	v_mfma_f32_16x16x32_bf16 v[86:89], v[130:133], v[216:219], v[86:89]
	v_mfma_f32_16x16x32_bf16 v[82:85], v[138:141], v[216:219], v[82:85]
	v_mfma_f32_16x16x32_bf16 v[54:57], v[130:133], v[228:231], v[54:57]
	v_mfma_f32_16x16x32_bf16 v[50:53], v[138:141], v[228:231], v[50:53]
	v_mfma_f32_16x16x32_bf16 v[22:25], v[130:133], v[232:235], v[22:25]
	v_mfma_f32_16x16x32_bf16 v[18:21], v[138:141], v[232:235], v[18:21]
	v_mfma_f32_16x16x32_bf16 v[118:121], v[134:137], v[220:223], v[118:121]
	v_mfma_f32_16x16x32_bf16 v[114:117], v[142:145], v[220:223], v[114:117]
	v_mfma_f32_16x16x32_bf16 v[86:89], v[134:137], v[224:227], v[86:89]
	v_mfma_f32_16x16x32_bf16 v[82:85], v[142:145], v[224:227], v[82:85]
	v_mfma_f32_16x16x32_bf16 v[54:57], v[134:137], v[236:239], v[54:57]
	v_mfma_f32_16x16x32_bf16 v[50:53], v[142:145], v[236:239], v[50:53]
	v_mfma_f32_16x16x32_bf16 v[22:25], v[134:137], v[240:243], v[22:25]
	v_mfma_f32_16x16x32_bf16 v[18:21], v[142:145], v[240:243], v[18:21]
	v_mfma_f32_16x16x32_bf16 v[102:105], v[180:183], v[212:215], v[102:105]
	v_mfma_f32_16x16x32_bf16 v[98:101], v[204:207], v[212:215], v[98:101]
	v_mfma_f32_16x16x32_bf16 v[70:73], v[180:183], v[216:219], v[70:73]
	v_mfma_f32_16x16x32_bf16 v[66:69], v[204:207], v[216:219], v[66:69]
	v_mfma_f32_16x16x32_bf16 v[38:41], v[180:183], v[228:231], v[38:41]
	v_mfma_f32_16x16x32_bf16 v[34:37], v[204:207], v[228:231], v[34:37]
	v_mfma_f32_16x16x32_bf16 v[6:9], v[180:183], v[232:235], v[6:9]
	v_mfma_f32_16x16x32_bf16 v[2:5], v[204:207], v[232:235], v[2:5]
	v_mfma_f32_16x16x32_bf16 v[102:105], v[200:203], v[220:223], v[102:105]
	v_mfma_f32_16x16x32_bf16 v[98:101], v[208:211], v[220:223], v[98:101]
	v_mfma_f32_16x16x32_bf16 v[70:73], v[200:203], v[224:227], v[70:73]
	v_mfma_f32_16x16x32_bf16 v[66:69], v[208:211], v[224:227], v[66:69]
	v_mfma_f32_16x16x32_bf16 v[38:41], v[200:203], v[236:239], v[38:41]
	v_mfma_f32_16x16x32_bf16 v[34:37], v[208:211], v[236:239], v[34:37]
	v_mfma_f32_16x16x32_bf16 v[6:9], v[200:203], v[240:243], v[6:9]
	v_mfma_f32_16x16x32_bf16 v[2:5], v[208:211], v[240:243], v[2:5]
	s_setprio 0
	s_barrier
	s_setprio 3
	s_add_i32 s18, 0, 0x18000
	s_add_i32 s19, 0, 0x1c000
	v_add_u32_e32 v130, s18, v161
	v_add_u32_e32 v134, s18, v188
	v_add_u32_e32 v138, s72, v161
	v_add_u32_e32 v142, s72, v188
	v_add_u32_e32 v158, s19, v161
	ds_read_b128 v[130:133], v130
	ds_read_b128 v[134:137], v134
	ds_read_b128 v[138:141], v138
	ds_read_b128 v[142:145], v142
	v_add_u32_e32 v195, s19, v188
	ds_read_b128 v[180:183], v158
	ds_read_b128 v[200:203], v195
	v_add_u32_e32 v158, s73, v161
	v_add_u32_e32 v195, s73, v188
	ds_read_b128 v[204:207], v158
	ds_read_b128 v[208:211], v195
	s_mov_b32 m0, s66
	v_lshl_add_u64 v[244:245], s[60:61], 0, v[154:155]
	ds_read_b128 v[212:215], v193 offset:32768
	ds_read_b128 v[216:219], v193 offset:34816
	ds_read_b128 v[220:223], v194 offset:32768
	ds_read_b128 v[224:227], v194 offset:34816
	ds_read_b128 v[228:231], v193 offset:36864
	ds_read_b128 v[232:235], v193 offset:38912
	ds_read_b128 v[236:239], v194 offset:36864
	ds_read_b128 v[240:243], v194 offset:38912
	global_load_lds_dwordx4 v[244:245], off
	v_lshl_add_u64 v[244:245], s[60:61], 0, v[156:157]
	s_mov_b32 m0, s67
	s_nop 0
	global_load_lds_dwordx4 v[244:245], off
	s_waitcnt vmcnt(8)
	s_waitcnt lgkmcnt(0)
	s_barrier
	s_setprio 1
	s_waitcnt lgkmcnt(0)
	v_mfma_f32_16x16x32_bf16 v[126:129], v[130:133], v[212:215], v[126:129]
	v_mfma_f32_16x16x32_bf16 v[122:125], v[138:141], v[212:215], v[122:125]
	v_mfma_f32_16x16x32_bf16 v[94:97], v[130:133], v[216:219], v[94:97]
	v_mfma_f32_16x16x32_bf16 v[90:93], v[138:141], v[216:219], v[90:93]
	v_mfma_f32_16x16x32_bf16 v[62:65], v[130:133], v[228:231], v[62:65]
	v_mfma_f32_16x16x32_bf16 v[58:61], v[138:141], v[228:231], v[58:61]
	v_mfma_f32_16x16x32_bf16 v[30:33], v[130:133], v[232:235], v[30:33]
	v_mfma_f32_16x16x32_bf16 v[26:29], v[138:141], v[232:235], v[26:29]
	v_mfma_f32_16x16x32_bf16 v[126:129], v[134:137], v[220:223], v[126:129]
	v_mfma_f32_16x16x32_bf16 v[122:125], v[142:145], v[220:223], v[122:125]
	v_mfma_f32_16x16x32_bf16 v[94:97], v[134:137], v[224:227], v[94:97]
	v_mfma_f32_16x16x32_bf16 v[90:93], v[142:145], v[224:227], v[90:93]
	v_mfma_f32_16x16x32_bf16 v[62:65], v[134:137], v[236:239], v[62:65]
	v_mfma_f32_16x16x32_bf16 v[58:61], v[142:145], v[236:239], v[58:61]
	v_mfma_f32_16x16x32_bf16 v[30:33], v[134:137], v[240:243], v[30:33]
	v_mfma_f32_16x16x32_bf16 v[26:29], v[142:145], v[240:243], v[26:29]
	v_mfma_f32_16x16x32_bf16 v[110:113], v[180:183], v[212:215], v[110:113]
	v_mfma_f32_16x16x32_bf16 v[106:109], v[204:207], v[212:215], v[106:109]
	v_mfma_f32_16x16x32_bf16 v[78:81], v[180:183], v[216:219], v[78:81]
	v_mfma_f32_16x16x32_bf16 v[74:77], v[204:207], v[216:219], v[74:77]
	v_mfma_f32_16x16x32_bf16 v[46:49], v[180:183], v[228:231], v[46:49]
	v_mfma_f32_16x16x32_bf16 v[42:45], v[204:207], v[228:231], v[42:45]
	v_mfma_f32_16x16x32_bf16 v[14:17], v[180:183], v[232:235], v[14:17]
	v_mfma_f32_16x16x32_bf16 v[10:13], v[204:207], v[232:235], v[10:13]
	v_mfma_f32_16x16x32_bf16 v[110:113], v[200:203], v[220:223], v[110:113]
	v_mfma_f32_16x16x32_bf16 v[106:109], v[208:211], v[220:223], v[106:109]
	v_mfma_f32_16x16x32_bf16 v[78:81], v[200:203], v[224:227], v[78:81]
	v_mfma_f32_16x16x32_bf16 v[74:77], v[208:211], v[224:227], v[74:77]
	v_mfma_f32_16x16x32_bf16 v[46:49], v[200:203], v[236:239], v[46:49]
	v_mfma_f32_16x16x32_bf16 v[42:45], v[208:211], v[236:239], v[42:45]
	v_mfma_f32_16x16x32_bf16 v[14:17], v[200:203], v[240:243], v[14:17]
	v_mfma_f32_16x16x32_bf16 v[10:13], v[208:211], v[240:243], v[10:13]
	s_setprio 0
	s_barrier
; #define PG8_STAGE(bufoff, gbase, voff) do { _Pragma("unroll") for (int _i = 0; _i < 2; ++_i) \
;         __builtin_amdgcn_global_load_lds((const unsigned*)((const char*)(gbase) + (voff)[_i]), (LAS unsigned*)(lds + (bufoff) + ldsw + _i * 8192), 16, 0, 0); } while (0)
; #define PG8_LDA(dst, b, h) do { _Pragma("unroll") for (int m = 0; m < 4; ++m) _Pragma("unroll") for (int k = 0; k < 2; ++k) dst[m][k] = *(const LAS bf16x8*)(lds + PG8_SA(b, h) + ((aoff ^ (k * 64)) + m * 2048)); } while (0)
; #define PG8_MMA(ai, bj, At, Bt) do { __builtin_amdgcn_s_setprio(1); _Pragma("unroll") for (int m = 0; m < 4; ++m) _Pragma("unroll") for (int n = 0; n < 2; ++n) _Pragma("unroll") for (int k = 0; k < 2; ++k) \
;         acc[ai][bj][m][n] = __builtin_amdgcn_mfma_f32_16x16x32_bf16(Bt[n][k], At[m][k], acc[ai][bj][m][n], 0, 0, 0); __builtin_amdgcn_s_setprio(0); } while (0)
; #define PG8_WAIT_V(n) asm volatile("s_waitcnt vmcnt(" #n ")" ::: "memory")
; #define PG8_WAIT_L(n) asm volatile("s_waitcnt lgkmcnt(" #n ")" ::: "memory")
; #define PG8_BAR __builtin_amdgcn_s_barrier()
; #define PG8_SCHED __builtin_amdgcn_sched_barrier(0)
;     ...
;             PG8_LDA(At, 1, 1); PG8_STAGE(PG8_SB(1, 0), b3, voffB); PG8_STAGE(PG8_SB(1, 1), b3 + hstep, voffB); PG8_STAGE(PG8_SA(1, 0), a3, vs[0]);
;             PG8_WAIT_V(8); PG8_WAIT_L(0); PG8_BAR; if (do1) { PG8_MMA(1, 0, At, B0); PG8_MMA(1, 1, At, B1); } PG8_BAR; PG8_SCHED;
;         }
;         if (wr == 0) PG8_BAR;
	s_setprio 3
	s_add_i32 s18, s18, s64
	v_lshl_add_u64 v[184:185], v[184:185], 0, s[10:11]
	s_mov_b32 m0, s18
	ds_read_b128 v[212:215], v193 offset:49152
	ds_read_b128 v[216:219], v193 offset:51200
	ds_read_b128 v[220:223], v194 offset:49152
	ds_read_b128 v[224:227], v194 offset:51200
	ds_read_b128 v[228:231], v193 offset:53248
	ds_read_b128 v[232:235], v193 offset:55296
	ds_read_b128 v[236:239], v194 offset:53248
	ds_read_b128 v[240:243], v194 offset:55296
	global_load_lds_dwordx4 v[184:185], off
	s_add_i32 m0, s18, 0x2000
	s_add_u32 s58, s58, 0x40080
	v_lshl_add_u64 v[184:185], v[196:197], 0, s[10:11]
	s_addc_u32 s59, s59, 0
	s_add_i32 s18, s19, s64
	global_load_lds_dwordx4 v[184:185], off
	v_lshl_add_u64 v[184:185], s[58:59], 0, v[146:147]
	s_mov_b32 m0, s18
	s_nop 0
	global_load_lds_dwordx4 v[184:185], off
	v_lshl_add_u64 v[184:185], s[58:59], 0, v[148:149]
	s_add_i32 m0, s18, 0x2000
	s_nop 0
	global_load_lds_dwordx4 v[184:185], off
	v_lshl_add_u64 v[184:185], s[56:57], 0, v[150:151]
	s_mov_b32 m0, s70
	s_nop 0
	global_load_lds_dwordx4 v[184:185], off
	v_lshl_add_u64 v[184:185], s[56:57], 0, v[152:153]
	s_mov_b32 m0, s71
	s_nop 0
	global_load_lds_dwordx4 v[184:185], off
	s_waitcnt vmcnt(8)
	s_waitcnt lgkmcnt(0)
	s_barrier
	s_setprio 1
	s_waitcnt lgkmcnt(0)
	v_mfma_f32_16x16x32_bf16 v[118:121], v[130:133], v[212:215], v[118:121]
	v_mfma_f32_16x16x32_bf16 v[114:117], v[138:141], v[212:215], v[114:117]
	v_mfma_f32_16x16x32_bf16 v[86:89], v[130:133], v[216:219], v[86:89]
	v_mfma_f32_16x16x32_bf16 v[82:85], v[138:141], v[216:219], v[82:85]
	v_mfma_f32_16x16x32_bf16 v[54:57], v[130:133], v[228:231], v[54:57]
	v_mfma_f32_16x16x32_bf16 v[50:53], v[138:141], v[228:231], v[50:53]
	v_mfma_f32_16x16x32_bf16 v[22:25], v[130:133], v[232:235], v[22:25]
	v_mfma_f32_16x16x32_bf16 v[18:21], v[138:141], v[232:235], v[18:21]
	v_mfma_f32_16x16x32_bf16 v[118:121], v[134:137], v[220:223], v[118:121]
	v_mfma_f32_16x16x32_bf16 v[114:117], v[142:145], v[220:223], v[114:117]
	v_mfma_f32_16x16x32_bf16 v[86:89], v[134:137], v[224:227], v[86:89]
	v_mfma_f32_16x16x32_bf16 v[82:85], v[142:145], v[224:227], v[82:85]
	v_mfma_f32_16x16x32_bf16 v[54:57], v[134:137], v[236:239], v[54:57]
	v_mfma_f32_16x16x32_bf16 v[50:53], v[142:145], v[236:239], v[50:53]
	v_mfma_f32_16x16x32_bf16 v[22:25], v[134:137], v[240:243], v[22:25]
	v_mfma_f32_16x16x32_bf16 v[18:21], v[142:145], v[240:243], v[18:21]
	v_mfma_f32_16x16x32_bf16 v[102:105], v[180:183], v[212:215], v[102:105]
	v_mfma_f32_16x16x32_bf16 v[98:101], v[204:207], v[212:215], v[98:101]
	v_mfma_f32_16x16x32_bf16 v[70:73], v[180:183], v[216:219], v[70:73]
	v_mfma_f32_16x16x32_bf16 v[66:69], v[204:207], v[216:219], v[66:69]
	v_mfma_f32_16x16x32_bf16 v[38:41], v[180:183], v[228:231], v[38:41]
	v_mfma_f32_16x16x32_bf16 v[34:37], v[204:207], v[228:231], v[34:37]
	v_mfma_f32_16x16x32_bf16 v[6:9], v[180:183], v[232:235], v[6:9]
	v_mfma_f32_16x16x32_bf16 v[2:5], v[204:207], v[232:235], v[2:5]
	v_mfma_f32_16x16x32_bf16 v[102:105], v[200:203], v[220:223], v[102:105]
	v_mfma_f32_16x16x32_bf16 v[98:101], v[208:211], v[220:223], v[98:101]
	v_mfma_f32_16x16x32_bf16 v[70:73], v[200:203], v[224:227], v[70:73]
	v_mfma_f32_16x16x32_bf16 v[66:69], v[208:211], v[224:227], v[66:69]
	v_mfma_f32_16x16x32_bf16 v[38:41], v[200:203], v[236:239], v[38:41]
	v_mfma_f32_16x16x32_bf16 v[34:37], v[208:211], v[236:239], v[34:37]
	v_mfma_f32_16x16x32_bf16 v[6:9], v[200:203], v[240:243], v[6:9]
	v_mfma_f32_16x16x32_bf16 v[2:5], v[208:211], v[240:243], v[2:5]
	s_setprio 0
	s_barrier
	s_setprio 3
	s_add_i32 s95, s95, 2
	s_add_u32 s74, s74, 0x100
	s_addc_u32 s94, s94, 0
	s_add_u32 s0, s0, 0x8000
	s_addc_u32 s1, s1, 0
	s_cmp_gt_u32 s95, 13
	s_cbranch_scc0 .LBB0_1343
	s_and_b64 vcc, exec, s[12:13]
	s_cbranch_vccz .LBB0_1346
	s_barrier

; #define PG8_STAGE(bufoff, gbase, voff) do { _Pragma("unroll") for (int _i = 0; _i < 2; ++_i) \
;         __builtin_amdgcn_global_load_lds((const unsigned*)((const char*)(gbase) + (voff)[_i]), (LAS unsigned*)(lds + (bufoff) + ldsw + _i * 8192), 16, 0, 0); } while (0)
; #define PG8_LDA(dst, b, h) do { _Pragma("unroll") for (int m = 0; m < 4; ++m) _Pragma("unroll") for (int k = 0; k < 2; ++k) dst[m][k] = *(const LAS bf16x8*)(lds + PG8_SA(b, h) + ((aoff ^ (k * 64)) + m * 2048)); } while (0)
; #define PG8_LDB(dst, b, h) do { _Pragma("unroll") for (int n = 0; n < 2; ++n) _Pragma("unroll") for (int k = 0; k < 2; ++k) dst[n][k] = *(const LAS bf16x8*)(lds + PG8_SB(b, h) + ((boff ^ (k * 64)) + n * 2048)); } while (0)
; #define PG8_WAIT_V(n) asm volatile("s_waitcnt vmcnt(" #n ")" ::: "memory")
; #define PG8_BAR __builtin_amdgcn_s_barrier()
;     ...
;         for (int t = 0; t < nt; t += 2) {
;             const bool last = (t == nt - 2);
;             const char* a1 = cA + (size_t)(t + 1) * kstepA;
;             const char* a2 = last ? nA : cA + (size_t)(t + 2) * kstepA; const char* b2 = last ? nB : cB + (size_t)(t + 2) * kstepB;
;             const char* a3 = a2 + kstepA; const char* b3 = b2 + kstepB;
;             unsigned vs[2][2];
;             if constexpr (GATHER) {
;                 if (last && has_next) {
; #pragma unroll
;                     for (int hh = 0; hh < 2; ++hh)
; #pragma unroll
;                         for (int i = 0; i < 2; ++i) voffN[hh][i] = (unsigned)idxl[(ui + 1) * 256 + hh * HALF + sR[i]] * (unsigned)(K * 2) + (unsigned)sC[i] * 2u;
;                 }
; #pragma unroll
;                 for (int hh = 0; hh < 2; ++hh)
; #pragma unroll
;                     for (int i = 0; i < 2; ++i) vs[hh][i] = last ? voffN[hh][i] : voffA[hh][i];
;             } else {
; #pragma unroll
;                 for (int hh = 0; hh < 2; ++hh)
; #pragma unroll
;                     for (int i = 0; i < 2; ++i) vs[hh][i] = voffA[hh][i];
;             }
;             PG8_LDB(B0, 0, 0); PG8_LDB(B1, 0, 1); PG8_SCHED; PG8_LDA(At, 0, 0); PG8_STAGE(PG8_SA(1, 1), a1, voffA[1]);
;             PG8_WAIT_V(8); PG8_WAIT_L(0); PG8_BAR; if (do0) { PG8_MMA(0, 0, At, B0); PG8_MMA(0, 1, At, B1); } PG8_BAR; PG8_SCHED;
;             PG8_LDA(At, 0, 1); PG8_STAGE(PG8_SB(0, 0), b2, voffB); PG8_STAGE(PG8_SB(0, 1), b2 + hstep, voffB); PG8_STAGE(PG8_SA(0, 0), a2, vs[0]);
.LBB0_1498:
	v_add_u32_e32 v130, s70, v153
	v_add_u32_e32 v134, s70, v184
	v_add_u32_e32 v150, s71, v153
	v_add_u32_e32 v176, s71, v184
	ds_read_b128 v[130:133], v130
	ds_read_b128 v[134:137], v134
	ds_read_b128 v[172:175], v150
	ds_read_b128 v[176:179], v176
	v_add_u32_e32 v150, s92, v153
	v_add_u32_e32 v180, s92, v184
	ds_read_b128 v[192:195], v150
	ds_read_b128 v[200:203], v180
	v_add_u32_e32 v150, s93, v153
	s_add_u32 s6, s0, 0x4000
	v_add_u32_e32 v180, s93, v184
	ds_read_b128 v[204:207], v150
	ds_read_b128 v[208:211], v180
	s_addc_u32 s7, s1, 0
	s_cmp_eq_u32 s63, 12
	s_cselect_b32 s58, s9, s6
	s_cselect_b32 s59, s3, s7
	s_cselect_b32 s56, s37, s49
	s_cselect_b32 s57, s23, s62
	s_add_u32 s6, s58, 0x4000
	s_addc_u32 s7, s59, 0
	v_lshl_add_u64 v[180:181], s[0:1], 0, v[168:169]
	s_add_i32 m0, s61, 0xc000
	ds_read_b128 v[212:215], v189
	ds_read_b128 v[216:219], v189 offset:2048
	ds_read_b128 v[220:223], v190
	ds_read_b128 v[224:227], v190 offset:2048
	ds_read_b128 v[228:231], v189 offset:4096
	ds_read_b128 v[232:235], v189 offset:6144
	ds_read_b128 v[236:239], v190 offset:4096
	ds_read_b128 v[240:243], v190 offset:6144
	global_load_lds_dwordx4 v[180:181], off
	v_lshl_add_u64 v[180:181], s[0:1], 0, v[170:171]
	s_add_i32 m0, s61, 0xe000
	s_nop 0
	global_load_lds_dwordx4 v[180:181], off
	s_waitcnt vmcnt(8)
	s_waitcnt lgkmcnt(0)
	s_barrier
	s_setprio 1
	s_waitcnt lgkmcnt(0)
	v_mfma_f32_16x16x32_bf16 v[126:129], v[130:133], v[212:215], v[126:129]
	v_mfma_f32_16x16x32_bf16 v[122:125], v[172:175], v[212:215], v[122:125]
	v_mfma_f32_16x16x32_bf16 v[94:97], v[130:133], v[216:219], v[94:97]
	v_mfma_f32_16x16x32_bf16 v[90:93], v[172:175], v[216:219], v[90:93]
	v_mfma_f32_16x16x32_bf16 v[62:65], v[130:133], v[228:231], v[62:65]
	v_mfma_f32_16x16x32_bf16 v[58:61], v[172:175], v[228:231], v[58:61]
	v_mfma_f32_16x16x32_bf16 v[30:33], v[130:133], v[232:235], v[30:33]
	v_mfma_f32_16x16x32_bf16 v[26:29], v[172:175], v[232:235], v[26:29]
	v_mfma_f32_16x16x32_bf16 v[126:129], v[134:137], v[220:223], v[126:129]
	v_mfma_f32_16x16x32_bf16 v[122:125], v[176:179], v[220:223], v[122:125]
	v_mfma_f32_16x16x32_bf16 v[94:97], v[134:137], v[224:227], v[94:97]
	v_mfma_f32_16x16x32_bf16 v[90:93], v[176:179], v[224:227], v[90:93]
	v_mfma_f32_16x16x32_bf16 v[62:65], v[134:137], v[236:239], v[62:65]
	v_mfma_f32_16x16x32_bf16 v[58:61], v[176:179], v[236:239], v[58:61]
	v_mfma_f32_16x16x32_bf16 v[30:33], v[134:137], v[240:243], v[30:33]
	v_mfma_f32_16x16x32_bf16 v[26:29], v[176:179], v[240:243], v[26:29]
	v_mfma_f32_16x16x32_bf16 v[110:113], v[192:195], v[212:215], v[110:113]
	v_mfma_f32_16x16x32_bf16 v[106:109], v[204:207], v[212:215], v[106:109]
	v_mfma_f32_16x16x32_bf16 v[78:81], v[192:195], v[216:219], v[78:81]
	v_mfma_f32_16x16x32_bf16 v[74:77], v[204:207], v[216:219], v[74:77]
	v_mfma_f32_16x16x32_bf16 v[46:49], v[192:195], v[228:231], v[46:49]
	v_mfma_f32_16x16x32_bf16 v[42:45], v[204:207], v[228:231], v[42:45]
	v_mfma_f32_16x16x32_bf16 v[14:17], v[192:195], v[232:235], v[14:17]
	v_mfma_f32_16x16x32_bf16 v[10:13], v[204:207], v[232:235], v[10:13]
	v_mfma_f32_16x16x32_bf16 v[110:113], v[200:203], v[220:223], v[110:113]
	v_mfma_f32_16x16x32_bf16 v[106:109], v[208:211], v[220:223], v[106:109]
	v_mfma_f32_16x16x32_bf16 v[78:81], v[200:203], v[224:227], v[78:81]
	v_mfma_f32_16x16x32_bf16 v[74:77], v[208:211], v[224:227], v[74:77]
	v_mfma_f32_16x16x32_bf16 v[46:49], v[200:203], v[236:239], v[46:49]
	v_mfma_f32_16x16x32_bf16 v[42:45], v[208:211], v[236:239], v[42:45]
	v_mfma_f32_16x16x32_bf16 v[14:17], v[200:203], v[240:243], v[14:17]
	v_mfma_f32_16x16x32_bf16 v[10:13], v[208:211], v[240:243], v[10:13]
	s_setprio 0
	s_barrier
	s_setprio 3
	s_add_i32 s18, s70, s60
	v_lshl_add_u64 v[180:181], s[56:57], 0, v[138:139]
	s_mov_b32 m0, s18
	ds_read_b128 v[212:215], v189 offset:16384
	ds_read_b128 v[216:219], v189 offset:18432
	ds_read_b128 v[220:223], v190 offset:16384
	ds_read_b128 v[224:227], v190 offset:18432
	ds_read_b128 v[228:231], v189 offset:20480
	ds_read_b128 v[232:235], v189 offset:22528
	ds_read_b128 v[236:239], v190 offset:20480
	ds_read_b128 v[240:243], v190 offset:22528
	global_load_lds_dwordx4 v[180:181], off
	s_add_i32 m0, s18, 0x2000
	s_add_u32 s72, s56, 0x40000
	v_lshl_add_u64 v[196:197], s[56:57], 0, v[140:141]
	s_addc_u32 s73, s57, 0
	s_add_i32 s18, s92, s60
	global_load_lds_dwordx4 v[196:197], off
	v_lshl_add_u64 v[244:245], s[72:73], 0, v[138:139]
	s_mov_b32 m0, s18
	s_nop 0
	global_load_lds_dwordx4 v[244:245], off
	v_lshl_add_u64 v[244:245], s[72:73], 0, v[140:141]
	s_add_i32 m0, s18, 0x2000
	s_nop 0
	global_load_lds_dwordx4 v[244:245], off
	v_lshl_add_u64 v[244:245], s[58:59], 0, v[142:143]
	s_mov_b32 m0, s61
	s_nop 0
	global_load_lds_dwordx4 v[244:245], off
	v_lshl_add_u64 v[244:245], s[58:59], 0, v[144:145]
	s_mov_b32 m0, s64
	s_nop 0
	global_load_lds_dwordx4 v[244:245], off
	s_waitcnt vmcnt(8)
	s_waitcnt lgkmcnt(0)
	s_barrier
; #define PG8_STAGE(bufoff, gbase, voff) do { _Pragma("unroll") for (int _i = 0; _i < 2; ++_i) \
;         __builtin_amdgcn_global_load_lds((const unsigned*)((const char*)(gbase) + (voff)[_i]), (LAS unsigned*)(lds + (bufoff) + ldsw + _i * 8192), 16, 0, 0); } while (0)
; #define PG8_LDA(dst, b, h) do { _Pragma("unroll") for (int m = 0; m < 4; ++m) _Pragma("unroll") for (int k = 0; k < 2; ++k) dst[m][k] = *(const LAS bf16x8*)(lds + PG8_SA(b, h) + ((aoff ^ (k * 64)) + m * 2048)); } while (0)
; #define PG8_LDB(dst, b, h) do { _Pragma("unroll") for (int n = 0; n < 2; ++n) _Pragma("unroll") for (int k = 0; k < 2; ++k) dst[n][k] = *(const LAS bf16x8*)(lds + PG8_SB(b, h) + ((boff ^ (k * 64)) + n * 2048)); } while (0)
; #define PG8_MMA(ai, bj, At, Bt) do { __builtin_amdgcn_s_setprio(1); _Pragma("unroll") for (int m = 0; m < 4; ++m) _Pragma("unroll") for (int n = 0; n < 2; ++n) _Pragma("unroll") for (int k = 0; k < 2; ++k) \
;         acc[ai][bj][m][n] = __builtin_amdgcn_mfma_f32_16x16x32_bf16(Bt[n][k], At[m][k], acc[ai][bj][m][n], 0, 0, 0); __builtin_amdgcn_s_setprio(0); } while (0)
; #define PG8_WAIT_V(n) asm volatile("s_waitcnt vmcnt(" #n ")" ::: "memory")
; #define PG8_WAIT_L(n) asm volatile("s_waitcnt lgkmcnt(" #n ")" ::: "memory")
; #define PG8_BAR __builtin_amdgcn_s_barrier()
; #define PG8_SCHED __builtin_amdgcn_sched_barrier(0)
;     ...
;             PG8_WAIT_V(8); PG8_WAIT_L(0); PG8_BAR; if (do1) { PG8_MMA(1, 0, At, B0); PG8_MMA(1, 1, At, B1); } PG8_BAR; PG8_SCHED;
;             PG8_LDB(B0, 1, 0); PG8_LDB(B1, 1, 1); PG8_SCHED; PG8_LDA(At, 1, 0); PG8_STAGE(PG8_SA(0, 1), a2, vs[1]);
;             PG8_WAIT_V(8); PG8_WAIT_L(0); PG8_BAR; if (do0) { PG8_MMA(0, 0, At, B0); PG8_MMA(0, 1, At, B1); } PG8_BAR; PG8_SCHED;
	s_setprio 1
	s_waitcnt lgkmcnt(0)
	v_mfma_f32_16x16x32_bf16 v[118:121], v[130:133], v[212:215], v[118:121]
	v_mfma_f32_16x16x32_bf16 v[114:117], v[172:175], v[212:215], v[114:117]
	v_mfma_f32_16x16x32_bf16 v[86:89], v[130:133], v[216:219], v[86:89]
	v_mfma_f32_16x16x32_bf16 v[82:85], v[172:175], v[216:219], v[82:85]
	v_mfma_f32_16x16x32_bf16 v[54:57], v[130:133], v[228:231], v[54:57]
	v_mfma_f32_16x16x32_bf16 v[50:53], v[172:175], v[228:231], v[50:53]
	v_mfma_f32_16x16x32_bf16 v[22:25], v[130:133], v[232:235], v[22:25]
	v_mfma_f32_16x16x32_bf16 v[18:21], v[172:175], v[232:235], v[18:21]
	v_mfma_f32_16x16x32_bf16 v[118:121], v[134:137], v[220:223], v[118:121]
	v_mfma_f32_16x16x32_bf16 v[114:117], v[176:179], v[220:223], v[114:117]
	v_mfma_f32_16x16x32_bf16 v[86:89], v[134:137], v[224:227], v[86:89]
	v_mfma_f32_16x16x32_bf16 v[82:85], v[176:179], v[224:227], v[82:85]
	v_mfma_f32_16x16x32_bf16 v[54:57], v[134:137], v[236:239], v[54:57]
	v_mfma_f32_16x16x32_bf16 v[50:53], v[176:179], v[236:239], v[50:53]
	v_mfma_f32_16x16x32_bf16 v[22:25], v[134:137], v[240:243], v[22:25]
	v_mfma_f32_16x16x32_bf16 v[18:21], v[176:179], v[240:243], v[18:21]
	v_mfma_f32_16x16x32_bf16 v[102:105], v[192:195], v[212:215], v[102:105]
	v_mfma_f32_16x16x32_bf16 v[98:101], v[204:207], v[212:215], v[98:101]
	v_mfma_f32_16x16x32_bf16 v[70:73], v[192:195], v[216:219], v[70:73]
	v_mfma_f32_16x16x32_bf16 v[66:69], v[204:207], v[216:219], v[66:69]
	v_mfma_f32_16x16x32_bf16 v[38:41], v[192:195], v[228:231], v[38:41]
	v_mfma_f32_16x16x32_bf16 v[34:37], v[204:207], v[228:231], v[34:37]
	v_mfma_f32_16x16x32_bf16 v[6:9], v[192:195], v[232:235], v[6:9]
	v_mfma_f32_16x16x32_bf16 v[2:5], v[204:207], v[232:235], v[2:5]
	v_mfma_f32_16x16x32_bf16 v[102:105], v[200:203], v[220:223], v[102:105]
	v_mfma_f32_16x16x32_bf16 v[98:101], v[208:211], v[220:223], v[98:101]
	v_mfma_f32_16x16x32_bf16 v[70:73], v[200:203], v[224:227], v[70:73]
	v_mfma_f32_16x16x32_bf16 v[66:69], v[208:211], v[224:227], v[66:69]
	v_mfma_f32_16x16x32_bf16 v[38:41], v[200:203], v[236:239], v[38:41]
	v_mfma_f32_16x16x32_bf16 v[34:37], v[208:211], v[236:239], v[34:37]
	v_mfma_f32_16x16x32_bf16 v[6:9], v[200:203], v[240:243], v[6:9]
	v_mfma_f32_16x16x32_bf16 v[2:5], v[208:211], v[240:243], v[2:5]
	s_setprio 0
	s_barrier
	s_setprio 3
	s_add_i32 s18, 0, 0x18000
	v_add_u32_e32 v130, s18, v153
	v_add_u32_e32 v134, s18, v184
	v_add_u32_e32 v150, s12, v153
	v_add_u32_e32 v176, s12, v184
	s_add_i32 s19, 0, 0x1c000
	ds_read_b128 v[130:133], v130
	ds_read_b128 v[134:137], v134
	ds_read_b128 v[172:175], v150
	ds_read_b128 v[176:179], v176
	v_add_u32_e32 v150, s19, v153
	v_add_u32_e32 v191, s19, v184
	ds_read_b128 v[192:195], v150
	ds_read_b128 v[200:203], v191
	v_add_u32_e32 v150, s13, v153
	v_add_u32_e32 v191, s13, v184
	ds_read_b128 v[204:207], v150
	ds_read_b128 v[208:211], v191
	s_mov_b32 m0, s65
	v_lshl_add_u64 v[244:245], s[58:59], 0, v[146:147]
	ds_read_b128 v[212:215], v189 offset:32768
	ds_read_b128 v[216:219], v189 offset:34816
	ds_read_b128 v[220:223], v190 offset:32768
	ds_read_b128 v[224:227], v190 offset:34816
	ds_read_b128 v[228:231], v189 offset:36864
	ds_read_b128 v[232:235], v189 offset:38912
	ds_read_b128 v[236:239], v190 offset:36864
	ds_read_b128 v[240:243], v190 offset:38912
	global_load_lds_dwordx4 v[244:245], off
	v_lshl_add_u64 v[244:245], s[58:59], 0, v[148:149]
	s_mov_b32 m0, s66
	s_nop 0
	global_load_lds_dwordx4 v[244:245], off
	s_waitcnt vmcnt(8)
	s_waitcnt lgkmcnt(0)
	s_barrier
	s_setprio 1
	s_waitcnt lgkmcnt(0)
	v_mfma_f32_16x16x32_bf16 v[126:129], v[130:133], v[212:215], v[126:129]
	v_mfma_f32_16x16x32_bf16 v[122:125], v[172:175], v[212:215], v[122:125]
	v_mfma_f32_16x16x32_bf16 v[94:97], v[130:133], v[216:219], v[94:97]
	v_mfma_f32_16x16x32_bf16 v[90:93], v[172:175], v[216:219], v[90:93]
	v_mfma_f32_16x16x32_bf16 v[62:65], v[130:133], v[228:231], v[62:65]
	v_mfma_f32_16x16x32_bf16 v[58:61], v[172:175], v[228:231], v[58:61]
	v_mfma_f32_16x16x32_bf16 v[30:33], v[130:133], v[232:235], v[30:33]
	v_mfma_f32_16x16x32_bf16 v[26:29], v[172:175], v[232:235], v[26:29]
	v_mfma_f32_16x16x32_bf16 v[126:129], v[134:137], v[220:223], v[126:129]
	v_mfma_f32_16x16x32_bf16 v[122:125], v[176:179], v[220:223], v[122:125]
	v_mfma_f32_16x16x32_bf16 v[94:97], v[134:137], v[224:227], v[94:97]
	v_mfma_f32_16x16x32_bf16 v[90:93], v[176:179], v[224:227], v[90:93]
	v_mfma_f32_16x16x32_bf16 v[62:65], v[134:137], v[236:239], v[62:65]
	v_mfma_f32_16x16x32_bf16 v[58:61], v[176:179], v[236:239], v[58:61]
	v_mfma_f32_16x16x32_bf16 v[30:33], v[134:137], v[240:243], v[30:33]
	v_mfma_f32_16x16x32_bf16 v[26:29], v[176:179], v[240:243], v[26:29]
	v_mfma_f32_16x16x32_bf16 v[110:113], v[192:195], v[212:215], v[110:113]
	v_mfma_f32_16x16x32_bf16 v[106:109], v[204:207], v[212:215], v[106:109]
	v_mfma_f32_16x16x32_bf16 v[78:81], v[192:195], v[216:219], v[78:81]
	v_mfma_f32_16x16x32_bf16 v[74:77], v[204:207], v[216:219], v[74:77]
	v_mfma_f32_16x16x32_bf16 v[46:49], v[192:195], v[228:231], v[46:49]
	v_mfma_f32_16x16x32_bf16 v[42:45], v[204:207], v[228:231], v[42:45]
	v_mfma_f32_16x16x32_bf16 v[14:17], v[192:195], v[232:235], v[14:17]
	v_mfma_f32_16x16x32_bf16 v[10:13], v[204:207], v[232:235], v[10:13]
	v_mfma_f32_16x16x32_bf16 v[110:113], v[200:203], v[220:223], v[110:113]
	v_mfma_f32_16x16x32_bf16 v[106:109], v[208:211], v[220:223], v[106:109]
	v_mfma_f32_16x16x32_bf16 v[78:81], v[200:203], v[224:227], v[78:81]
	v_mfma_f32_16x16x32_bf16 v[74:77], v[208:211], v[224:227], v[74:77]
	v_mfma_f32_16x16x32_bf16 v[46:49], v[200:203], v[236:239], v[46:49]
	v_mfma_f32_16x16x32_bf16 v[42:45], v[208:211], v[236:239], v[42:45]
	v_mfma_f32_16x16x32_bf16 v[14:17], v[200:203], v[240:243], v[14:17]
	v_mfma_f32_16x16x32_bf16 v[10:13], v[208:211], v[240:243], v[10:13]
	s_setprio 0
	s_barrier
; #define PG8_STAGE(bufoff, gbase, voff) do { _Pragma("unroll") for (int _i = 0; _i < 2; ++_i) \
;         __builtin_amdgcn_global_load_lds((const unsigned*)((const char*)(gbase) + (voff)[_i]), (LAS unsigned*)(lds + (bufoff) + ldsw + _i * 8192), 16, 0, 0); } while (0)
; #define PG8_LDA(dst, b, h) do { _Pragma("unroll") for (int m = 0; m < 4; ++m) _Pragma("unroll") for (int k = 0; k < 2; ++k) dst[m][k] = *(const LAS bf16x8*)(lds + PG8_SA(b, h) + ((aoff ^ (k * 64)) + m * 2048)); } while (0)
; #define PG8_MMA(ai, bj, At, Bt) do { __builtin_amdgcn_s_setprio(1); _Pragma("unroll") for (int m = 0; m < 4; ++m) _Pragma("unroll") for (int n = 0; n < 2; ++n) _Pragma("unroll") for (int k = 0; k < 2; ++k) \
;         acc[ai][bj][m][n] = __builtin_amdgcn_mfma_f32_16x16x32_bf16(Bt[n][k], At[m][k], acc[ai][bj][m][n], 0, 0, 0); __builtin_amdgcn_s_setprio(0); } while (0)
; #define PG8_WAIT_V(n) asm volatile("s_waitcnt vmcnt(" #n ")" ::: "memory")
; #define PG8_WAIT_L(n) asm volatile("s_waitcnt lgkmcnt(" #n ")" ::: "memory")
; #define PG8_BAR __builtin_amdgcn_s_barrier()
; #define PG8_SCHED __builtin_amdgcn_sched_barrier(0)
;     ...
;             PG8_LDA(At, 1, 1); PG8_STAGE(PG8_SB(1, 0), b3, voffB); PG8_STAGE(PG8_SB(1, 1), b3 + hstep, voffB); PG8_STAGE(PG8_SA(1, 0), a3, vs[0]);
;             PG8_WAIT_V(8); PG8_WAIT_L(0); PG8_BAR; if (do1) { PG8_MMA(1, 0, At, B0); PG8_MMA(1, 1, At, B1); } PG8_BAR; PG8_SCHED;
;         }
;         if (wr == 0) PG8_BAR;
	s_setprio 3
	s_add_i32 s18, s18, s60
	v_lshl_add_u64 v[180:181], v[180:181], 0, s[24:25]
	s_mov_b32 m0, s18
	ds_read_b128 v[212:215], v189 offset:49152
	ds_read_b128 v[216:219], v189 offset:51200
	ds_read_b128 v[220:223], v190 offset:49152
	ds_read_b128 v[224:227], v190 offset:51200
	ds_read_b128 v[228:231], v189 offset:53248
	ds_read_b128 v[232:235], v189 offset:55296
	ds_read_b128 v[236:239], v190 offset:53248
	ds_read_b128 v[240:243], v190 offset:55296
	global_load_lds_dwordx4 v[180:181], off
	s_add_i32 m0, s18, 0x2000
	s_add_u32 s56, s56, 0x40080
	v_lshl_add_u64 v[180:181], v[196:197], 0, s[24:25]
	s_addc_u32 s57, s57, 0
	s_add_i32 s18, s19, s60
	global_load_lds_dwordx4 v[180:181], off
	v_lshl_add_u64 v[180:181], s[56:57], 0, v[138:139]
	s_mov_b32 m0, s18
	s_nop 0
	global_load_lds_dwordx4 v[180:181], off
	v_lshl_add_u64 v[180:181], s[56:57], 0, v[140:141]
	s_add_i32 m0, s18, 0x2000
	s_nop 0
	global_load_lds_dwordx4 v[180:181], off
	v_lshl_add_u64 v[180:181], s[6:7], 0, v[142:143]
	s_mov_b32 m0, s68
	s_nop 0
	global_load_lds_dwordx4 v[180:181], off
	v_lshl_add_u64 v[180:181], s[6:7], 0, v[144:145]
	s_mov_b32 m0, s69
	s_nop 0
	global_load_lds_dwordx4 v[180:181], off
	s_waitcnt vmcnt(8)
	s_waitcnt lgkmcnt(0)
	s_barrier
	s_setprio 1
	s_waitcnt lgkmcnt(0)
	v_mfma_f32_16x16x32_bf16 v[118:121], v[130:133], v[212:215], v[118:121]
	v_mfma_f32_16x16x32_bf16 v[114:117], v[172:175], v[212:215], v[114:117]
	v_mfma_f32_16x16x32_bf16 v[86:89], v[130:133], v[216:219], v[86:89]
	v_mfma_f32_16x16x32_bf16 v[82:85], v[172:175], v[216:219], v[82:85]
	v_mfma_f32_16x16x32_bf16 v[54:57], v[130:133], v[228:231], v[54:57]
	v_mfma_f32_16x16x32_bf16 v[50:53], v[172:175], v[228:231], v[50:53]
	v_mfma_f32_16x16x32_bf16 v[22:25], v[130:133], v[232:235], v[22:25]
	v_mfma_f32_16x16x32_bf16 v[18:21], v[172:175], v[232:235], v[18:21]
	v_mfma_f32_16x16x32_bf16 v[118:121], v[134:137], v[220:223], v[118:121]
	v_mfma_f32_16x16x32_bf16 v[114:117], v[176:179], v[220:223], v[114:117]
	v_mfma_f32_16x16x32_bf16 v[86:89], v[134:137], v[224:227], v[86:89]
	v_mfma_f32_16x16x32_bf16 v[82:85], v[176:179], v[224:227], v[82:85]
	v_mfma_f32_16x16x32_bf16 v[54:57], v[134:137], v[236:239], v[54:57]
	v_mfma_f32_16x16x32_bf16 v[50:53], v[176:179], v[236:239], v[50:53]
	v_mfma_f32_16x16x32_bf16 v[22:25], v[134:137], v[240:243], v[22:25]
	v_mfma_f32_16x16x32_bf16 v[18:21], v[176:179], v[240:243], v[18:21]
	v_mfma_f32_16x16x32_bf16 v[102:105], v[192:195], v[212:215], v[102:105]
	v_mfma_f32_16x16x32_bf16 v[98:101], v[204:207], v[212:215], v[98:101]
	v_mfma_f32_16x16x32_bf16 v[70:73], v[192:195], v[216:219], v[70:73]
	v_mfma_f32_16x16x32_bf16 v[66:69], v[204:207], v[216:219], v[66:69]
	v_mfma_f32_16x16x32_bf16 v[38:41], v[192:195], v[228:231], v[38:41]
	v_mfma_f32_16x16x32_bf16 v[34:37], v[204:207], v[228:231], v[34:37]
	v_mfma_f32_16x16x32_bf16 v[6:9], v[192:195], v[232:235], v[6:9]
	v_mfma_f32_16x16x32_bf16 v[2:5], v[204:207], v[232:235], v[2:5]
	v_mfma_f32_16x16x32_bf16 v[102:105], v[200:203], v[220:223], v[102:105]
	v_mfma_f32_16x16x32_bf16 v[98:101], v[208:211], v[220:223], v[98:101]
	v_mfma_f32_16x16x32_bf16 v[70:73], v[200:203], v[224:227], v[70:73]
	v_mfma_f32_16x16x32_bf16 v[66:69], v[208:211], v[224:227], v[66:69]
	v_mfma_f32_16x16x32_bf16 v[38:41], v[200:203], v[236:239], v[38:41]
	v_mfma_f32_16x16x32_bf16 v[34:37], v[208:211], v[236:239], v[34:37]
	v_mfma_f32_16x16x32_bf16 v[6:9], v[200:203], v[240:243], v[6:9]
	v_mfma_f32_16x16x32_bf16 v[2:5], v[208:211], v[240:243], v[2:5]
	s_setprio 0
	s_barrier
	s_setprio 3
	s_add_i32 s63, s63, 2
	s_add_u32 s49, s49, 0x100
	s_addc_u32 s62, s62, 0
	s_add_u32 s0, s0, 0x8000
	s_addc_u32 s1, s1, 0
	s_cmp_gt_u32 s63, 13
	s_cbranch_scc0 .LBB0_1498
	s_and_b64 vcc, exec, s[26:27]
	s_cbranch_vccz .LBB0_1502
	s_barrier
	s_cmp_gt_i32 s8, 7
	s_mov_b64 s[0:1], -1
	s_cbranch_scc1 .LBB0_1503

; #define PG8_STAGE(bufoff, gbase, voff) do { _Pragma("unroll") for (int _i = 0; _i < 2; ++_i) \
;         __builtin_amdgcn_global_load_lds((const unsigned*)((const char*)(gbase) + (voff)[_i]), (LAS unsigned*)(lds + (bufoff) + ldsw + _i * 8192), 16, 0, 0); } while (0)
; #define PG8_LDA(dst, b, h) do { _Pragma("unroll") for (int m = 0; m < 4; ++m) _Pragma("unroll") for (int k = 0; k < 2; ++k) dst[m][k] = *(const LAS bf16x8*)(lds + PG8_SA(b, h) + ((aoff ^ (k * 64)) + m * 2048)); } while (0)
; #define PG8_LDB(dst, b, h) do { _Pragma("unroll") for (int n = 0; n < 2; ++n) _Pragma("unroll") for (int k = 0; k < 2; ++k) dst[n][k] = *(const LAS bf16x8*)(lds + PG8_SB(b, h) + ((boff ^ (k * 64)) + n * 2048)); } while (0)
; #define PG8_MMA(ai, bj, At, Bt) do { __builtin_amdgcn_s_setprio(1); _Pragma("unroll") for (int m = 0; m < 4; ++m) _Pragma("unroll") for (int n = 0; n < 2; ++n) _Pragma("unroll") for (int k = 0; k < 2; ++k) \
;         acc[ai][bj][m][n] = __builtin_amdgcn_mfma_f32_16x16x32_bf16(Bt[n][k], At[m][k], acc[ai][bj][m][n], 0, 0, 0); __builtin_amdgcn_s_setprio(0); } while (0)
; #define PG8_WAIT_V(n) asm volatile("s_waitcnt vmcnt(" #n ")" ::: "memory")
; #define PG8_WAIT_L(n) asm volatile("s_waitcnt lgkmcnt(" #n ")" ::: "memory")
; #define PG8_BAR __builtin_amdgcn_s_barrier()
; #define PG8_SCHED __builtin_amdgcn_sched_barrier(0)
;     ...
;             PG8_LDB(B0, 1, 0); PG8_LDB(B1, 1, 1); PG8_SCHED; PG8_LDA(At, 1, 0); PG8_STAGE(PG8_SA(0, 1), a2, vs[1]);
;             PG8_WAIT_V(8); PG8_WAIT_L(0); PG8_BAR; if (do0) { PG8_MMA(0, 0, At, B0); PG8_MMA(0, 1, At, B1); } PG8_BAR; PG8_SCHED;
.LBB0_1663:
	s_barrier
	s_setprio 3
	v_add_u32_e32 v130, s58, v216
	v_add_u32_e32 v131, s58, v217
	ds_read_b128 v[146:149], v130
	ds_read_b128 v[150:153], v131
	v_add_u32_e32 v130, s56, v216
	v_add_u32_e32 v131, s56, v217
	ds_read_b128 v[154:157], v130
	ds_read_b128 v[158:161], v131
	v_add_u32_e32 v130, s59, v216
	v_add_u32_e32 v134, s59, v217
	v_add_u32_e32 v138, s57, v216
	v_add_u32_e32 v142, s57, v217
	ds_read_b128 v[130:133], v130
	ds_read_b128 v[134:137], v134
	ds_read_b128 v[138:141], v138
	ds_read_b128 v[142:145], v142
	s_mov_b32 m0, s39
	v_lshl_add_u64 v[228:229], s[26:27], 0, v[204:205]
	s_waitcnt lgkmcnt(0)
	ds_read_b128 v[186:189], v226 offset:32768
	ds_read_b128 v[174:177], v226 offset:34816
	ds_read_b128 v[190:193], v227 offset:32768
	ds_read_b128 v[178:181], v227 offset:34816
	ds_read_b128 v[170:173], v226 offset:36864
	ds_read_b128 v[162:165], v226 offset:38912
	ds_read_b128 v[182:185], v227 offset:36864
	ds_read_b128 v[166:169], v227 offset:38912
	global_load_lds_dwordx4 v[228:229], off
	v_lshl_add_u64 v[228:229], s[26:27], 0, v[206:207]
	s_mov_b32 m0, s40
	s_and_b64 vcc, exec, s[0:1]
	global_load_lds_dwordx4 v[228:229], off
	s_waitcnt vmcnt(8)
	s_waitcnt lgkmcnt(0)
	s_barrier
	s_cbranch_vccnz .LBB0_1665
	s_setprio 1
	s_waitcnt lgkmcnt(0)
	v_mfma_f32_16x16x32_bf16 v[114:117], v[146:149], v[186:189], v[114:117]
	v_mfma_f32_16x16x32_bf16 v[118:121], v[154:157], v[186:189], v[118:121]
	v_mfma_f32_16x16x32_bf16 v[82:85], v[146:149], v[174:177], v[82:85]
	v_mfma_f32_16x16x32_bf16 v[86:89], v[154:157], v[174:177], v[86:89]
	v_mfma_f32_16x16x32_bf16 v[50:53], v[146:149], v[170:173], v[50:53]
	v_mfma_f32_16x16x32_bf16 v[54:57], v[154:157], v[170:173], v[54:57]
	v_mfma_f32_16x16x32_bf16 v[18:21], v[146:149], v[162:165], v[18:21]
	v_mfma_f32_16x16x32_bf16 v[22:25], v[154:157], v[162:165], v[22:25]
	v_mfma_f32_16x16x32_bf16 v[114:117], v[150:153], v[190:193], v[114:117]
	v_mfma_f32_16x16x32_bf16 v[118:121], v[158:161], v[190:193], v[118:121]
	v_mfma_f32_16x16x32_bf16 v[82:85], v[150:153], v[178:181], v[82:85]
	v_mfma_f32_16x16x32_bf16 v[86:89], v[158:161], v[178:181], v[86:89]
	v_mfma_f32_16x16x32_bf16 v[50:53], v[150:153], v[182:185], v[50:53]
	v_mfma_f32_16x16x32_bf16 v[54:57], v[158:161], v[182:185], v[54:57]
	v_mfma_f32_16x16x32_bf16 v[18:21], v[150:153], v[166:169], v[18:21]
	v_mfma_f32_16x16x32_bf16 v[22:25], v[158:161], v[166:169], v[22:25]
	v_mfma_f32_16x16x32_bf16 v[98:101], v[130:133], v[186:189], v[98:101]
	v_mfma_f32_16x16x32_bf16 v[102:105], v[138:141], v[186:189], v[102:105]
	v_mfma_f32_16x16x32_bf16 v[66:69], v[130:133], v[174:177], v[66:69]
	v_mfma_f32_16x16x32_bf16 v[70:73], v[138:141], v[174:177], v[70:73]
	v_mfma_f32_16x16x32_bf16 v[34:37], v[130:133], v[170:173], v[34:37]
	v_mfma_f32_16x16x32_bf16 v[38:41], v[138:141], v[170:173], v[38:41]
	v_mfma_f32_16x16x32_bf16 v[6:9], v[130:133], v[162:165], v[6:9]
	v_mfma_f32_16x16x32_bf16 v[10:13], v[138:141], v[162:165], v[10:13]
	v_mfma_f32_16x16x32_bf16 v[98:101], v[134:137], v[190:193], v[98:101]
	v_mfma_f32_16x16x32_bf16 v[102:105], v[142:145], v[190:193], v[102:105]
	v_mfma_f32_16x16x32_bf16 v[66:69], v[134:137], v[178:181], v[66:69]
	v_mfma_f32_16x16x32_bf16 v[70:73], v[142:145], v[178:181], v[70:73]
	v_mfma_f32_16x16x32_bf16 v[34:37], v[134:137], v[182:185], v[34:37]
	v_mfma_f32_16x16x32_bf16 v[38:41], v[142:145], v[182:185], v[38:41]
	v_mfma_f32_16x16x32_bf16 v[6:9], v[134:137], v[166:169], v[6:9]
	v_mfma_f32_16x16x32_bf16 v[10:13], v[142:145], v[166:169], v[10:13]
	s_setprio 0
; #define PG8_STAGE(bufoff, gbase, voff) do { _Pragma("unroll") for (int _i = 0; _i < 2; ++_i) \
;         __builtin_amdgcn_global_load_lds((const unsigned*)((const char*)(gbase) + (voff)[_i]), (LAS unsigned*)(lds + (bufoff) + ldsw + _i * 8192), 16, 0, 0); } while (0)
; #define PG8_LDA(dst, b, h) do { _Pragma("unroll") for (int m = 0; m < 4; ++m) _Pragma("unroll") for (int k = 0; k < 2; ++k) dst[m][k] = *(const LAS bf16x8*)(lds + PG8_SA(b, h) + ((aoff ^ (k * 64)) + m * 2048)); } while (0)
; #define PG8_MMA(ai, bj, At, Bt) do { __builtin_amdgcn_s_setprio(1); _Pragma("unroll") for (int m = 0; m < 4; ++m) _Pragma("unroll") for (int n = 0; n < 2; ++n) _Pragma("unroll") for (int k = 0; k < 2; ++k) \
;         acc[ai][bj][m][n] = __builtin_amdgcn_mfma_f32_16x16x32_bf16(Bt[n][k], At[m][k], acc[ai][bj][m][n], 0, 0, 0); __builtin_amdgcn_s_setprio(0); } while (0)
; #define PG8_WAIT_V(n) asm volatile("s_waitcnt vmcnt(" #n ")" ::: "memory")
; #define PG8_WAIT_L(n) asm volatile("s_waitcnt lgkmcnt(" #n ")" ::: "memory")
; #define PG8_BAR __builtin_amdgcn_s_barrier()
; #define PG8_SCHED __builtin_amdgcn_sched_barrier(0)
;     ...
;     if (wr == 1) PG8_BAR;
;     ...
;             PG8_LDA(At, 1, 1); PG8_STAGE(PG8_SB(1, 0), b3, voffB); PG8_STAGE(PG8_SB(1, 1), b3 + hstep, voffB); PG8_STAGE(PG8_SA(1, 0), a3, vs[0]);
;             PG8_WAIT_V(8); PG8_WAIT_L(0); PG8_BAR; if (do1) { PG8_MMA(1, 0, At, B0); PG8_MMA(1, 1, At, B1); } PG8_BAR; PG8_SCHED;
;         }
.LBB0_1665:
	s_add_u32 s26, s26, 0x4000
	s_addc_u32 s27, s27, 0
	s_barrier
	s_setprio 3
	s_mov_b32 m0, s44
	v_lshl_add_u64 v[212:213], v[212:213], 0, s[14:15]
	s_add_u32 s24, s24, 0x40080
	s_waitcnt lgkmcnt(0)
	ds_read_b128 v[186:189], v226 offset:49152
	ds_read_b128 v[174:177], v226 offset:51200
	ds_read_b128 v[190:193], v227 offset:49152
	ds_read_b128 v[178:181], v227 offset:51200
	ds_read_b128 v[170:173], v226 offset:53248
	ds_read_b128 v[162:165], v226 offset:55296
	ds_read_b128 v[182:185], v227 offset:53248
	ds_read_b128 v[166:169], v227 offset:55296
	global_load_lds_dwordx4 v[212:213], off
	v_lshl_add_u64 v[212:213], v[214:215], 0, s[14:15]
	s_mov_b32 m0, s45
	s_addc_u32 s25, s25, 0
	global_load_lds_dwordx4 v[212:213], off
	v_lshl_add_u64 v[212:213], s[24:25], 0, v[196:197]
	s_mov_b32 m0, s48
	s_and_b64 vcc, exec, s[6:7]
	global_load_lds_dwordx4 v[212:213], off
	v_lshl_add_u64 v[212:213], s[24:25], 0, v[194:195]
	s_mov_b32 m0, s49
	s_nop 0
	global_load_lds_dwordx4 v[212:213], off
	v_lshl_add_u64 v[212:213], s[26:27], 0, v[200:201]
	s_mov_b32 m0, s46
	s_nop 0
	global_load_lds_dwordx4 v[212:213], off
	v_lshl_add_u64 v[212:213], s[26:27], 0, v[202:203]
	s_mov_b32 m0, s47
	s_nop 0
	global_load_lds_dwordx4 v[212:213], off
	s_waitcnt vmcnt(8)
	s_waitcnt lgkmcnt(0)
	s_barrier
	s_cbranch_vccnz .LBB0_1658
	s_setprio 1
	s_waitcnt lgkmcnt(0)
	v_mfma_f32_16x16x32_bf16 v[126:129], v[146:149], v[186:189], v[126:129]
	v_mfma_f32_16x16x32_bf16 v[122:125], v[154:157], v[186:189], v[122:125]
	v_mfma_f32_16x16x32_bf16 v[94:97], v[146:149], v[174:177], v[94:97]
	v_mfma_f32_16x16x32_bf16 v[90:93], v[154:157], v[174:177], v[90:93]
	v_mfma_f32_16x16x32_bf16 v[62:65], v[146:149], v[170:173], v[62:65]
	v_mfma_f32_16x16x32_bf16 v[58:61], v[154:157], v[170:173], v[58:61]
	v_mfma_f32_16x16x32_bf16 v[30:33], v[146:149], v[162:165], v[30:33]
	v_mfma_f32_16x16x32_bf16 v[26:29], v[154:157], v[162:165], v[26:29]
	v_mfma_f32_16x16x32_bf16 v[126:129], v[150:153], v[190:193], v[126:129]
	v_mfma_f32_16x16x32_bf16 v[122:125], v[158:161], v[190:193], v[122:125]
	v_mfma_f32_16x16x32_bf16 v[94:97], v[150:153], v[178:181], v[94:97]
	v_mfma_f32_16x16x32_bf16 v[90:93], v[158:161], v[178:181], v[90:93]
	v_mfma_f32_16x16x32_bf16 v[62:65], v[150:153], v[182:185], v[62:65]
	v_mfma_f32_16x16x32_bf16 v[58:61], v[158:161], v[182:185], v[58:61]
	v_mfma_f32_16x16x32_bf16 v[30:33], v[150:153], v[166:169], v[30:33]
	v_mfma_f32_16x16x32_bf16 v[26:29], v[158:161], v[166:169], v[26:29]
	v_mfma_f32_16x16x32_bf16 v[110:113], v[130:133], v[186:189], v[110:113]
	v_mfma_f32_16x16x32_bf16 v[106:109], v[138:141], v[186:189], v[106:109]
	v_mfma_f32_16x16x32_bf16 v[78:81], v[130:133], v[174:177], v[78:81]
	v_mfma_f32_16x16x32_bf16 v[74:77], v[138:141], v[174:177], v[74:77]
	v_mfma_f32_16x16x32_bf16 v[46:49], v[130:133], v[170:173], v[46:49]
	v_mfma_f32_16x16x32_bf16 v[42:45], v[138:141], v[170:173], v[42:45]
	v_mfma_f32_16x16x32_bf16 v[14:17], v[130:133], v[162:165], v[14:17]
	v_mfma_f32_16x16x32_bf16 v[2:5], v[138:141], v[162:165], v[2:5]
	v_mfma_f32_16x16x32_bf16 v[110:113], v[134:137], v[190:193], v[110:113]
	v_mfma_f32_16x16x32_bf16 v[106:109], v[142:145], v[190:193], v[106:109]
	v_mfma_f32_16x16x32_bf16 v[78:81], v[134:137], v[178:181], v[78:81]
	v_mfma_f32_16x16x32_bf16 v[74:77], v[142:145], v[178:181], v[74:77]
	v_mfma_f32_16x16x32_bf16 v[46:49], v[134:137], v[182:185], v[46:49]
	v_mfma_f32_16x16x32_bf16 v[42:45], v[142:145], v[182:185], v[42:45]
	v_mfma_f32_16x16x32_bf16 v[14:17], v[134:137], v[166:169], v[14:17]
	v_mfma_f32_16x16x32_bf16 v[2:5], v[142:145], v[166:169], v[2:5]
	s_setprio 0
	s_branch .LBB0_1658
.LBB0_1667:
	s_cmpk_lt_u32 s30, 0x100
	s_cbranch_scc0 .LBB0_1670
	s_barrier
	s_setprio 3
	s_cmp_gt_i32 s8, 7
	s_mov_b64 s[0:1], -1
	s_cbranch_scc1 .LBB0_1671

; #define PG8_STAGE(bufoff, gbase, voff) do { _Pragma("unroll") for (int _i = 0; _i < 2; ++_i) \
;         __builtin_amdgcn_global_load_lds((const unsigned*)((const char*)(gbase) + (voff)[_i]), (LAS unsigned*)(lds + (bufoff) + ldsw + _i * 8192), 16, 0, 0); } while (0)
; #define PG8_LDA(dst, b, h) do { _Pragma("unroll") for (int m = 0; m < 4; ++m) _Pragma("unroll") for (int k = 0; k < 2; ++k) dst[m][k] = *(const LAS bf16x8*)(lds + PG8_SA(b, h) + ((aoff ^ (k * 64)) + m * 2048)); } while (0)
; #define PG8_LDB(dst, b, h) do { _Pragma("unroll") for (int n = 0; n < 2; ++n) _Pragma("unroll") for (int k = 0; k < 2; ++k) dst[n][k] = *(const LAS bf16x8*)(lds + PG8_SB(b, h) + ((boff ^ (k * 64)) + n * 2048)); } while (0)
; #define PG8_WAIT_V(n) asm volatile("s_waitcnt vmcnt(" #n ")" ::: "memory")
; #define PG8_BAR __builtin_amdgcn_s_barrier()
;     ...
;         for (int t = 0; t < nt; t += 2) {
;             const bool last = (t == nt - 2);
;             const char* a1 = cA + (size_t)(t + 1) * kstepA;
;             const char* a2 = last ? nA : cA + (size_t)(t + 2) * kstepA; const char* b2 = last ? nB : cB + (size_t)(t + 2) * kstepB;
;             const char* a3 = a2 + kstepA; const char* b3 = b2 + kstepB;
;             unsigned vs[2][2];
;             if constexpr (GATHER) {
;                 if (last && has_next) {
; #pragma unroll
;                     for (int hh = 0; hh < 2; ++hh)
; #pragma unroll
;                         for (int i = 0; i < 2; ++i) voffN[hh][i] = (unsigned)idxl[(ui + 1) * 256 + hh * HALF + sR[i]] * (unsigned)(K * 2) + (unsigned)sC[i] * 2u;
;                 }
; #pragma unroll
;                 for (int hh = 0; hh < 2; ++hh)
; #pragma unroll
;                     for (int i = 0; i < 2; ++i) vs[hh][i] = last ? voffN[hh][i] : voffA[hh][i];
;             } else {
; #pragma unroll
;                 for (int hh = 0; hh < 2; ++hh)
; #pragma unroll
;                     for (int i = 0; i < 2; ++i) vs[hh][i] = voffA[hh][i];
;             }
;             PG8_LDB(B0, 0, 0); PG8_LDB(B1, 0, 1); PG8_SCHED; PG8_LDA(At, 0, 0); PG8_STAGE(PG8_SA(1, 1), a1, voffA[1]);
;             PG8_WAIT_V(8); PG8_WAIT_L(0); PG8_BAR; if (do0) { PG8_MMA(0, 0, At, B0); PG8_MMA(0, 1, At, B1); } PG8_BAR; PG8_SCHED;
;             PG8_LDA(At, 0, 1); PG8_STAGE(PG8_SB(0, 0), b2, voffB); PG8_STAGE(PG8_SB(0, 1), b2 + hstep, voffB); PG8_STAGE(PG8_SA(0, 0), a2, vs[0]);
.LBB0_1934:
	ds_read_b128 v[74:77], v191
	ds_read_b128 v[78:81], v192
	ds_read_b128 v[102:105], v193
	ds_read_b128 v[106:109], v194
	ds_read_b128 v[168:171], v195
	ds_read_b128 v[172:175], v196
	ds_read_b128 v[176:179], v197
	ds_read_b128 v[180:183], v199
	s_add_u32 s38, s0, 0x80
	s_addc_u32 s39, s1, 0
	s_cmp_eq_u32 s45, 28
	s_cselect_b32 s43, s7, s39
	s_cselect_b32 s42, s8, s38
	s_cselect_b32 s39, s27, s44
	s_cselect_b32 s38, s29, s37
	v_lshl_add_u64 v[184:185], s[0:1], 0, v[162:163]
	s_add_i32 m0, s52, 0xc000
	ds_read_b128 v[210:213], v200
	ds_read_b128 v[214:217], v200 offset:2048
	ds_read_b128 v[218:221], v201
	ds_read_b128 v[222:225], v201 offset:2048
	ds_read_b128 v[226:229], v200 offset:4096
	ds_read_b128 v[230:233], v200 offset:6144
	ds_read_b128 v[234:237], v201 offset:4096
	ds_read_b128 v[238:241], v201 offset:6144
	global_load_lds_dwordx4 v[184:185], off
	v_lshl_add_u64 v[184:185], s[0:1], 0, v[160:161]
	s_add_i32 m0, s52, 0xe000
	s_add_u32 s40, s38, 0x4000
	global_load_lds_dwordx4 v[184:185], off
	s_waitcnt vmcnt(8)
	s_waitcnt lgkmcnt(0)
	s_addc_u32 s41, s39, 0
	s_barrier
	s_setprio 1
	s_waitcnt lgkmcnt(0)
	v_mfma_f32_16x16x32_bf16 v[142:145], v[74:77], v[210:213], v[142:145]
	v_mfma_f32_16x16x32_bf16 v[10:13], v[102:105], v[210:213], v[10:13]
	v_mfma_f32_16x16x32_bf16 v[134:137], v[74:77], v[214:217], v[134:137]
	v_mfma_f32_16x16x32_bf16 v[18:21], v[102:105], v[214:217], v[18:21]
	v_mfma_f32_16x16x32_bf16 v[126:129], v[74:77], v[226:229], v[126:129]
	v_mfma_f32_16x16x32_bf16 v[22:25], v[102:105], v[226:229], v[22:25]
	v_mfma_f32_16x16x32_bf16 v[118:121], v[74:77], v[230:233], v[118:121]
	v_mfma_f32_16x16x32_bf16 v[34:37], v[102:105], v[230:233], v[34:37]
	v_mfma_f32_16x16x32_bf16 v[142:145], v[78:81], v[218:221], v[142:145]
	v_mfma_f32_16x16x32_bf16 v[10:13], v[106:109], v[218:221], v[10:13]
	v_mfma_f32_16x16x32_bf16 v[134:137], v[78:81], v[222:225], v[134:137]
	v_mfma_f32_16x16x32_bf16 v[18:21], v[106:109], v[222:225], v[18:21]
	v_mfma_f32_16x16x32_bf16 v[126:129], v[78:81], v[234:237], v[126:129]
	v_mfma_f32_16x16x32_bf16 v[22:25], v[106:109], v[234:237], v[22:25]
	v_mfma_f32_16x16x32_bf16 v[118:121], v[78:81], v[238:241], v[118:121]
	v_mfma_f32_16x16x32_bf16 v[34:37], v[106:109], v[238:241], v[34:37]
	v_mfma_f32_16x16x32_bf16 v[138:141], v[168:171], v[210:213], v[138:141]
	v_mfma_f32_16x16x32_bf16 v[14:17], v[176:179], v[210:213], v[14:17]
	v_mfma_f32_16x16x32_bf16 v[130:133], v[168:171], v[214:217], v[130:133]
	v_mfma_f32_16x16x32_bf16 v[30:33], v[176:179], v[214:217], v[30:33]
	v_mfma_f32_16x16x32_bf16 v[122:125], v[168:171], v[226:229], v[122:125]
	v_mfma_f32_16x16x32_bf16 v[26:29], v[176:179], v[226:229], v[26:29]
	v_mfma_f32_16x16x32_bf16 v[114:117], v[168:171], v[230:233], v[114:117]
	v_mfma_f32_16x16x32_bf16 v[46:49], v[176:179], v[230:233], v[46:49]
	v_mfma_f32_16x16x32_bf16 v[138:141], v[172:175], v[218:221], v[138:141]
	v_mfma_f32_16x16x32_bf16 v[14:17], v[180:183], v[218:221], v[14:17]
	v_mfma_f32_16x16x32_bf16 v[130:133], v[172:175], v[222:225], v[130:133]
	v_mfma_f32_16x16x32_bf16 v[30:33], v[180:183], v[222:225], v[30:33]
	v_mfma_f32_16x16x32_bf16 v[122:125], v[172:175], v[234:237], v[122:125]
	v_mfma_f32_16x16x32_bf16 v[26:29], v[180:183], v[234:237], v[26:29]
	v_mfma_f32_16x16x32_bf16 v[114:117], v[172:175], v[238:241], v[114:117]
	v_mfma_f32_16x16x32_bf16 v[46:49], v[180:183], v[238:241], v[46:49]
	s_setprio 0
	s_barrier
	s_setprio 3
	s_add_i32 s46, s67, s51
	v_lshl_add_u64 v[184:185], s[38:39], 0, v[146:147]
	s_mov_b32 m0, s46
	ds_read_b128 v[210:213], v200 offset:16384
	ds_read_b128 v[214:217], v200 offset:18432
	ds_read_b128 v[218:221], v201 offset:16384
	ds_read_b128 v[222:225], v201 offset:18432
	ds_read_b128 v[226:229], v200 offset:20480
	ds_read_b128 v[230:233], v200 offset:22528
	ds_read_b128 v[234:237], v201 offset:20480
	ds_read_b128 v[238:241], v201 offset:22528
	global_load_lds_dwordx4 v[184:185], off
	s_add_i32 m0, s46, 0x2000
	s_add_u32 s46, s38, 0x80000
	v_lshl_add_u64 v[184:185], s[38:39], 0, v[148:149]
	s_addc_u32 s47, s39, 0
	s_add_i32 s72, s68, s51
	global_load_lds_dwordx4 v[184:185], off
	v_lshl_add_u64 v[184:185], s[46:47], 0, v[146:147]
	s_mov_b32 m0, s72
	v_lshl_add_u64 v[242:243], s[42:43], 0, v[152:153]
	global_load_lds_dwordx4 v[184:185], off
	v_lshl_add_u64 v[184:185], s[46:47], 0, v[148:149]
	s_add_i32 m0, s72, 0x2000
	s_nop 0
	global_load_lds_dwordx4 v[184:185], off
	v_lshl_add_u64 v[184:185], s[42:43], 0, v[150:151]
	s_mov_b32 m0, s52
	s_nop 0
	global_load_lds_dwordx4 v[184:185], off
	s_mov_b32 m0, s53
	s_nop 0
	global_load_lds_dwordx4 v[242:243], off
	s_waitcnt vmcnt(8)
	s_waitcnt lgkmcnt(0)
	s_barrier
; #define PG8_STAGE(bufoff, gbase, voff) do { _Pragma("unroll") for (int _i = 0; _i < 2; ++_i) \
;         __builtin_amdgcn_global_load_lds((const unsigned*)((const char*)(gbase) + (voff)[_i]), (LAS unsigned*)(lds + (bufoff) + ldsw + _i * 8192), 16, 0, 0); } while (0)
; #define PG8_LDA(dst, b, h) do { _Pragma("unroll") for (int m = 0; m < 4; ++m) _Pragma("unroll") for (int k = 0; k < 2; ++k) dst[m][k] = *(const LAS bf16x8*)(lds + PG8_SA(b, h) + ((aoff ^ (k * 64)) + m * 2048)); } while (0)
; #define PG8_LDB(dst, b, h) do { _Pragma("unroll") for (int n = 0; n < 2; ++n) _Pragma("unroll") for (int k = 0; k < 2; ++k) dst[n][k] = *(const LAS bf16x8*)(lds + PG8_SB(b, h) + ((boff ^ (k * 64)) + n * 2048)); } while (0)
; #define PG8_MMA(ai, bj, At, Bt) do { __builtin_amdgcn_s_setprio(1); _Pragma("unroll") for (int m = 0; m < 4; ++m) _Pragma("unroll") for (int n = 0; n < 2; ++n) _Pragma("unroll") for (int k = 0; k < 2; ++k) \
;         acc[ai][bj][m][n] = __builtin_amdgcn_mfma_f32_16x16x32_bf16(Bt[n][k], At[m][k], acc[ai][bj][m][n], 0, 0, 0); __builtin_amdgcn_s_setprio(0); } while (0)
; #define PG8_WAIT_V(n) asm volatile("s_waitcnt vmcnt(" #n ")" ::: "memory")
; #define PG8_WAIT_L(n) asm volatile("s_waitcnt lgkmcnt(" #n ")" ::: "memory")
; #define PG8_BAR __builtin_amdgcn_s_barrier()
; #define PG8_SCHED __builtin_amdgcn_sched_barrier(0)
;     ...
;             PG8_WAIT_V(8); PG8_WAIT_L(0); PG8_BAR; if (do1) { PG8_MMA(1, 0, At, B0); PG8_MMA(1, 1, At, B1); } PG8_BAR; PG8_SCHED;
;             PG8_LDB(B0, 1, 0); PG8_LDB(B1, 1, 1); PG8_SCHED; PG8_LDA(At, 1, 0); PG8_STAGE(PG8_SA(0, 1), a2, vs[1]);
;             PG8_WAIT_V(8); PG8_WAIT_L(0); PG8_BAR; if (do0) { PG8_MMA(0, 0, At, B0); PG8_MMA(0, 1, At, B1); } PG8_BAR; PG8_SCHED;
	s_setprio 1
	s_waitcnt lgkmcnt(0)
	v_mfma_f32_16x16x32_bf16 v[110:113], v[74:77], v[210:213], v[110:113]
	v_mfma_f32_16x16x32_bf16 v[58:61], v[102:105], v[210:213], v[58:61]
	v_mfma_f32_16x16x32_bf16 v[94:97], v[74:77], v[214:217], v[94:97]
	v_mfma_f32_16x16x32_bf16 v[82:85], v[102:105], v[214:217], v[82:85]
	v_mfma_f32_16x16x32_bf16 v[66:69], v[74:77], v[226:229], v[66:69]
	v_mfma_f32_16x16x32_bf16 v[62:65], v[102:105], v[226:229], v[62:65]
	v_mfma_f32_16x16x32_bf16 v[42:45], v[74:77], v[230:233], v[42:45]
	v_mfma_f32_16x16x32_bf16 v[38:41], v[102:105], v[230:233], v[38:41]
	v_mfma_f32_16x16x32_bf16 v[110:113], v[78:81], v[218:221], v[110:113]
	v_mfma_f32_16x16x32_bf16 v[58:61], v[106:109], v[218:221], v[58:61]
	v_mfma_f32_16x16x32_bf16 v[94:97], v[78:81], v[222:225], v[94:97]
	v_mfma_f32_16x16x32_bf16 v[82:85], v[106:109], v[222:225], v[82:85]
	v_mfma_f32_16x16x32_bf16 v[66:69], v[78:81], v[234:237], v[66:69]
	v_mfma_f32_16x16x32_bf16 v[62:65], v[106:109], v[234:237], v[62:65]
	v_mfma_f32_16x16x32_bf16 v[42:45], v[78:81], v[238:241], v[42:45]
	v_mfma_f32_16x16x32_bf16 v[38:41], v[106:109], v[238:241], v[38:41]
	v_mfma_f32_16x16x32_bf16 v[70:73], v[176:179], v[210:213], v[70:73]
	v_mfma_f32_16x16x32_bf16 v[86:89], v[176:179], v[214:217], v[86:89]
	v_mfma_f32_16x16x32_bf16 v[54:57], v[168:171], v[226:229], v[54:57]
	v_mfma_f32_16x16x32_bf16 v[50:53], v[176:179], v[226:229], v[50:53]
	v_mfma_f32_16x16x32_bf16 v[6:9], v[168:171], v[230:233], v[6:9]
	v_mfma_f32_16x16x32_bf16 v[2:5], v[176:179], v[230:233], v[2:5]
	v_mfma_f32_16x16x32_bf16 v[74:77], v[168:171], v[210:213], v[98:101]
	v_mfma_f32_16x16x32_bf16 v[70:73], v[180:183], v[218:221], v[70:73]
	v_mfma_f32_16x16x32_bf16 v[78:81], v[168:171], v[214:217], v[90:93]
	v_mfma_f32_16x16x32_bf16 v[86:89], v[180:183], v[222:225], v[86:89]
	v_mfma_f32_16x16x32_bf16 v[54:57], v[172:175], v[234:237], v[54:57]
	v_mfma_f32_16x16x32_bf16 v[50:53], v[180:183], v[234:237], v[50:53]
	v_mfma_f32_16x16x32_bf16 v[6:9], v[172:175], v[238:241], v[6:9]
	v_mfma_f32_16x16x32_bf16 v[2:5], v[180:183], v[238:241], v[2:5]
	v_mfma_f32_16x16x32_bf16 v[74:77], v[172:175], v[218:221], v[74:77]
	v_mfma_f32_16x16x32_bf16 v[78:81], v[172:175], v[222:225], v[78:81]
	s_setprio 0
	s_barrier
	s_setprio 3
	s_add_i32 s46, 0, 0x18000
	s_add_i32 s47, 0, 0x1c000
	v_add_u32_e32 v90, s46, v189
	v_add_u32_e32 v98, s46, v190
	v_add_u32_e32 v158, s47, v189
	v_add_u32_e32 v172, s47, v190
	ds_read_b128 v[90:93], v90
	ds_read_b128 v[98:101], v98
	ds_read_b128 v[102:105], v202
	ds_read_b128 v[106:109], v203
	ds_read_b128 v[168:171], v158
	ds_read_b128 v[172:175], v172
	ds_read_b128 v[176:179], v204
	ds_read_b128 v[180:183], v205
	s_mov_b32 m0, s54
	v_lshl_add_u64 v[244:245], s[42:43], 0, v[154:155]
	ds_read_b128 v[210:213], v200 offset:32768
	ds_read_b128 v[214:217], v200 offset:34816
	ds_read_b128 v[218:221], v201 offset:32768
	ds_read_b128 v[222:225], v201 offset:34816
	ds_read_b128 v[226:229], v200 offset:36864
	ds_read_b128 v[230:233], v200 offset:38912
	ds_read_b128 v[234:237], v201 offset:36864
	ds_read_b128 v[238:241], v201 offset:38912
	global_load_lds_dwordx4 v[244:245], off
	v_lshl_add_u64 v[244:245], s[42:43], 0, v[156:157]
	s_mov_b32 m0, s55
	s_nop 0
	global_load_lds_dwordx4 v[244:245], off
	s_waitcnt vmcnt(8)
	s_waitcnt lgkmcnt(0)
	s_barrier
	s_setprio 1
	s_waitcnt lgkmcnt(0)
	v_mfma_f32_16x16x32_bf16 v[142:145], v[90:93], v[210:213], v[142:145]
	v_mfma_f32_16x16x32_bf16 v[10:13], v[102:105], v[210:213], v[10:13]
	v_mfma_f32_16x16x32_bf16 v[134:137], v[90:93], v[214:217], v[134:137]
	v_mfma_f32_16x16x32_bf16 v[18:21], v[102:105], v[214:217], v[18:21]
	v_mfma_f32_16x16x32_bf16 v[126:129], v[90:93], v[226:229], v[126:129]
	v_mfma_f32_16x16x32_bf16 v[22:25], v[102:105], v[226:229], v[22:25]
	v_mfma_f32_16x16x32_bf16 v[118:121], v[90:93], v[230:233], v[118:121]
	v_mfma_f32_16x16x32_bf16 v[34:37], v[102:105], v[230:233], v[34:37]
	v_mfma_f32_16x16x32_bf16 v[142:145], v[98:101], v[218:221], v[142:145]
	v_mfma_f32_16x16x32_bf16 v[10:13], v[106:109], v[218:221], v[10:13]
	v_mfma_f32_16x16x32_bf16 v[134:137], v[98:101], v[222:225], v[134:137]
	v_mfma_f32_16x16x32_bf16 v[18:21], v[106:109], v[222:225], v[18:21]
	v_mfma_f32_16x16x32_bf16 v[126:129], v[98:101], v[234:237], v[126:129]
	v_mfma_f32_16x16x32_bf16 v[22:25], v[106:109], v[234:237], v[22:25]
	v_mfma_f32_16x16x32_bf16 v[118:121], v[98:101], v[238:241], v[118:121]
	v_mfma_f32_16x16x32_bf16 v[34:37], v[106:109], v[238:241], v[34:37]
	v_mfma_f32_16x16x32_bf16 v[138:141], v[168:171], v[210:213], v[138:141]
	v_mfma_f32_16x16x32_bf16 v[14:17], v[176:179], v[210:213], v[14:17]
	v_mfma_f32_16x16x32_bf16 v[130:133], v[168:171], v[214:217], v[130:133]
	v_mfma_f32_16x16x32_bf16 v[30:33], v[176:179], v[214:217], v[30:33]
	v_mfma_f32_16x16x32_bf16 v[122:125], v[168:171], v[226:229], v[122:125]
	v_mfma_f32_16x16x32_bf16 v[26:29], v[176:179], v[226:229], v[26:29]
	v_mfma_f32_16x16x32_bf16 v[114:117], v[168:171], v[230:233], v[114:117]
	v_mfma_f32_16x16x32_bf16 v[46:49], v[176:179], v[230:233], v[46:49]
	v_mfma_f32_16x16x32_bf16 v[138:141], v[172:175], v[218:221], v[138:141]
	v_mfma_f32_16x16x32_bf16 v[14:17], v[180:183], v[218:221], v[14:17]
	v_mfma_f32_16x16x32_bf16 v[130:133], v[172:175], v[222:225], v[130:133]
	v_mfma_f32_16x16x32_bf16 v[30:33], v[180:183], v[222:225], v[30:33]
	v_mfma_f32_16x16x32_bf16 v[122:125], v[172:175], v[234:237], v[122:125]
	v_mfma_f32_16x16x32_bf16 v[26:29], v[180:183], v[234:237], v[26:29]
	v_mfma_f32_16x16x32_bf16 v[114:117], v[172:175], v[238:241], v[114:117]
	v_mfma_f32_16x16x32_bf16 v[46:49], v[180:183], v[238:241], v[46:49]
	s_setprio 0
	s_barrier
; #define PG8_STAGE(bufoff, gbase, voff) do { _Pragma("unroll") for (int _i = 0; _i < 2; ++_i) \
;         __builtin_amdgcn_global_load_lds((const unsigned*)((const char*)(gbase) + (voff)[_i]), (LAS unsigned*)(lds + (bufoff) + ldsw + _i * 8192), 16, 0, 0); } while (0)
; #define PG8_LDA(dst, b, h) do { _Pragma("unroll") for (int m = 0; m < 4; ++m) _Pragma("unroll") for (int k = 0; k < 2; ++k) dst[m][k] = *(const LAS bf16x8*)(lds + PG8_SA(b, h) + ((aoff ^ (k * 64)) + m * 2048)); } while (0)
; #define PG8_MMA(ai, bj, At, Bt) do { __builtin_amdgcn_s_setprio(1); _Pragma("unroll") for (int m = 0; m < 4; ++m) _Pragma("unroll") for (int n = 0; n < 2; ++n) _Pragma("unroll") for (int k = 0; k < 2; ++k) \
;         acc[ai][bj][m][n] = __builtin_amdgcn_mfma_f32_16x16x32_bf16(Bt[n][k], At[m][k], acc[ai][bj][m][n], 0, 0, 0); __builtin_amdgcn_s_setprio(0); } while (0)
; #define PG8_WAIT_V(n) asm volatile("s_waitcnt vmcnt(" #n ")" ::: "memory")
; #define PG8_WAIT_L(n) asm volatile("s_waitcnt lgkmcnt(" #n ")" ::: "memory")
; #define PG8_BAR __builtin_amdgcn_s_barrier()
; #define PG8_SCHED __builtin_amdgcn_sched_barrier(0)
;     ...
;             PG8_LDA(At, 1, 1); PG8_STAGE(PG8_SB(1, 0), b3, voffB); PG8_STAGE(PG8_SB(1, 1), b3 + hstep, voffB); PG8_STAGE(PG8_SA(1, 0), a3, vs[0]);
;             PG8_WAIT_V(8); PG8_WAIT_L(0); PG8_BAR; if (do1) { PG8_MMA(1, 0, At, B0); PG8_MMA(1, 1, At, B1); } PG8_BAR; PG8_SCHED;
;         }
;         if (wr == 0) PG8_BAR;
	s_setprio 3
	s_add_i32 s42, s46, s51
	v_lshl_add_u64 v[244:245], s[40:41], 0, v[146:147]
	s_mov_b32 m0, s42
	ds_read_b128 v[210:213], v200 offset:49152
	ds_read_b128 v[214:217], v200 offset:51200
	ds_read_b128 v[218:221], v201 offset:49152
	ds_read_b128 v[222:225], v201 offset:51200
	ds_read_b128 v[226:229], v200 offset:53248
	ds_read_b128 v[230:233], v200 offset:55296
	ds_read_b128 v[234:237], v201 offset:53248
	ds_read_b128 v[238:241], v201 offset:55296
	global_load_lds_dwordx4 v[244:245], off
	s_add_i32 m0, s42, 0x2000
	s_add_u32 s38, s38, 0x84000
	v_lshl_add_u64 v[244:245], s[40:41], 0, v[148:149]
	s_addc_u32 s39, s39, 0
	s_add_i32 s40, s47, s51
	global_load_lds_dwordx4 v[244:245], off
	v_lshl_add_u64 v[244:245], s[38:39], 0, v[146:147]
	s_mov_b32 m0, s40
	v_lshl_add_u64 v[184:185], v[184:185], 0, s[16:17]
	global_load_lds_dwordx4 v[244:245], off
	v_lshl_add_u64 v[244:245], s[38:39], 0, v[148:149]
	s_add_i32 m0, s40, 0x2000
	s_nop 0
	global_load_lds_dwordx4 v[244:245], off
	s_mov_b32 m0, s57
	s_nop 0
	global_load_lds_dwordx4 v[184:185], off
	v_lshl_add_u64 v[184:185], v[242:243], 0, s[16:17]
	s_mov_b32 m0, s58
	s_nop 0
	global_load_lds_dwordx4 v[184:185], off
	s_waitcnt vmcnt(8)
	s_waitcnt lgkmcnt(0)
	s_barrier
	s_setprio 1
	s_waitcnt lgkmcnt(0)
	v_mfma_f32_16x16x32_bf16 v[110:113], v[90:93], v[210:213], v[110:113]
	v_mfma_f32_16x16x32_bf16 v[58:61], v[102:105], v[210:213], v[58:61]
	v_mfma_f32_16x16x32_bf16 v[94:97], v[90:93], v[214:217], v[94:97]
	v_mfma_f32_16x16x32_bf16 v[82:85], v[102:105], v[214:217], v[82:85]
	v_mfma_f32_16x16x32_bf16 v[66:69], v[90:93], v[226:229], v[66:69]
	v_mfma_f32_16x16x32_bf16 v[62:65], v[102:105], v[226:229], v[62:65]
	v_mfma_f32_16x16x32_bf16 v[42:45], v[90:93], v[230:233], v[42:45]
	v_mfma_f32_16x16x32_bf16 v[38:41], v[102:105], v[230:233], v[38:41]
	v_mfma_f32_16x16x32_bf16 v[110:113], v[98:101], v[218:221], v[110:113]
	v_mfma_f32_16x16x32_bf16 v[58:61], v[106:109], v[218:221], v[58:61]
	v_mfma_f32_16x16x32_bf16 v[94:97], v[98:101], v[222:225], v[94:97]
	v_mfma_f32_16x16x32_bf16 v[82:85], v[106:109], v[222:225], v[82:85]
	v_mfma_f32_16x16x32_bf16 v[66:69], v[98:101], v[234:237], v[66:69]
	v_mfma_f32_16x16x32_bf16 v[62:65], v[106:109], v[234:237], v[62:65]
	v_mfma_f32_16x16x32_bf16 v[42:45], v[98:101], v[238:241], v[42:45]
	v_mfma_f32_16x16x32_bf16 v[38:41], v[106:109], v[238:241], v[38:41]
	v_mfma_f32_16x16x32_bf16 v[74:77], v[168:171], v[210:213], v[74:77]
	v_mfma_f32_16x16x32_bf16 v[98:101], v[172:175], v[218:221], v[74:77]
	v_mfma_f32_16x16x32_bf16 v[74:77], v[168:171], v[214:217], v[78:81]
	v_mfma_f32_16x16x32_bf16 v[70:73], v[176:179], v[210:213], v[70:73]
	v_mfma_f32_16x16x32_bf16 v[90:93], v[172:175], v[222:225], v[74:77]
	v_mfma_f32_16x16x32_bf16 v[74:77], v[176:179], v[214:217], v[86:89]
	v_mfma_f32_16x16x32_bf16 v[54:57], v[168:171], v[226:229], v[54:57]
	v_mfma_f32_16x16x32_bf16 v[50:53], v[176:179], v[226:229], v[50:53]
	v_mfma_f32_16x16x32_bf16 v[6:9], v[168:171], v[230:233], v[6:9]
	v_mfma_f32_16x16x32_bf16 v[2:5], v[176:179], v[230:233], v[2:5]
	v_mfma_f32_16x16x32_bf16 v[70:73], v[180:183], v[218:221], v[70:73]
	v_mfma_f32_16x16x32_bf16 v[86:89], v[180:183], v[222:225], v[74:77]
	v_mfma_f32_16x16x32_bf16 v[54:57], v[172:175], v[234:237], v[54:57]
	v_mfma_f32_16x16x32_bf16 v[50:53], v[180:183], v[234:237], v[50:53]
	v_mfma_f32_16x16x32_bf16 v[6:9], v[172:175], v[238:241], v[6:9]
	v_mfma_f32_16x16x32_bf16 v[2:5], v[180:183], v[238:241], v[2:5]
	s_setprio 0
	s_barrier
	s_setprio 3
	s_add_i32 s45, s45, 2
	s_add_u32 s37, s37, 0x8000
	s_addc_u32 s44, s44, 0
	s_add_u32 s0, s0, 0x100
	s_addc_u32 s1, s1, 0
	s_cmp_gt_u32 s45, 29
	s_cbranch_scc0 .LBB0_1934
	s_and_b64 vcc, exec, s[18:19]
	s_cbranch_vccz .LBB0_1937
	s_barrier

; #define PG8_STAGE(bufoff, gbase, voff) do { _Pragma("unroll") for (int _i = 0; _i < 2; ++_i) \
;         __builtin_amdgcn_global_load_lds((const unsigned*)((const char*)(gbase) + (voff)[_i]), (LAS unsigned*)(lds + (bufoff) + ldsw + _i * 8192), 16, 0, 0); } while (0)
; #define PG8_LDA(dst, b, h) do { _Pragma("unroll") for (int m = 0; m < 4; ++m) _Pragma("unroll") for (int k = 0; k < 2; ++k) dst[m][k] = *(const LAS bf16x8*)(lds + PG8_SA(b, h) + ((aoff ^ (k * 64)) + m * 2048)); } while (0)
; #define PG8_LDB(dst, b, h) do { _Pragma("unroll") for (int n = 0; n < 2; ++n) _Pragma("unroll") for (int k = 0; k < 2; ++k) dst[n][k] = *(const LAS bf16x8*)(lds + PG8_SB(b, h) + ((boff ^ (k * 64)) + n * 2048)); } while (0)
; #define PG8_WAIT_V(n) asm volatile("s_waitcnt vmcnt(" #n ")" ::: "memory")
; #define PG8_BAR __builtin_amdgcn_s_barrier()
;     ...
;         for (int t = 0; t < nt; t += 2) {
;             const bool last = (t == nt - 2);
;             const char* a1 = cA + (size_t)(t + 1) * kstepA;
;             const char* a2 = last ? nA : cA + (size_t)(t + 2) * kstepA; const char* b2 = last ? nB : cB + (size_t)(t + 2) * kstepB;
;             const char* a3 = a2 + kstepA; const char* b3 = b2 + kstepB;
;             unsigned vs[2][2];
;             if constexpr (GATHER) {
;                 if (last && has_next) {
; #pragma unroll
;                     for (int hh = 0; hh < 2; ++hh)
; #pragma unroll
;                         for (int i = 0; i < 2; ++i) voffN[hh][i] = (unsigned)idxl[(ui + 1) * 256 + hh * HALF + sR[i]] * (unsigned)(K * 2) + (unsigned)sC[i] * 2u;
;                 }
; #pragma unroll
;                 for (int hh = 0; hh < 2; ++hh)
; #pragma unroll
;                     for (int i = 0; i < 2; ++i) vs[hh][i] = last ? voffN[hh][i] : voffA[hh][i];
;             } else {
; #pragma unroll
;                 for (int hh = 0; hh < 2; ++hh)
; #pragma unroll
;                     for (int i = 0; i < 2; ++i) vs[hh][i] = voffA[hh][i];
;             }
;             PG8_LDB(B0, 0, 0); PG8_LDB(B1, 0, 1); PG8_SCHED; PG8_LDA(At, 0, 0); PG8_STAGE(PG8_SA(1, 1), a1, voffA[1]);
;             PG8_WAIT_V(8); PG8_WAIT_L(0); PG8_BAR; if (do0) { PG8_MMA(0, 0, At, B0); PG8_MMA(0, 1, At, B1); } PG8_BAR; PG8_SCHED;
;             PG8_LDA(At, 0, 1); PG8_STAGE(PG8_SB(0, 0), b2, voffB); PG8_STAGE(PG8_SB(0, 1), b2 + hstep, voffB); PG8_STAGE(PG8_SA(0, 0), a2, vs[0]);
.LBB0_2337:
	v_add_u32_e32 v136, s43, v159
	v_add_u32_e32 v145, s43, v160
	ds_read_b128 v[166:169], v136
	ds_read_b128 v[170:173], v145
	v_add_u32_e32 v136, s44, v159
	s_add_u32 s22, s90, s20
	v_add_u32_e32 v145, s44, v160
	ds_read_b128 v[174:177], v136
	ds_read_b128 v[178:181], v145
	v_add_u32_e32 v136, s45, v159
	s_addc_u32 s23, s91, s21
	v_add_u32_e32 v145, s45, v160
	ds_read_b128 v[182:185], v136
	ds_read_b128 v[186:189], v145
	v_add_u32_e32 v136, s46, v159
	s_add_u32 s24, s22, 0x4213700
	v_add_u32_e32 v145, s46, v160
	ds_read_b128 v[190:193], v136
	ds_read_b128 v[194:197], v145
	s_addc_u32 s25, s23, 0
	s_and_b64 s[22:23], s[2:3], exec
	s_cselect_b32 s22, s14, s13
	s_cselect_b32 s27, s83, s25
	s_cselect_b32 s26, s82, s24
	s_cselect_b32 s23, s15, s53
	s_add_u32 s24, s22, 0x4000
	s_addc_u32 s25, s23, 0
	v_cndmask_b32_e64 v136, v152, v146, s[2:3]
	v_cndmask_b32_e64 v232, v153, v147, s[2:3]
	v_cndmask_b32_e64 v145, v148, v164, s[2:3]
	v_cndmask_b32_e64 v149, v150, v165, s[2:3]
	v_lshl_add_u64 v[234:235], v[156:157], 0, s[20:21]
	s_add_i32 m0, s17, 0xc000
	ds_read_b128 v[200:203], v161
	ds_read_b128 v[204:207], v161 offset:2048
	ds_read_b128 v[208:211], v162
	ds_read_b128 v[212:215], v162 offset:2048
	ds_read_b128 v[216:219], v161 offset:4096
	ds_read_b128 v[220:223], v161 offset:6144
	ds_read_b128 v[224:227], v162 offset:4096
	ds_read_b128 v[228:231], v162 offset:6144
	global_load_lds_dwordx4 v[234:235], off
	v_lshl_add_u64 v[234:235], v[154:155], 0, s[20:21]
	s_add_i32 m0, s17, 0xe000
	s_nop 0
	global_load_lds_dwordx4 v[234:235], off
	s_waitcnt vmcnt(8)
	s_waitcnt lgkmcnt(0)
	s_barrier
	s_setprio 1
	s_waitcnt lgkmcnt(0)
	v_mfma_f32_16x16x32_bf16 v[126:129], v[166:169], v[200:203], v[126:129]
	v_mfma_f32_16x16x32_bf16 v[122:125], v[174:177], v[200:203], v[122:125]
	v_mfma_f32_16x16x32_bf16 v[110:113], v[166:169], v[204:207], v[110:113]
	v_mfma_f32_16x16x32_bf16 v[106:109], v[174:177], v[204:207], v[106:109]
	v_mfma_f32_16x16x32_bf16 v[94:97], v[166:169], v[216:219], v[94:97]
	v_mfma_f32_16x16x32_bf16 v[90:93], v[174:177], v[216:219], v[90:93]
	v_mfma_f32_16x16x32_bf16 v[78:81], v[166:169], v[220:223], v[78:81]
	v_mfma_f32_16x16x32_bf16 v[74:77], v[174:177], v[220:223], v[74:77]
	v_mfma_f32_16x16x32_bf16 v[126:129], v[170:173], v[208:211], v[126:129]
	v_mfma_f32_16x16x32_bf16 v[122:125], v[178:181], v[208:211], v[122:125]
	v_mfma_f32_16x16x32_bf16 v[110:113], v[170:173], v[212:215], v[110:113]
	v_mfma_f32_16x16x32_bf16 v[106:109], v[178:181], v[212:215], v[106:109]
	v_mfma_f32_16x16x32_bf16 v[94:97], v[170:173], v[224:227], v[94:97]
	v_mfma_f32_16x16x32_bf16 v[90:93], v[178:181], v[224:227], v[90:93]
	v_mfma_f32_16x16x32_bf16 v[78:81], v[170:173], v[228:231], v[78:81]
	v_mfma_f32_16x16x32_bf16 v[74:77], v[178:181], v[228:231], v[74:77]
	v_mfma_f32_16x16x32_bf16 v[118:121], v[182:185], v[200:203], v[118:121]
	v_mfma_f32_16x16x32_bf16 v[114:117], v[190:193], v[200:203], v[114:117]
	v_mfma_f32_16x16x32_bf16 v[102:105], v[182:185], v[204:207], v[102:105]
	v_mfma_f32_16x16x32_bf16 v[98:101], v[190:193], v[204:207], v[98:101]
	v_mfma_f32_16x16x32_bf16 v[86:89], v[182:185], v[216:219], v[86:89]
	v_mfma_f32_16x16x32_bf16 v[82:85], v[190:193], v[216:219], v[82:85]
	v_mfma_f32_16x16x32_bf16 v[70:73], v[182:185], v[220:223], v[70:73]
	v_mfma_f32_16x16x32_bf16 v[66:69], v[190:193], v[220:223], v[66:69]
	v_mfma_f32_16x16x32_bf16 v[118:121], v[186:189], v[208:211], v[118:121]
	v_mfma_f32_16x16x32_bf16 v[114:117], v[194:197], v[208:211], v[114:117]
	v_mfma_f32_16x16x32_bf16 v[102:105], v[186:189], v[212:215], v[102:105]
	v_mfma_f32_16x16x32_bf16 v[98:101], v[194:197], v[212:215], v[98:101]
	v_mfma_f32_16x16x32_bf16 v[86:89], v[186:189], v[224:227], v[86:89]
	v_mfma_f32_16x16x32_bf16 v[82:85], v[194:197], v[224:227], v[82:85]
	v_mfma_f32_16x16x32_bf16 v[70:73], v[186:189], v[228:231], v[70:73]
	v_mfma_f32_16x16x32_bf16 v[66:69], v[194:197], v[228:231], v[66:69]
	s_setprio 0
	s_barrier
	s_setprio 3
	s_add_i32 s2, s43, s34
	v_lshl_add_u64 v[234:235], s[22:23], 0, v[132:133]
	s_mov_b32 m0, s2
	ds_read_b128 v[200:203], v161 offset:16384
	ds_read_b128 v[204:207], v161 offset:18432
	ds_read_b128 v[208:211], v162 offset:16384
	ds_read_b128 v[212:215], v162 offset:18432
	ds_read_b128 v[216:219], v161 offset:20480
	ds_read_b128 v[220:223], v161 offset:22528
	ds_read_b128 v[224:227], v162 offset:20480
	ds_read_b128 v[228:231], v162 offset:22528
	global_load_lds_dwordx4 v[234:235], off
	s_add_i32 m0, s2, 0x2000
	s_add_u32 s2, s22, 0x40000
	v_lshl_add_u64 v[234:235], s[22:23], 0, v[134:135]
	s_addc_u32 s3, s23, 0
	s_add_i32 s55, s45, s34
	global_load_lds_dwordx4 v[234:235], off
	v_lshl_add_u64 v[234:235], s[2:3], 0, v[132:133]
	s_mov_b32 m0, s55
	v_mov_b32_e32 v233, v137
	global_load_lds_dwordx4 v[234:235], off
	v_lshl_add_u64 v[234:235], s[2:3], 0, v[134:135]
	s_add_i32 m0, s55, 0x2000
	s_nop 0
	global_load_lds_dwordx4 v[234:235], off
	s_mov_b32 m0, s17
	v_lshl_add_u64 v[234:235], s[26:27], 0, v[136:137]
	global_load_lds_dwordx4 v136, s[26:27]
	s_mov_b32 m0, s35
	s_nop 0
	global_load_lds_dwordx4 v232, s[26:27]
	s_waitcnt vmcnt(8)
	s_waitcnt lgkmcnt(0)
	v_lshl_add_u64 v[232:233], s[26:27], 0, v[232:233]
	s_barrier
; #define PG8_STAGE(bufoff, gbase, voff) do { _Pragma("unroll") for (int _i = 0; _i < 2; ++_i) \
;         __builtin_amdgcn_global_load_lds((const unsigned*)((const char*)(gbase) + (voff)[_i]), (LAS unsigned*)(lds + (bufoff) + ldsw + _i * 8192), 16, 0, 0); } while (0)
; #define PG8_LDA(dst, b, h) do { _Pragma("unroll") for (int m = 0; m < 4; ++m) _Pragma("unroll") for (int k = 0; k < 2; ++k) dst[m][k] = *(const LAS bf16x8*)(lds + PG8_SA(b, h) + ((aoff ^ (k * 64)) + m * 2048)); } while (0)
; #define PG8_LDB(dst, b, h) do { _Pragma("unroll") for (int n = 0; n < 2; ++n) _Pragma("unroll") for (int k = 0; k < 2; ++k) dst[n][k] = *(const LAS bf16x8*)(lds + PG8_SB(b, h) + ((boff ^ (k * 64)) + n * 2048)); } while (0)
; #define PG8_MMA(ai, bj, At, Bt) do { __builtin_amdgcn_s_setprio(1); _Pragma("unroll") for (int m = 0; m < 4; ++m) _Pragma("unroll") for (int n = 0; n < 2; ++n) _Pragma("unroll") for (int k = 0; k < 2; ++k) \
;         acc[ai][bj][m][n] = __builtin_amdgcn_mfma_f32_16x16x32_bf16(Bt[n][k], At[m][k], acc[ai][bj][m][n], 0, 0, 0); __builtin_amdgcn_s_setprio(0); } while (0)
; #define PG8_WAIT_V(n) asm volatile("s_waitcnt vmcnt(" #n ")" ::: "memory")
; #define PG8_WAIT_L(n) asm volatile("s_waitcnt lgkmcnt(" #n ")" ::: "memory")
; #define PG8_BAR __builtin_amdgcn_s_barrier()
; #define PG8_SCHED __builtin_amdgcn_sched_barrier(0)
;     ...
;             PG8_WAIT_V(8); PG8_WAIT_L(0); PG8_BAR; if (do1) { PG8_MMA(1, 0, At, B0); PG8_MMA(1, 1, At, B1); } PG8_BAR; PG8_SCHED;
;             PG8_LDB(B0, 1, 0); PG8_LDB(B1, 1, 1); PG8_SCHED; PG8_LDA(At, 1, 0); PG8_STAGE(PG8_SA(0, 1), a2, vs[1]);
;             PG8_WAIT_V(8); PG8_WAIT_L(0); PG8_BAR; if (do0) { PG8_MMA(0, 0, At, B0); PG8_MMA(0, 1, At, B1); } PG8_BAR; PG8_SCHED;
	s_setprio 1
	s_waitcnt lgkmcnt(0)
	v_mfma_f32_16x16x32_bf16 v[62:65], v[166:169], v[200:203], v[62:65]
	v_mfma_f32_16x16x32_bf16 v[58:61], v[174:177], v[200:203], v[58:61]
	v_mfma_f32_16x16x32_bf16 v[46:49], v[166:169], v[204:207], v[46:49]
	v_mfma_f32_16x16x32_bf16 v[42:45], v[174:177], v[204:207], v[42:45]
	v_mfma_f32_16x16x32_bf16 v[30:33], v[166:169], v[216:219], v[30:33]
	v_mfma_f32_16x16x32_bf16 v[26:29], v[174:177], v[216:219], v[26:29]
	v_mfma_f32_16x16x32_bf16 v[14:17], v[166:169], v[220:223], v[14:17]
	v_mfma_f32_16x16x32_bf16 v[10:13], v[174:177], v[220:223], v[10:13]
	v_mfma_f32_16x16x32_bf16 v[62:65], v[170:173], v[208:211], v[62:65]
	v_mfma_f32_16x16x32_bf16 v[58:61], v[178:181], v[208:211], v[58:61]
	v_mfma_f32_16x16x32_bf16 v[46:49], v[170:173], v[212:215], v[46:49]
	v_mfma_f32_16x16x32_bf16 v[42:45], v[178:181], v[212:215], v[42:45]
	v_mfma_f32_16x16x32_bf16 v[30:33], v[170:173], v[224:227], v[30:33]
	v_mfma_f32_16x16x32_bf16 v[26:29], v[178:181], v[224:227], v[26:29]
	v_mfma_f32_16x16x32_bf16 v[14:17], v[170:173], v[228:231], v[14:17]
	v_mfma_f32_16x16x32_bf16 v[10:13], v[178:181], v[228:231], v[10:13]
	v_mfma_f32_16x16x32_bf16 v[54:57], v[182:185], v[200:203], v[54:57]
	v_mfma_f32_16x16x32_bf16 v[50:53], v[190:193], v[200:203], v[50:53]
	v_mfma_f32_16x16x32_bf16 v[38:41], v[182:185], v[204:207], v[38:41]
	v_mfma_f32_16x16x32_bf16 v[34:37], v[190:193], v[204:207], v[34:37]
	v_mfma_f32_16x16x32_bf16 v[22:25], v[182:185], v[216:219], v[22:25]
	v_mfma_f32_16x16x32_bf16 v[18:21], v[190:193], v[216:219], v[18:21]
	v_mfma_f32_16x16x32_bf16 v[6:9], v[182:185], v[220:223], v[6:9]
	v_mfma_f32_16x16x32_bf16 v[2:5], v[190:193], v[220:223], v[2:5]
	v_mfma_f32_16x16x32_bf16 v[54:57], v[186:189], v[208:211], v[54:57]
	v_mfma_f32_16x16x32_bf16 v[50:53], v[194:197], v[208:211], v[50:53]
	v_mfma_f32_16x16x32_bf16 v[38:41], v[186:189], v[212:215], v[38:41]
	v_mfma_f32_16x16x32_bf16 v[34:37], v[194:197], v[212:215], v[34:37]
	v_mfma_f32_16x16x32_bf16 v[22:25], v[186:189], v[224:227], v[22:25]
	v_mfma_f32_16x16x32_bf16 v[18:21], v[194:197], v[224:227], v[18:21]
	v_mfma_f32_16x16x32_bf16 v[6:9], v[186:189], v[228:231], v[6:9]
	v_mfma_f32_16x16x32_bf16 v[2:5], v[194:197], v[228:231], v[2:5]
	s_setprio 0
	s_barrier
	s_setprio 3
	s_add_i32 s2, 0, 0x18000
	v_add_u32_e32 v136, s2, v159
	v_add_u32_e32 v151, s2, v160
	ds_read_b128 v[166:169], v136
	ds_read_b128 v[170:173], v151
	v_add_u32_e32 v136, s47, v159
	s_add_i32 s55, 0, 0x1c000
	v_add_u32_e32 v151, s47, v160
	ds_read_b128 v[174:177], v136
	ds_read_b128 v[178:181], v151
	v_add_u32_e32 v136, s55, v159
	v_add_u32_e32 v151, s55, v160
	ds_read_b128 v[182:185], v136
	ds_read_b128 v[186:189], v151
	v_add_u32_e32 v136, s48, v159
	v_add_u32_e32 v151, s48, v160
	ds_read_b128 v[190:193], v136
	ds_read_b128 v[194:197], v151
	s_mov_b32 m0, s36
	ds_read_b128 v[200:203], v161 offset:32768
	ds_read_b128 v[204:207], v161 offset:34816
	ds_read_b128 v[208:211], v162 offset:32768
	ds_read_b128 v[212:215], v162 offset:34816
	ds_read_b128 v[216:219], v161 offset:36864
	ds_read_b128 v[220:223], v161 offset:38912
	ds_read_b128 v[224:227], v162 offset:36864
	ds_read_b128 v[228:231], v162 offset:38912
	global_load_lds_dwordx4 v145, s[26:27]
	s_mov_b32 m0, s37
	s_nop 0
	global_load_lds_dwordx4 v149, s[26:27]
	s_waitcnt vmcnt(8)
	s_waitcnt lgkmcnt(0)
	s_barrier
	s_setprio 1
	s_waitcnt lgkmcnt(0)
	v_mfma_f32_16x16x32_bf16 v[126:129], v[166:169], v[200:203], v[126:129]
	v_mfma_f32_16x16x32_bf16 v[122:125], v[174:177], v[200:203], v[122:125]
	v_mfma_f32_16x16x32_bf16 v[110:113], v[166:169], v[204:207], v[110:113]
	v_mfma_f32_16x16x32_bf16 v[106:109], v[174:177], v[204:207], v[106:109]
	v_mfma_f32_16x16x32_bf16 v[94:97], v[166:169], v[216:219], v[94:97]
	v_mfma_f32_16x16x32_bf16 v[90:93], v[174:177], v[216:219], v[90:93]
	v_mfma_f32_16x16x32_bf16 v[78:81], v[166:169], v[220:223], v[78:81]
	v_mfma_f32_16x16x32_bf16 v[74:77], v[174:177], v[220:223], v[74:77]
	v_mfma_f32_16x16x32_bf16 v[126:129], v[170:173], v[208:211], v[126:129]
	v_mfma_f32_16x16x32_bf16 v[122:125], v[178:181], v[208:211], v[122:125]
	v_mfma_f32_16x16x32_bf16 v[110:113], v[170:173], v[212:215], v[110:113]
	v_mfma_f32_16x16x32_bf16 v[106:109], v[178:181], v[212:215], v[106:109]
	v_mfma_f32_16x16x32_bf16 v[94:97], v[170:173], v[224:227], v[94:97]
	v_mfma_f32_16x16x32_bf16 v[90:93], v[178:181], v[224:227], v[90:93]
	v_mfma_f32_16x16x32_bf16 v[78:81], v[170:173], v[228:231], v[78:81]
	v_mfma_f32_16x16x32_bf16 v[74:77], v[178:181], v[228:231], v[74:77]
	v_mfma_f32_16x16x32_bf16 v[118:121], v[182:185], v[200:203], v[118:121]
	v_mfma_f32_16x16x32_bf16 v[114:117], v[190:193], v[200:203], v[114:117]
	v_mfma_f32_16x16x32_bf16 v[102:105], v[182:185], v[204:207], v[102:105]
	v_mfma_f32_16x16x32_bf16 v[98:101], v[190:193], v[204:207], v[98:101]
	v_mfma_f32_16x16x32_bf16 v[86:89], v[182:185], v[216:219], v[86:89]
	v_mfma_f32_16x16x32_bf16 v[82:85], v[190:193], v[216:219], v[82:85]
	v_mfma_f32_16x16x32_bf16 v[70:73], v[182:185], v[220:223], v[70:73]
	v_mfma_f32_16x16x32_bf16 v[66:69], v[190:193], v[220:223], v[66:69]
	v_mfma_f32_16x16x32_bf16 v[118:121], v[186:189], v[208:211], v[118:121]
	v_mfma_f32_16x16x32_bf16 v[114:117], v[194:197], v[208:211], v[114:117]
	v_mfma_f32_16x16x32_bf16 v[102:105], v[186:189], v[212:215], v[102:105]
	v_mfma_f32_16x16x32_bf16 v[98:101], v[194:197], v[212:215], v[98:101]
	v_mfma_f32_16x16x32_bf16 v[86:89], v[186:189], v[224:227], v[86:89]
	v_mfma_f32_16x16x32_bf16 v[82:85], v[194:197], v[224:227], v[82:85]
	v_mfma_f32_16x16x32_bf16 v[70:73], v[186:189], v[228:231], v[70:73]
	v_mfma_f32_16x16x32_bf16 v[66:69], v[194:197], v[228:231], v[66:69]
	s_setprio 0
	s_barrier
; #define PG8_STAGE(bufoff, gbase, voff) do { _Pragma("unroll") for (int _i = 0; _i < 2; ++_i) \
;         __builtin_amdgcn_global_load_lds((const unsigned*)((const char*)(gbase) + (voff)[_i]), (LAS unsigned*)(lds + (bufoff) + ldsw + _i * 8192), 16, 0, 0); } while (0)
; #define PG8_LDA(dst, b, h) do { _Pragma("unroll") for (int m = 0; m < 4; ++m) _Pragma("unroll") for (int k = 0; k < 2; ++k) dst[m][k] = *(const LAS bf16x8*)(lds + PG8_SA(b, h) + ((aoff ^ (k * 64)) + m * 2048)); } while (0)
; #define PG8_MMA(ai, bj, At, Bt) do { __builtin_amdgcn_s_setprio(1); _Pragma("unroll") for (int m = 0; m < 4; ++m) _Pragma("unroll") for (int n = 0; n < 2; ++n) _Pragma("unroll") for (int k = 0; k < 2; ++k) \
;         acc[ai][bj][m][n] = __builtin_amdgcn_mfma_f32_16x16x32_bf16(Bt[n][k], At[m][k], acc[ai][bj][m][n], 0, 0, 0); __builtin_amdgcn_s_setprio(0); } while (0)
; #define PG8_WAIT_V(n) asm volatile("s_waitcnt vmcnt(" #n ")" ::: "memory")
; #define PG8_WAIT_L(n) asm volatile("s_waitcnt lgkmcnt(" #n ")" ::: "memory")
; #define PG8_BAR __builtin_amdgcn_s_barrier()
; #define PG8_SCHED __builtin_amdgcn_sched_barrier(0)
;     ...
;             PG8_LDA(At, 1, 1); PG8_STAGE(PG8_SB(1, 0), b3, voffB); PG8_STAGE(PG8_SB(1, 1), b3 + hstep, voffB); PG8_STAGE(PG8_SA(1, 0), a3, vs[0]);
;             PG8_WAIT_V(8); PG8_WAIT_L(0); PG8_BAR; if (do1) { PG8_MMA(1, 0, At, B0); PG8_MMA(1, 1, At, B1); } PG8_BAR; PG8_SCHED;
;         }
	s_setprio 3
	s_add_i32 s2, s2, s34
	v_lshl_add_u64 v[236:237], s[24:25], 0, v[132:133]
	s_mov_b32 m0, s2
	ds_read_b128 v[200:203], v161 offset:49152
	ds_read_b128 v[204:207], v161 offset:51200
	ds_read_b128 v[208:211], v162 offset:49152
	ds_read_b128 v[212:215], v162 offset:51200
	ds_read_b128 v[216:219], v161 offset:53248
	ds_read_b128 v[220:223], v161 offset:55296
	ds_read_b128 v[224:227], v162 offset:53248
	ds_read_b128 v[228:231], v162 offset:55296
	global_load_lds_dwordx4 v[236:237], off
	s_add_i32 m0, s2, 0x2000
	s_add_u32 s2, s22, 0x44000
	v_lshl_add_u64 v[236:237], s[24:25], 0, v[134:135]
	s_addc_u32 s3, s23, 0
	s_add_i32 s22, s55, s34
	global_load_lds_dwordx4 v[236:237], off
	v_lshl_add_u64 v[236:237], s[2:3], 0, v[132:133]
	s_mov_b32 m0, s22
	v_lshl_add_u64 v[234:235], v[234:235], 0, s[10:11]
	global_load_lds_dwordx4 v[236:237], off
	v_lshl_add_u64 v[236:237], s[2:3], 0, v[134:135]
	s_add_i32 m0, s22, 0x2000
	v_lshl_add_u64 v[232:233], v[232:233], 0, s[10:11]
	global_load_lds_dwordx4 v[236:237], off
	s_mov_b32 m0, s41
	s_nop 0
	global_load_lds_dwordx4 v[234:235], off
	s_mov_b32 m0, s42
	s_nop 0
	global_load_lds_dwordx4 v[232:233], off
	s_waitcnt vmcnt(8)
	s_waitcnt lgkmcnt(0)
	s_barrier
	s_setprio 1
	s_waitcnt lgkmcnt(0)
	v_mfma_f32_16x16x32_bf16 v[62:65], v[166:169], v[200:203], v[62:65]
	v_mfma_f32_16x16x32_bf16 v[58:61], v[174:177], v[200:203], v[58:61]
	v_mfma_f32_16x16x32_bf16 v[46:49], v[166:169], v[204:207], v[46:49]
	v_mfma_f32_16x16x32_bf16 v[42:45], v[174:177], v[204:207], v[42:45]
	v_mfma_f32_16x16x32_bf16 v[30:33], v[166:169], v[216:219], v[30:33]
	v_mfma_f32_16x16x32_bf16 v[26:29], v[174:177], v[216:219], v[26:29]
	v_mfma_f32_16x16x32_bf16 v[14:17], v[166:169], v[220:223], v[14:17]
	v_mfma_f32_16x16x32_bf16 v[10:13], v[174:177], v[220:223], v[10:13]
	v_mfma_f32_16x16x32_bf16 v[62:65], v[170:173], v[208:211], v[62:65]
	v_mfma_f32_16x16x32_bf16 v[58:61], v[178:181], v[208:211], v[58:61]
	v_mfma_f32_16x16x32_bf16 v[46:49], v[170:173], v[212:215], v[46:49]
	v_mfma_f32_16x16x32_bf16 v[42:45], v[178:181], v[212:215], v[42:45]
	v_mfma_f32_16x16x32_bf16 v[30:33], v[170:173], v[224:227], v[30:33]
	v_mfma_f32_16x16x32_bf16 v[26:29], v[178:181], v[224:227], v[26:29]
	v_mfma_f32_16x16x32_bf16 v[14:17], v[170:173], v[228:231], v[14:17]
	v_mfma_f32_16x16x32_bf16 v[10:13], v[178:181], v[228:231], v[10:13]
	v_mfma_f32_16x16x32_bf16 v[54:57], v[182:185], v[200:203], v[54:57]
	v_mfma_f32_16x16x32_bf16 v[50:53], v[190:193], v[200:203], v[50:53]
	v_mfma_f32_16x16x32_bf16 v[38:41], v[182:185], v[204:207], v[38:41]
	v_mfma_f32_16x16x32_bf16 v[34:37], v[190:193], v[204:207], v[34:37]
	v_mfma_f32_16x16x32_bf16 v[22:25], v[182:185], v[216:219], v[22:25]
	v_mfma_f32_16x16x32_bf16 v[18:21], v[190:193], v[216:219], v[18:21]
	v_mfma_f32_16x16x32_bf16 v[6:9], v[182:185], v[220:223], v[6:9]
	v_mfma_f32_16x16x32_bf16 v[2:5], v[190:193], v[220:223], v[2:5]
	v_mfma_f32_16x16x32_bf16 v[54:57], v[186:189], v[208:211], v[54:57]
	v_mfma_f32_16x16x32_bf16 v[50:53], v[194:197], v[208:211], v[50:53]
	v_mfma_f32_16x16x32_bf16 v[38:41], v[186:189], v[212:215], v[38:41]
	v_mfma_f32_16x16x32_bf16 v[34:37], v[194:197], v[212:215], v[34:37]
	v_mfma_f32_16x16x32_bf16 v[22:25], v[186:189], v[224:227], v[22:25]
	v_mfma_f32_16x16x32_bf16 v[18:21], v[194:197], v[224:227], v[18:21]
	v_mfma_f32_16x16x32_bf16 v[6:9], v[186:189], v[228:231], v[6:9]
	v_mfma_f32_16x16x32_bf16 v[2:5], v[194:197], v[228:231], v[2:5]
	s_setprio 0
	s_barrier
	s_setprio 3
	s_add_i32 s54, s54, 2
	s_add_u32 s13, s13, 0x8000
	s_addc_u32 s53, s53, 0
	s_add_u32 s20, s20, 0x100
	s_addc_u32 s21, s21, 0
	s_cmp_gt_u32 s54, 13
	s_cbranch_scc1 .LBB0_2340

; #define PG8_STAGE(bufoff, gbase, voff) do { _Pragma("unroll") for (int _i = 0; _i < 2; ++_i) \
;         __builtin_amdgcn_global_load_lds((const unsigned*)((const char*)(gbase) + (voff)[_i]), (LAS unsigned*)(lds + (bufoff) + ldsw + _i * 8192), 16, 0, 0); } while (0)
; #define PG8_LDA(dst, b, h) do { _Pragma("unroll") for (int m = 0; m < 4; ++m) _Pragma("unroll") for (int k = 0; k < 2; ++k) dst[m][k] = *(const LAS bf16x8*)(lds + PG8_SA(b, h) + ((aoff ^ (k * 64)) + m * 2048)); } while (0)
; #define PG8_LDB(dst, b, h) do { _Pragma("unroll") for (int n = 0; n < 2; ++n) _Pragma("unroll") for (int k = 0; k < 2; ++k) dst[n][k] = *(const LAS bf16x8*)(lds + PG8_SB(b, h) + ((boff ^ (k * 64)) + n * 2048)); } while (0)
; #define PG8_WAIT_V(n) asm volatile("s_waitcnt vmcnt(" #n ")" ::: "memory")
; #define PG8_BAR __builtin_amdgcn_s_barrier()
;     ...
;         for (int t = 0; t < nt; t += 2) {
;             const bool last = (t == nt - 2);
;             const char* a1 = cA + (size_t)(t + 1) * kstepA;
;             const char* a2 = last ? nA : cA + (size_t)(t + 2) * kstepA; const char* b2 = last ? nB : cB + (size_t)(t + 2) * kstepB;
;             const char* a3 = a2 + kstepA; const char* b3 = b2 + kstepB;
;             unsigned vs[2][2];
;             if constexpr (GATHER) {
;                 if (last && has_next) {
; #pragma unroll
;                     for (int hh = 0; hh < 2; ++hh)
; #pragma unroll
;                         for (int i = 0; i < 2; ++i) voffN[hh][i] = (unsigned)idxl[(ui + 1) * 256 + hh * HALF + sR[i]] * (unsigned)(K * 2) + (unsigned)sC[i] * 2u;
;                 }
; #pragma unroll
;                 for (int hh = 0; hh < 2; ++hh)
; #pragma unroll
;                     for (int i = 0; i < 2; ++i) vs[hh][i] = last ? voffN[hh][i] : voffA[hh][i];
;             } else {
; #pragma unroll
;                 for (int hh = 0; hh < 2; ++hh)
; #pragma unroll
;                     for (int i = 0; i < 2; ++i) vs[hh][i] = voffA[hh][i];
;             }
;             PG8_LDB(B0, 0, 0); PG8_LDB(B1, 0, 1); PG8_SCHED; PG8_LDA(At, 0, 0); PG8_STAGE(PG8_SA(1, 1), a1, voffA[1]);
;             PG8_WAIT_V(8); PG8_WAIT_L(0); PG8_BAR; if (do0) { PG8_MMA(0, 0, At, B0); PG8_MMA(0, 1, At, B1); } PG8_BAR; PG8_SCHED;
;             PG8_LDA(At, 0, 1); PG8_STAGE(PG8_SB(0, 0), b2, voffB); PG8_STAGE(PG8_SB(0, 1), b2 + hstep, voffB); PG8_STAGE(PG8_SA(0, 0), a2, vs[0]);
.LBB0_2411:
	ds_read_b128 v[146:149], v153
	ds_read_b128 v[168:171], v154
	ds_read_b128 v[172:175], v155
	ds_read_b128 v[176:179], v156
	ds_read_b128 v[180:183], v157
	ds_read_b128 v[184:187], v158
	ds_read_b128 v[188:191], v159
	ds_read_b128 v[192:195], v160
	s_add_u32 s20, s18, 0x4000
	s_addc_u32 s21, s19, 0
	s_cmp_eq_u32 s56, 40
	s_cselect_b32 s26, s14, s20
	s_cselect_b32 s27, s15, s21
	s_cselect_b32 s22, s16, s54
	s_cselect_b32 s23, s17, s55
	s_add_u32 s20, s26, 0x4000
	s_addc_u32 s21, s27, 0
	v_lshl_add_u64 v[196:197], s[18:19], 0, v[142:143]
	s_add_i32 m0, s34, 0xc000
	ds_read_b128 v[200:203], v161
	ds_read_b128 v[204:207], v161 offset:2048
	ds_read_b128 v[208:211], v162
	ds_read_b128 v[212:215], v162 offset:2048
	ds_read_b128 v[216:219], v161 offset:4096
	ds_read_b128 v[220:223], v161 offset:6144
	ds_read_b128 v[224:227], v162 offset:4096
	ds_read_b128 v[228:231], v162 offset:6144
	global_load_lds_dwordx4 v[196:197], off
	v_lshl_add_u64 v[196:197], s[18:19], 0, v[144:145]
	s_add_i32 m0, s34, 0xe000
	s_add_u32 s24, s22, 0x4000
	global_load_lds_dwordx4 v[196:197], off
	s_waitcnt vmcnt(8)
	s_waitcnt lgkmcnt(0)
	s_addc_u32 s25, s23, 0
	s_barrier
	s_setprio 1
	s_waitcnt lgkmcnt(0)
	v_mfma_f32_16x16x32_bf16 v[126:129], v[146:149], v[200:203], v[126:129]
	v_mfma_f32_16x16x32_bf16 v[122:125], v[172:175], v[200:203], v[122:125]
	v_mfma_f32_16x16x32_bf16 v[114:117], v[146:149], v[204:207], v[114:117]
	v_mfma_f32_16x16x32_bf16 v[106:109], v[172:175], v[204:207], v[106:109]
	v_mfma_f32_16x16x32_bf16 v[98:101], v[146:149], v[216:219], v[98:101]
	v_mfma_f32_16x16x32_bf16 v[90:93], v[172:175], v[216:219], v[90:93]
	v_mfma_f32_16x16x32_bf16 v[82:85], v[146:149], v[220:223], v[82:85]
	v_mfma_f32_16x16x32_bf16 v[74:77], v[172:175], v[220:223], v[74:77]
	v_mfma_f32_16x16x32_bf16 v[126:129], v[168:171], v[208:211], v[126:129]
	v_mfma_f32_16x16x32_bf16 v[122:125], v[176:179], v[208:211], v[122:125]
	v_mfma_f32_16x16x32_bf16 v[114:117], v[168:171], v[212:215], v[114:117]
	v_mfma_f32_16x16x32_bf16 v[106:109], v[176:179], v[212:215], v[106:109]
	v_mfma_f32_16x16x32_bf16 v[98:101], v[168:171], v[224:227], v[98:101]
	v_mfma_f32_16x16x32_bf16 v[90:93], v[176:179], v[224:227], v[90:93]
	v_mfma_f32_16x16x32_bf16 v[82:85], v[168:171], v[228:231], v[82:85]
	v_mfma_f32_16x16x32_bf16 v[74:77], v[176:179], v[228:231], v[74:77]
	v_mfma_f32_16x16x32_bf16 v[118:121], v[180:183], v[200:203], v[118:121]
	v_mfma_f32_16x16x32_bf16 v[110:113], v[188:191], v[200:203], v[110:113]
	v_mfma_f32_16x16x32_bf16 v[102:105], v[180:183], v[204:207], v[102:105]
	v_mfma_f32_16x16x32_bf16 v[94:97], v[188:191], v[204:207], v[94:97]
	v_mfma_f32_16x16x32_bf16 v[86:89], v[180:183], v[216:219], v[86:89]
	v_mfma_f32_16x16x32_bf16 v[78:81], v[188:191], v[216:219], v[78:81]
	v_mfma_f32_16x16x32_bf16 v[70:73], v[180:183], v[220:223], v[70:73]
	v_mfma_f32_16x16x32_bf16 v[66:69], v[188:191], v[220:223], v[66:69]
	v_mfma_f32_16x16x32_bf16 v[118:121], v[184:187], v[208:211], v[118:121]
	v_mfma_f32_16x16x32_bf16 v[110:113], v[192:195], v[208:211], v[110:113]
	v_mfma_f32_16x16x32_bf16 v[102:105], v[184:187], v[212:215], v[102:105]
	v_mfma_f32_16x16x32_bf16 v[94:97], v[192:195], v[212:215], v[94:97]
	v_mfma_f32_16x16x32_bf16 v[86:89], v[184:187], v[224:227], v[86:89]
	v_mfma_f32_16x16x32_bf16 v[78:81], v[192:195], v[224:227], v[78:81]
	v_mfma_f32_16x16x32_bf16 v[70:73], v[184:187], v[228:231], v[70:73]
	v_mfma_f32_16x16x32_bf16 v[66:69], v[192:195], v[228:231], v[66:69]
	s_setprio 0
	s_barrier
	s_setprio 3
	s_add_i32 s57, s42, s30
	v_lshl_add_u64 v[196:197], s[22:23], 0, v[132:133]
	s_mov_b32 m0, s57
	ds_read_b128 v[200:203], v161 offset:16384
	ds_read_b128 v[204:207], v161 offset:18432
	ds_read_b128 v[208:211], v162 offset:16384
	ds_read_b128 v[212:215], v162 offset:18432
	ds_read_b128 v[216:219], v161 offset:20480
	ds_read_b128 v[220:223], v161 offset:22528
	ds_read_b128 v[224:227], v162 offset:20480
	ds_read_b128 v[228:231], v162 offset:22528
	global_load_lds_dwordx4 v[196:197], off
	s_add_i32 m0, s57, 0x2000
	s_add_u32 s58, s22, 0xb0000
	v_lshl_add_u64 v[196:197], s[22:23], 0, v[130:131]
	s_addc_u32 s59, s23, 0
	s_add_i32 s57, s43, s30
	global_load_lds_dwordx4 v[196:197], off
	v_lshl_add_u64 v[196:197], s[58:59], 0, v[132:133]
	s_mov_b32 m0, s57
	s_nop 0
	global_load_lds_dwordx4 v[196:197], off
	v_lshl_add_u64 v[196:197], s[58:59], 0, v[130:131]
	s_add_i32 m0, s57, 0x2000
	s_nop 0
	global_load_lds_dwordx4 v[196:197], off
	v_lshl_add_u64 v[196:197], s[26:27], 0, v[134:135]
	s_mov_b32 m0, s34
	s_nop 0
	global_load_lds_dwordx4 v[196:197], off
	v_lshl_add_u64 v[196:197], s[26:27], 0, v[136:137]
	s_mov_b32 m0, s35
	s_nop 0
	global_load_lds_dwordx4 v[196:197], off
	s_waitcnt vmcnt(8)
	s_waitcnt lgkmcnt(0)
	s_barrier
; #define PG8_STAGE(bufoff, gbase, voff) do { _Pragma("unroll") for (int _i = 0; _i < 2; ++_i) \
;         __builtin_amdgcn_global_load_lds((const unsigned*)((const char*)(gbase) + (voff)[_i]), (LAS unsigned*)(lds + (bufoff) + ldsw + _i * 8192), 16, 0, 0); } while (0)
; #define PG8_LDA(dst, b, h) do { _Pragma("unroll") for (int m = 0; m < 4; ++m) _Pragma("unroll") for (int k = 0; k < 2; ++k) dst[m][k] = *(const LAS bf16x8*)(lds + PG8_SA(b, h) + ((aoff ^ (k * 64)) + m * 2048)); } while (0)
; #define PG8_LDB(dst, b, h) do { _Pragma("unroll") for (int n = 0; n < 2; ++n) _Pragma("unroll") for (int k = 0; k < 2; ++k) dst[n][k] = *(const LAS bf16x8*)(lds + PG8_SB(b, h) + ((boff ^ (k * 64)) + n * 2048)); } while (0)
; #define PG8_MMA(ai, bj, At, Bt) do { __builtin_amdgcn_s_setprio(1); _Pragma("unroll") for (int m = 0; m < 4; ++m) _Pragma("unroll") for (int n = 0; n < 2; ++n) _Pragma("unroll") for (int k = 0; k < 2; ++k) \
;         acc[ai][bj][m][n] = __builtin_amdgcn_mfma_f32_16x16x32_bf16(Bt[n][k], At[m][k], acc[ai][bj][m][n], 0, 0, 0); __builtin_amdgcn_s_setprio(0); } while (0)
; #define PG8_WAIT_V(n) asm volatile("s_waitcnt vmcnt(" #n ")" ::: "memory")
; #define PG8_WAIT_L(n) asm volatile("s_waitcnt lgkmcnt(" #n ")" ::: "memory")
; #define PG8_BAR __builtin_amdgcn_s_barrier()
; #define PG8_SCHED __builtin_amdgcn_sched_barrier(0)
;     ...
;             PG8_WAIT_V(8); PG8_WAIT_L(0); PG8_BAR; if (do1) { PG8_MMA(1, 0, At, B0); PG8_MMA(1, 1, At, B1); } PG8_BAR; PG8_SCHED;
;             PG8_LDB(B0, 1, 0); PG8_LDB(B1, 1, 1); PG8_SCHED; PG8_LDA(At, 1, 0); PG8_STAGE(PG8_SA(0, 1), a2, vs[1]);
;             PG8_WAIT_V(8); PG8_WAIT_L(0); PG8_BAR; if (do0) { PG8_MMA(0, 0, At, B0); PG8_MMA(0, 1, At, B1); } PG8_BAR; PG8_SCHED;
	s_setprio 1
	s_waitcnt lgkmcnt(0)
	v_mfma_f32_16x16x32_bf16 v[62:65], v[146:149], v[200:203], v[62:65]
	v_mfma_f32_16x16x32_bf16 v[58:61], v[172:175], v[200:203], v[58:61]
	v_mfma_f32_16x16x32_bf16 v[46:49], v[146:149], v[204:207], v[46:49]
	v_mfma_f32_16x16x32_bf16 v[42:45], v[172:175], v[204:207], v[42:45]
	v_mfma_f32_16x16x32_bf16 v[30:33], v[146:149], v[216:219], v[30:33]
	v_mfma_f32_16x16x32_bf16 v[26:29], v[172:175], v[216:219], v[26:29]
	v_mfma_f32_16x16x32_bf16 v[14:17], v[146:149], v[220:223], v[14:17]
	v_mfma_f32_16x16x32_bf16 v[10:13], v[172:175], v[220:223], v[10:13]
	v_mfma_f32_16x16x32_bf16 v[62:65], v[168:171], v[208:211], v[62:65]
	v_mfma_f32_16x16x32_bf16 v[58:61], v[176:179], v[208:211], v[58:61]
	v_mfma_f32_16x16x32_bf16 v[46:49], v[168:171], v[212:215], v[46:49]
	v_mfma_f32_16x16x32_bf16 v[42:45], v[176:179], v[212:215], v[42:45]
	v_mfma_f32_16x16x32_bf16 v[30:33], v[168:171], v[224:227], v[30:33]
	v_mfma_f32_16x16x32_bf16 v[26:29], v[176:179], v[224:227], v[26:29]
	v_mfma_f32_16x16x32_bf16 v[14:17], v[168:171], v[228:231], v[14:17]
	v_mfma_f32_16x16x32_bf16 v[10:13], v[176:179], v[228:231], v[10:13]
	v_mfma_f32_16x16x32_bf16 v[54:57], v[180:183], v[200:203], v[54:57]
	v_mfma_f32_16x16x32_bf16 v[50:53], v[188:191], v[200:203], v[50:53]
	v_mfma_f32_16x16x32_bf16 v[38:41], v[180:183], v[204:207], v[38:41]
	v_mfma_f32_16x16x32_bf16 v[34:37], v[188:191], v[204:207], v[34:37]
	v_mfma_f32_16x16x32_bf16 v[22:25], v[180:183], v[216:219], v[22:25]
	v_mfma_f32_16x16x32_bf16 v[18:21], v[188:191], v[216:219], v[18:21]
	v_mfma_f32_16x16x32_bf16 v[6:9], v[180:183], v[220:223], v[6:9]
	v_mfma_f32_16x16x32_bf16 v[2:5], v[188:191], v[220:223], v[2:5]
	v_mfma_f32_16x16x32_bf16 v[54:57], v[184:187], v[208:211], v[54:57]
	v_mfma_f32_16x16x32_bf16 v[50:53], v[192:195], v[208:211], v[50:53]
	v_mfma_f32_16x16x32_bf16 v[38:41], v[184:187], v[212:215], v[38:41]
	v_mfma_f32_16x16x32_bf16 v[34:37], v[192:195], v[212:215], v[34:37]
	v_mfma_f32_16x16x32_bf16 v[22:25], v[184:187], v[224:227], v[22:25]
	v_mfma_f32_16x16x32_bf16 v[18:21], v[192:195], v[224:227], v[18:21]
	v_mfma_f32_16x16x32_bf16 v[6:9], v[184:187], v[228:231], v[6:9]
	v_mfma_f32_16x16x32_bf16 v[2:5], v[192:195], v[228:231], v[2:5]
	s_setprio 0
	s_barrier
	s_setprio 3
	s_add_i32 s57, 0, 0x18000
	v_add_u32_e32 v146, s57, v150
	v_add_u32_e32 v167, s57, v151
	s_add_i32 s58, 0, 0x1c000
	ds_read_b128 v[146:149], v146
	ds_read_b128 v[168:171], v167
	ds_read_b128 v[172:175], v163
	ds_read_b128 v[176:179], v164
	v_add_u32_e32 v167, s58, v150
	v_add_u32_e32 v184, s58, v151
	ds_read_b128 v[180:183], v167
	ds_read_b128 v[184:187], v184
	ds_read_b128 v[188:191], v165
	ds_read_b128 v[192:195], v166
	s_mov_b32 m0, s36
	v_lshl_add_u64 v[196:197], s[26:27], 0, v[138:139]
	ds_read_b128 v[200:203], v161 offset:32768
	ds_read_b128 v[204:207], v161 offset:34816
	ds_read_b128 v[208:211], v162 offset:32768
	ds_read_b128 v[212:215], v162 offset:34816
	ds_read_b128 v[216:219], v161 offset:36864
	ds_read_b128 v[220:223], v161 offset:38912
	ds_read_b128 v[224:227], v162 offset:36864
	ds_read_b128 v[228:231], v162 offset:38912
	global_load_lds_dwordx4 v[196:197], off
	v_lshl_add_u64 v[196:197], s[26:27], 0, v[140:141]
	s_mov_b32 m0, s37
	s_nop 0
	global_load_lds_dwordx4 v[196:197], off
	s_waitcnt vmcnt(8)
	s_waitcnt lgkmcnt(0)
	s_barrier
	s_setprio 1
	s_waitcnt lgkmcnt(0)
	v_mfma_f32_16x16x32_bf16 v[126:129], v[146:149], v[200:203], v[126:129]
	v_mfma_f32_16x16x32_bf16 v[122:125], v[172:175], v[200:203], v[122:125]
	v_mfma_f32_16x16x32_bf16 v[114:117], v[146:149], v[204:207], v[114:117]
	v_mfma_f32_16x16x32_bf16 v[106:109], v[172:175], v[204:207], v[106:109]
	v_mfma_f32_16x16x32_bf16 v[98:101], v[146:149], v[216:219], v[98:101]
	v_mfma_f32_16x16x32_bf16 v[90:93], v[172:175], v[216:219], v[90:93]
	v_mfma_f32_16x16x32_bf16 v[82:85], v[146:149], v[220:223], v[82:85]
	v_mfma_f32_16x16x32_bf16 v[74:77], v[172:175], v[220:223], v[74:77]
	v_mfma_f32_16x16x32_bf16 v[126:129], v[168:171], v[208:211], v[126:129]
	v_mfma_f32_16x16x32_bf16 v[122:125], v[176:179], v[208:211], v[122:125]
	v_mfma_f32_16x16x32_bf16 v[114:117], v[168:171], v[212:215], v[114:117]
	v_mfma_f32_16x16x32_bf16 v[106:109], v[176:179], v[212:215], v[106:109]
	v_mfma_f32_16x16x32_bf16 v[98:101], v[168:171], v[224:227], v[98:101]
	v_mfma_f32_16x16x32_bf16 v[90:93], v[176:179], v[224:227], v[90:93]
	v_mfma_f32_16x16x32_bf16 v[82:85], v[168:171], v[228:231], v[82:85]
	v_mfma_f32_16x16x32_bf16 v[74:77], v[176:179], v[228:231], v[74:77]
	v_mfma_f32_16x16x32_bf16 v[118:121], v[180:183], v[200:203], v[118:121]
	v_mfma_f32_16x16x32_bf16 v[110:113], v[188:191], v[200:203], v[110:113]
	v_mfma_f32_16x16x32_bf16 v[102:105], v[180:183], v[204:207], v[102:105]
	v_mfma_f32_16x16x32_bf16 v[94:97], v[188:191], v[204:207], v[94:97]
	v_mfma_f32_16x16x32_bf16 v[86:89], v[180:183], v[216:219], v[86:89]
	v_mfma_f32_16x16x32_bf16 v[78:81], v[188:191], v[216:219], v[78:81]
	v_mfma_f32_16x16x32_bf16 v[70:73], v[180:183], v[220:223], v[70:73]
	v_mfma_f32_16x16x32_bf16 v[66:69], v[188:191], v[220:223], v[66:69]
	v_mfma_f32_16x16x32_bf16 v[118:121], v[184:187], v[208:211], v[118:121]
	v_mfma_f32_16x16x32_bf16 v[110:113], v[192:195], v[208:211], v[110:113]
	v_mfma_f32_16x16x32_bf16 v[102:105], v[184:187], v[212:215], v[102:105]
	v_mfma_f32_16x16x32_bf16 v[94:97], v[192:195], v[212:215], v[94:97]
	v_mfma_f32_16x16x32_bf16 v[86:89], v[184:187], v[224:227], v[86:89]
	v_mfma_f32_16x16x32_bf16 v[78:81], v[192:195], v[224:227], v[78:81]
	v_mfma_f32_16x16x32_bf16 v[70:73], v[184:187], v[228:231], v[70:73]
	v_mfma_f32_16x16x32_bf16 v[66:69], v[192:195], v[228:231], v[66:69]
	s_setprio 0
	s_barrier
; #define PG8_STAGE(bufoff, gbase, voff) do { _Pragma("unroll") for (int _i = 0; _i < 2; ++_i) \
;         __builtin_amdgcn_global_load_lds((const unsigned*)((const char*)(gbase) + (voff)[_i]), (LAS unsigned*)(lds + (bufoff) + ldsw + _i * 8192), 16, 0, 0); } while (0)
; #define PG8_LDA(dst, b, h) do { _Pragma("unroll") for (int m = 0; m < 4; ++m) _Pragma("unroll") for (int k = 0; k < 2; ++k) dst[m][k] = *(const LAS bf16x8*)(lds + PG8_SA(b, h) + ((aoff ^ (k * 64)) + m * 2048)); } while (0)
; #define PG8_MMA(ai, bj, At, Bt) do { __builtin_amdgcn_s_setprio(1); _Pragma("unroll") for (int m = 0; m < 4; ++m) _Pragma("unroll") for (int n = 0; n < 2; ++n) _Pragma("unroll") for (int k = 0; k < 2; ++k) \
;         acc[ai][bj][m][n] = __builtin_amdgcn_mfma_f32_16x16x32_bf16(Bt[n][k], At[m][k], acc[ai][bj][m][n], 0, 0, 0); __builtin_amdgcn_s_setprio(0); } while (0)
; #define PG8_WAIT_V(n) asm volatile("s_waitcnt vmcnt(" #n ")" ::: "memory")
; #define PG8_WAIT_L(n) asm volatile("s_waitcnt lgkmcnt(" #n ")" ::: "memory")
; #define PG8_BAR __builtin_amdgcn_s_barrier()
; #define PG8_SCHED __builtin_amdgcn_sched_barrier(0)
;     ...
;             PG8_LDA(At, 1, 1); PG8_STAGE(PG8_SB(1, 0), b3, voffB); PG8_STAGE(PG8_SB(1, 1), b3 + hstep, voffB); PG8_STAGE(PG8_SA(1, 0), a3, vs[0]);
;             PG8_WAIT_V(8); PG8_WAIT_L(0); PG8_BAR; if (do1) { PG8_MMA(1, 0, At, B0); PG8_MMA(1, 1, At, B1); } PG8_BAR; PG8_SCHED;
;         }
	s_setprio 3
	s_add_i32 s26, s57, s30
	v_lshl_add_u64 v[196:197], s[24:25], 0, v[132:133]
	s_mov_b32 m0, s26
	ds_read_b128 v[200:203], v161 offset:49152
	ds_read_b128 v[204:207], v161 offset:51200
	ds_read_b128 v[208:211], v162 offset:49152
	ds_read_b128 v[212:215], v162 offset:51200
	ds_read_b128 v[216:219], v161 offset:53248
	ds_read_b128 v[220:223], v161 offset:55296
	ds_read_b128 v[224:227], v162 offset:53248
	ds_read_b128 v[228:231], v162 offset:55296
	global_load_lds_dwordx4 v[196:197], off
	s_add_i32 m0, s26, 0x2000
	s_add_u32 s22, s22, 0xb4000
	v_lshl_add_u64 v[196:197], s[24:25], 0, v[130:131]
	s_addc_u32 s23, s23, 0
	s_add_i32 s24, s58, s30
	global_load_lds_dwordx4 v[196:197], off
	v_lshl_add_u64 v[196:197], s[22:23], 0, v[132:133]
	s_mov_b32 m0, s24
	s_nop 0
	global_load_lds_dwordx4 v[196:197], off
	v_lshl_add_u64 v[196:197], s[22:23], 0, v[130:131]
	s_add_i32 m0, s24, 0x2000
	s_nop 0
	global_load_lds_dwordx4 v[196:197], off
	v_lshl_add_u64 v[196:197], s[20:21], 0, v[134:135]
	s_mov_b32 m0, s39
	s_nop 0
	global_load_lds_dwordx4 v[196:197], off
	v_lshl_add_u64 v[196:197], s[20:21], 0, v[136:137]
	s_mov_b32 m0, s40
	s_nop 0
	global_load_lds_dwordx4 v[196:197], off
	s_waitcnt vmcnt(8)
	s_waitcnt lgkmcnt(0)
	s_barrier
	s_setprio 1
	s_waitcnt lgkmcnt(0)
	v_mfma_f32_16x16x32_bf16 v[62:65], v[146:149], v[200:203], v[62:65]
	v_mfma_f32_16x16x32_bf16 v[58:61], v[172:175], v[200:203], v[58:61]
	v_mfma_f32_16x16x32_bf16 v[46:49], v[146:149], v[204:207], v[46:49]
	v_mfma_f32_16x16x32_bf16 v[42:45], v[172:175], v[204:207], v[42:45]
	v_mfma_f32_16x16x32_bf16 v[30:33], v[146:149], v[216:219], v[30:33]
	v_mfma_f32_16x16x32_bf16 v[26:29], v[172:175], v[216:219], v[26:29]
	v_mfma_f32_16x16x32_bf16 v[14:17], v[146:149], v[220:223], v[14:17]
	v_mfma_f32_16x16x32_bf16 v[10:13], v[172:175], v[220:223], v[10:13]
	v_mfma_f32_16x16x32_bf16 v[62:65], v[168:171], v[208:211], v[62:65]
	v_mfma_f32_16x16x32_bf16 v[58:61], v[176:179], v[208:211], v[58:61]
	v_mfma_f32_16x16x32_bf16 v[46:49], v[168:171], v[212:215], v[46:49]
	v_mfma_f32_16x16x32_bf16 v[42:45], v[176:179], v[212:215], v[42:45]
	v_mfma_f32_16x16x32_bf16 v[30:33], v[168:171], v[224:227], v[30:33]
	v_mfma_f32_16x16x32_bf16 v[26:29], v[176:179], v[224:227], v[26:29]
	v_mfma_f32_16x16x32_bf16 v[14:17], v[168:171], v[228:231], v[14:17]
	v_mfma_f32_16x16x32_bf16 v[10:13], v[176:179], v[228:231], v[10:13]
	v_mfma_f32_16x16x32_bf16 v[54:57], v[180:183], v[200:203], v[54:57]
	v_mfma_f32_16x16x32_bf16 v[50:53], v[188:191], v[200:203], v[50:53]
	v_mfma_f32_16x16x32_bf16 v[38:41], v[180:183], v[204:207], v[38:41]
	v_mfma_f32_16x16x32_bf16 v[34:37], v[188:191], v[204:207], v[34:37]
	v_mfma_f32_16x16x32_bf16 v[22:25], v[180:183], v[216:219], v[22:25]
	v_mfma_f32_16x16x32_bf16 v[18:21], v[188:191], v[216:219], v[18:21]
	v_mfma_f32_16x16x32_bf16 v[6:9], v[180:183], v[220:223], v[6:9]
	v_mfma_f32_16x16x32_bf16 v[2:5], v[188:191], v[220:223], v[2:5]
	v_mfma_f32_16x16x32_bf16 v[54:57], v[184:187], v[208:211], v[54:57]
	v_mfma_f32_16x16x32_bf16 v[50:53], v[192:195], v[208:211], v[50:53]
	v_mfma_f32_16x16x32_bf16 v[38:41], v[184:187], v[212:215], v[38:41]
	v_mfma_f32_16x16x32_bf16 v[34:37], v[192:195], v[212:215], v[34:37]
	v_mfma_f32_16x16x32_bf16 v[22:25], v[184:187], v[224:227], v[22:25]
	v_mfma_f32_16x16x32_bf16 v[18:21], v[192:195], v[224:227], v[18:21]
	v_mfma_f32_16x16x32_bf16 v[6:9], v[184:187], v[228:231], v[6:9]
	v_mfma_f32_16x16x32_bf16 v[2:5], v[192:195], v[228:231], v[2:5]
	s_setprio 0
	s_barrier
	s_setprio 3
	s_add_i32 s56, s56, 2
	s_add_u32 s18, s18, 0x8000
	s_addc_u32 s19, s19, 0
	s_add_u32 s54, s54, 0x8000
	s_addc_u32 s55, s55, 0
	s_cmp_gt_u32 s56, 41
	s_cbranch_scc0 .LBB0_2411
	s_and_b64 vcc, exec, s[4:5]
	s_cbranch_vccz .LBB0_2414
	s_barrier
